# speedup vs baseline: 1.0155x; 1.0155x over previous
_Z11proj_kernelPKDF16_S0_S0_S0_PKiPKfS4_S4_S4_S4_PDF16_S5_S5_:
	s_cmpk_lt_u32 s2, 0x100
	s_cbranch_scc1 .Lpf_go
	s_cmpk_lt_u32 s2, 0x200
	s_cbranch_scc0 .Lpf_old
	s_endpgm
.Lpf_go:
	s_load_dwordx8 s[24:31], s[0:1], 0x0
	s_load_dwordx8 s[32:39], s[0:1], 0x20
	s_load_dwordx8 s[40:47], s[0:1], 0x40
	s_load_dwordx2 s[48:49], s[0:1], 0x60
	v_and_b32_e32 v1, 63, v0
	v_lshrrev_b32_e32 v2, 6, v0
	v_and_b32_e32 v3, 15, v0
	v_bfe_u32 v4, v0, 4, 2
	s_and_b32 s3, s2, 7
	s_lshr_b32 s4, s2, 3
	s_and_b32 s5, s4, 7
	s_bfe_u32 s6, s4, 0x10003
	s_lshr_b32 s7, s4, 4
	v_readfirstlane_b32 s18, v2
	s_movk_i32 s20, 0x80
	s_cmp_eq_u32 s7, 0
	s_cbranch_scc0 .Lpf_kv
	s_lshl_b32 s8, s3, 1
	s_add_u32 s8, s8, s6
	s_lshr_b32 s9, s8, 3
	s_and_b32 s10, s8, 7
	s_lshl_b32 s10, s10, 8
	s_lshl_b32 s11, s8, 8
	s_mov_b32 s21, 0
	s_waitcnt lgkmcnt(0)
	s_mov_b32 s12, s24
	s_mov_b32 s13, s25
	s_mov_b32 s14, s34
	s_mov_b32 s15, s35
	s_mov_b32 s16, s40
	s_mov_b32 s17, s41
	s_mov_b32 s22, s44
	s_mov_b32 s23, s45
	s_mov_b32 s19, 0x3e38aa3b
	s_branch .Lpf_common
.Lpf_kv:
	s_lshr_b32 s8, s3, 2
	s_add_u32 s21, s8, 1
	s_and_b32 s8, s3, 3
	s_and_b32 s9, s8, 1
	s_lshr_b32 s8, s8, 1
	s_lshl_b32 s8, s8, 1
	s_add_u32 s8, s8, s6
	s_lshl_b32 s10, s8, 8
	s_lshl_b32 s11, s9, 11
	s_add_u32 s11, s11, s10
	s_lshl_b32 s8, s9, 2
	s_waitcnt lgkmcnt(0)
	s_load_dword s51, s[32:33], s8 offset:0x0
	s_cmp_eq_u32 s21, 1
	s_cselect_b32 s12, s26, s28
	s_cselect_b32 s13, s27, s29
	s_cselect_b32 s14, s36, s38
	s_cselect_b32 s15, s37, s39
	s_mov_b32 s16, s42
	s_mov_b32 s17, s43
	s_cselect_b32 s22, s46, s48
	s_cselect_b32 s23, s47, s49
	s_mov_b32 s19, 1.0
	s_waitcnt lgkmcnt(0)
	s_cmp_ge_i32 s10, s51
	s_cbranch_scc0 .Lpf_common
	s_endpgm
.Lpf_common:
	s_mul_i32 s8, s11, 0x880
	s_mul_hi_u32 s24, s11, 0x880
	s_add_u32 s12, s12, s8
	s_addc_u32 s13, s13, s24
	s_lshl_b32 s8, s21, 10
	s_lshl_b32 s24, s5, 7
	s_add_u32 s8, s8, s24
	s_mul_i32 s8, s8, 0x880
	s_add_u32 s6, s30, s8
	s_addc_u32 s7, s31, 0
	s_mov_b32 s4, s12
	s_mov_b32 s5, s13
	s_and_b32 s24, s18, 1
	s_lshr_b32 s25, s18, 1
	s_lshr_b32 s26, s2, 3
	s_and_b32 s26, s26, 7
	s_lshl_b32 s26, s26, 1
	s_add_u32 s26, s26, s24
	s_lshl_b32 s27, s9, 4
	s_add_u32 s27, s27, s26
	s_lshl_b32 s28, s18, 10
	s_lshl_b32 s8, s26, 8
	s_add_u32 s14, s14, s8
	s_addc_u32 s15, s15, 0
	v_lshrrev_b32_e32 v5, 3, v1
	v_lshl_add_u32 v5, v2, 3, v5
	v_mul_u32_u24_e32 v5, 0x880, v5
	v_and_b32_e32 v6, 7, v1
	v_lshrrev_b32_e32 v7, 4, v1
	v_and_b32_e32 v8, 1, v2
	v_lshl_or_b32 v7, v8, 2, v7
	v_xor_b32_e32 v6, v6, v7
	v_lshl_add_u32 v10, v6, 4, v5
	v_add_u32_e32 v11, 0x22000, v10
	v_add_u32_e32 v12, 0x44000, v10
	v_add_u32_e32 v13, 0x66000, v10
	v_lshrrev_b32_e32 v5, 1, v3
	v_xor_b32_e32 v6, v4, v5
	v_lshlrev_b32_e32 v6, 4, v6
	v_or_b32_e32 v7, 4, v4
	v_xor_b32_e32 v7, v7, v5
	v_lshlrev_b32_e32 v7, 4, v7
	v_lshrrev_b32_e32 v9, 1, v2
	v_lshl_add_u32 v9, v9, 6, v3
	v_lshlrev_b32_e32 v9, 7, v9
	v_add_u32_e32 v14, v9, v6
	v_add_u32_e32 v15, v9, v7
	v_lshl_add_u32 v9, v8, 6, v3
	v_lshlrev_b32_e32 v9, 7, v9
	v_add_u32_e32 v9, 0x8000, v9
	v_add_u32_e32 v16, v9, v6
	v_add_u32_e32 v17, v9, v7
	v_add_u32_e32 v18, 0x18000, v14
	v_add_u32_e32 v19, 0x18000, v15
	v_add_u32_e32 v20, 0x18000, v16
	v_add_u32_e32 v21, 0x18000, v17
	v_and_b32_e32 v5, 1, v4
	v_lshl_add_u32 v5, v5, 5, v3
	v_lshlrev_b32_e32 v5, 4, v5
	v_lshrrev_b32_e32 v6, 1, v4
	v_lshl_add_u32 v22, v6, 3, v5
	v_add_u32_e32 v23, 0x1000, v22
	s_cmp_eq_u32 s21, 2
	s_cbranch_scc1 .Lpf_v
	v_lshlrev_b32_e32 v5, 4, v4
	global_load_dwordx4 v[24:27], v5, s[14:15] offset:0
	global_load_dwordx4 v[28:31], v5, s[14:15] offset:64
	global_load_dwordx4 v[32:35], v5, s[14:15] offset:128
	global_load_dwordx4 v[36:39], v5, s[14:15] offset:192
	global_load_dwordx4 v[40:43], v5, s[16:17] offset:0
	global_load_dwordx4 v[44:47], v5, s[16:17] offset:64
	global_load_dwordx4 v[48:51], v5, s[16:17] offset:128
	global_load_dwordx4 v[52:55], v5, s[16:17] offset:192
	s_lshl_b32 s8, s27, 6
	s_lshr_b32 s24, s10, 5
	s_add_u32 s8, s8, s24
	s_lshl_b32 s24, s25, 1
	s_add_u32 s8, s8, s24
	s_lshl_b32 s8, s8, 12
	s_add_u32 s22, s22, s8
	s_addc_u32 s23, s23, 0
	s_add_u32 m0, s28, 0x0
	s_nop 0
	global_load_lds_dwordx4 v10, s[4:5]
	s_add_u32 m0, s28, 0x2000
	s_nop 0
	global_load_lds_dwordx4 v11, s[4:5]
	s_add_u32 m0, s28, 0x4000
	s_nop 0
	global_load_lds_dwordx4 v12, s[4:5]
	s_add_u32 m0, s28, 0x6000
	s_nop 0
	global_load_lds_dwordx4 v13, s[4:5]
	s_add_u32 m0, s28, 0x8000
	s_nop 0
	global_load_lds_dwordx4 v10, s[6:7]
	s_add_u32 m0, s28, 0xa000
	s_nop 0
	global_load_lds_dwordx4 v11, s[6:7]
	s_add_u32 s4, s4, s20
	s_addc_u32 s5, s5, 0
	s_add_u32 s6, s6, s20
	s_addc_u32 s7, s7, 0
	s_add_u32 m0, s28, 0xc000
	s_nop 0
	global_load_lds_dwordx4 v10, s[4:5]
	s_add_u32 m0, s28, 0xe000
	s_nop 0
	global_load_lds_dwordx4 v11, s[4:5]
	s_add_u32 m0, s28, 0x10000
	s_nop 0
	global_load_lds_dwordx4 v12, s[4:5]
	s_add_u32 m0, s28, 0x12000
	s_nop 0
	global_load_lds_dwordx4 v13, s[4:5]
	s_add_u32 m0, s28, 0x14000
	s_nop 0
	global_load_lds_dwordx4 v10, s[6:7]
	s_add_u32 m0, s28, 0x16000
	s_nop 0
	global_load_lds_dwordx4 v11, s[6:7]
	s_add_u32 s4, s4, s20
	s_addc_u32 s5, s5, 0
	s_add_u32 s6, s6, s20
	s_addc_u32 s7, s7, 0
	s_add_u32 m0, s28, 0x18000
	s_nop 0
	global_load_lds_dwordx4 v10, s[4:5]
	s_add_u32 m0, s28, 0x1a000
	s_nop 0
	global_load_lds_dwordx4 v11, s[4:5]
	s_add_u32 m0, s28, 0x1c000
	s_nop 0
	global_load_lds_dwordx4 v12, s[4:5]
	s_add_u32 m0, s28, 0x1e000
	s_nop 0
	global_load_lds_dwordx4 v13, s[4:5]
	s_add_u32 m0, s28, 0x20000
	s_nop 0
	global_load_lds_dwordx4 v10, s[6:7]
	s_add_u32 m0, s28, 0x22000
	s_nop 0
	global_load_lds_dwordx4 v11, s[6:7]
	s_add_u32 s4, s4, s20
	s_addc_u32 s5, s5, 0
	s_add_u32 s6, s6, s20
	s_addc_u32 s7, s7, 0
	s_waitcnt vmcnt(12)
	s_barrier
	s_waitcnt lgkmcnt(7)
	ds_read_b128 v[120:123], v14
	ds_read_b128 v[136:139], v16
	ds_read_b128 v[140:143], v16 offset:2048
	ds_read_b128 v[144:147], v16 offset:4096
	ds_read_b128 v[148:151], v16 offset:6144
	ds_read_b128 v[124:127], v14 offset:2048
	ds_read_b128 v[128:131], v14 offset:4096
	ds_read_b128 v[132:135], v14 offset:6144
	s_waitcnt lgkmcnt(7)
	ds_read_b128 v[152:155], v15
	ds_read_b128 v[168:171], v17
	ds_read_b128 v[172:175], v17 offset:2048
	ds_read_b128 v[176:179], v17 offset:4096
	ds_read_b128 v[180:183], v17 offset:6144
	ds_read_b128 v[156:159], v15 offset:2048
	ds_read_b128 v[160:163], v15 offset:4096
	ds_read_b128 v[164:167], v15 offset:6144
	s_waitcnt lgkmcnt(14)
	v_mfma_f32_16x16x32_f16 v[56:59], v[136:139], v[120:123], 0
	s_waitcnt lgkmcnt(13)
	v_mfma_f32_16x16x32_f16 v[60:63], v[140:143], v[120:123], 0
	s_waitcnt lgkmcnt(12)
	v_mfma_f32_16x16x32_f16 v[64:67], v[144:147], v[120:123], 0
	s_waitcnt lgkmcnt(11)
	v_mfma_f32_16x16x32_f16 v[68:71], v[148:151], v[120:123], 0
	s_waitcnt lgkmcnt(10)
	v_mfma_f32_16x16x32_f16 v[72:75], v[136:139], v[124:127], 0
	v_mfma_f32_16x16x32_f16 v[76:79], v[140:143], v[124:127], 0
	v_mfma_f32_16x16x32_f16 v[80:83], v[144:147], v[124:127], 0
	v_mfma_f32_16x16x32_f16 v[84:87], v[148:151], v[124:127], 0
	s_waitcnt lgkmcnt(9)
	v_mfma_f32_16x16x32_f16 v[88:91], v[136:139], v[128:131], 0
	v_mfma_f32_16x16x32_f16 v[92:95], v[140:143], v[128:131], 0
	v_mfma_f32_16x16x32_f16 v[96:99], v[144:147], v[128:131], 0
	v_mfma_f32_16x16x32_f16 v[100:103], v[148:151], v[128:131], 0
	s_waitcnt lgkmcnt(8)
	v_mfma_f32_16x16x32_f16 v[104:107], v[136:139], v[132:135], 0
	v_mfma_f32_16x16x32_f16 v[108:111], v[140:143], v[132:135], 0
	v_mfma_f32_16x16x32_f16 v[112:115], v[144:147], v[132:135], 0
	v_mfma_f32_16x16x32_f16 v[116:119], v[148:151], v[132:135], 0
	s_waitcnt vmcnt(6) lgkmcnt(0)
	s_barrier
	s_add_u32 m0, s28, 0x0
	s_nop 0
	global_load_lds_dwordx4 v10, s[4:5]
	s_add_u32 m0, s28, 0x2000
	s_nop 0
	global_load_lds_dwordx4 v11, s[4:5]
	s_add_u32 m0, s28, 0x4000
	s_nop 0
	global_load_lds_dwordx4 v12, s[4:5]
	s_add_u32 m0, s28, 0x6000
	s_nop 0
	global_load_lds_dwordx4 v13, s[4:5]
	s_add_u32 m0, s28, 0x8000
	s_nop 0
	global_load_lds_dwordx4 v10, s[6:7]
	s_add_u32 m0, s28, 0xa000
	s_nop 0
	global_load_lds_dwordx4 v11, s[6:7]
	s_add_u32 s4, s4, s20
	s_addc_u32 s5, s5, 0
	s_add_u32 s6, s6, s20
	s_addc_u32 s7, s7, 0
	s_waitcnt lgkmcnt(7)
	ds_read_b128 v[120:123], v14 offset:49152
	ds_read_b128 v[136:139], v16 offset:49152
	ds_read_b128 v[140:143], v16 offset:51200
	ds_read_b128 v[144:147], v16 offset:53248
	ds_read_b128 v[148:151], v16 offset:55296
	ds_read_b128 v[124:127], v14 offset:51200
	ds_read_b128 v[128:131], v14 offset:53248
	ds_read_b128 v[132:135], v14 offset:55296
	s_waitcnt lgkmcnt(14)
	v_mfma_f32_16x16x32_f16 v[56:59], v[168:171], v[152:155], v[56:59]
	s_waitcnt lgkmcnt(13)
	v_mfma_f32_16x16x32_f16 v[60:63], v[172:175], v[152:155], v[60:63]
	s_waitcnt lgkmcnt(12)
	v_mfma_f32_16x16x32_f16 v[64:67], v[176:179], v[152:155], v[64:67]
	s_waitcnt lgkmcnt(11)
	v_mfma_f32_16x16x32_f16 v[68:71], v[180:183], v[152:155], v[68:71]
	s_waitcnt lgkmcnt(10)
	v_mfma_f32_16x16x32_f16 v[72:75], v[168:171], v[156:159], v[72:75]
	v_mfma_f32_16x16x32_f16 v[76:79], v[172:175], v[156:159], v[76:79]
	v_mfma_f32_16x16x32_f16 v[80:83], v[176:179], v[156:159], v[80:83]
	v_mfma_f32_16x16x32_f16 v[84:87], v[180:183], v[156:159], v[84:87]
	s_waitcnt lgkmcnt(9)
	v_mfma_f32_16x16x32_f16 v[88:91], v[168:171], v[160:163], v[88:91]
	v_mfma_f32_16x16x32_f16 v[92:95], v[172:175], v[160:163], v[92:95]
	v_mfma_f32_16x16x32_f16 v[96:99], v[176:179], v[160:163], v[96:99]
	v_mfma_f32_16x16x32_f16 v[100:103], v[180:183], v[160:163], v[100:103]
	s_waitcnt lgkmcnt(8)
	v_mfma_f32_16x16x32_f16 v[104:107], v[168:171], v[164:167], v[104:107]
	v_mfma_f32_16x16x32_f16 v[108:111], v[172:175], v[164:167], v[108:111]
	v_mfma_f32_16x16x32_f16 v[112:115], v[176:179], v[164:167], v[112:115]
	v_mfma_f32_16x16x32_f16 v[116:119], v[180:183], v[164:167], v[116:119]
	s_waitcnt lgkmcnt(7)
	ds_read_b128 v[152:155], v15 offset:49152
	ds_read_b128 v[168:171], v17 offset:49152
	ds_read_b128 v[172:175], v17 offset:51200
	ds_read_b128 v[176:179], v17 offset:53248
	ds_read_b128 v[180:183], v17 offset:55296
	ds_read_b128 v[156:159], v15 offset:51200
	ds_read_b128 v[160:163], v15 offset:53248
	ds_read_b128 v[164:167], v15 offset:55296
	s_waitcnt lgkmcnt(14)
	v_mfma_f32_16x16x32_f16 v[56:59], v[136:139], v[120:123], v[56:59]
	s_waitcnt lgkmcnt(13)
	v_mfma_f32_16x16x32_f16 v[60:63], v[140:143], v[120:123], v[60:63]
	s_waitcnt lgkmcnt(12)
	v_mfma_f32_16x16x32_f16 v[64:67], v[144:147], v[120:123], v[64:67]
	s_waitcnt lgkmcnt(11)
	v_mfma_f32_16x16x32_f16 v[68:71], v[148:151], v[120:123], v[68:71]
	s_waitcnt lgkmcnt(10)
	v_mfma_f32_16x16x32_f16 v[72:75], v[136:139], v[124:127], v[72:75]
	v_mfma_f32_16x16x32_f16 v[76:79], v[140:143], v[124:127], v[76:79]
	v_mfma_f32_16x16x32_f16 v[80:83], v[144:147], v[124:127], v[80:83]
	v_mfma_f32_16x16x32_f16 v[84:87], v[148:151], v[124:127], v[84:87]
	s_waitcnt lgkmcnt(9)
	v_mfma_f32_16x16x32_f16 v[88:91], v[136:139], v[128:131], v[88:91]
	v_mfma_f32_16x16x32_f16 v[92:95], v[140:143], v[128:131], v[92:95]
	v_mfma_f32_16x16x32_f16 v[96:99], v[144:147], v[128:131], v[96:99]
	v_mfma_f32_16x16x32_f16 v[100:103], v[148:151], v[128:131], v[100:103]
	s_waitcnt lgkmcnt(8)
	v_mfma_f32_16x16x32_f16 v[104:107], v[136:139], v[132:135], v[104:107]
	v_mfma_f32_16x16x32_f16 v[108:111], v[140:143], v[132:135], v[108:111]
	v_mfma_f32_16x16x32_f16 v[112:115], v[144:147], v[132:135], v[112:115]
	v_mfma_f32_16x16x32_f16 v[116:119], v[148:151], v[132:135], v[116:119]
	s_waitcnt vmcnt(6) lgkmcnt(0)
	s_barrier
	s_add_u32 m0, s28, 0xc000
	s_nop 0
	global_load_lds_dwordx4 v10, s[4:5]
	s_add_u32 m0, s28, 0xe000
	s_nop 0
	global_load_lds_dwordx4 v11, s[4:5]
	s_add_u32 m0, s28, 0x10000
	s_nop 0
	global_load_lds_dwordx4 v12, s[4:5]
	s_add_u32 m0, s28, 0x12000
	s_nop 0
	global_load_lds_dwordx4 v13, s[4:5]
	s_add_u32 m0, s28, 0x14000
	s_nop 0
	global_load_lds_dwordx4 v10, s[6:7]
	s_add_u32 m0, s28, 0x16000
	s_nop 0
	global_load_lds_dwordx4 v11, s[6:7]
	s_add_u32 s4, s4, s20
	s_addc_u32 s5, s5, 0
	s_add_u32 s6, s6, s20
	s_addc_u32 s7, s7, 0
	s_waitcnt lgkmcnt(7)
	ds_read_b128 v[120:123], v18
	ds_read_b128 v[136:139], v20
	ds_read_b128 v[140:143], v20 offset:2048
	ds_read_b128 v[144:147], v20 offset:4096
	ds_read_b128 v[148:151], v20 offset:6144
	ds_read_b128 v[124:127], v18 offset:2048
	ds_read_b128 v[128:131], v18 offset:4096
	ds_read_b128 v[132:135], v18 offset:6144
	s_waitcnt lgkmcnt(14)
	v_mfma_f32_16x16x32_f16 v[56:59], v[168:171], v[152:155], v[56:59]
	s_waitcnt lgkmcnt(13)
	v_mfma_f32_16x16x32_f16 v[60:63], v[172:175], v[152:155], v[60:63]
	s_waitcnt lgkmcnt(12)
	v_mfma_f32_16x16x32_f16 v[64:67], v[176:179], v[152:155], v[64:67]
	s_waitcnt lgkmcnt(11)
	v_mfma_f32_16x16x32_f16 v[68:71], v[180:183], v[152:155], v[68:71]
	s_waitcnt lgkmcnt(10)
	v_mfma_f32_16x16x32_f16 v[72:75], v[168:171], v[156:159], v[72:75]
	v_mfma_f32_16x16x32_f16 v[76:79], v[172:175], v[156:159], v[76:79]
	v_mfma_f32_16x16x32_f16 v[80:83], v[176:179], v[156:159], v[80:83]
	v_mfma_f32_16x16x32_f16 v[84:87], v[180:183], v[156:159], v[84:87]
	s_waitcnt lgkmcnt(9)
	v_mfma_f32_16x16x32_f16 v[88:91], v[168:171], v[160:163], v[88:91]
	v_mfma_f32_16x16x32_f16 v[92:95], v[172:175], v[160:163], v[92:95]
	v_mfma_f32_16x16x32_f16 v[96:99], v[176:179], v[160:163], v[96:99]
	v_mfma_f32_16x16x32_f16 v[100:103], v[180:183], v[160:163], v[100:103]
	s_waitcnt lgkmcnt(8)
	v_mfma_f32_16x16x32_f16 v[104:107], v[168:171], v[164:167], v[104:107]
	v_mfma_f32_16x16x32_f16 v[108:111], v[172:175], v[164:167], v[108:111]
	v_mfma_f32_16x16x32_f16 v[112:115], v[176:179], v[164:167], v[112:115]
	v_mfma_f32_16x16x32_f16 v[116:119], v[180:183], v[164:167], v[116:119]
	s_waitcnt lgkmcnt(7)
	ds_read_b128 v[152:155], v19
	ds_read_b128 v[168:171], v21
	ds_read_b128 v[172:175], v21 offset:2048
	ds_read_b128 v[176:179], v21 offset:4096
	ds_read_b128 v[180:183], v21 offset:6144
	ds_read_b128 v[156:159], v19 offset:2048
	ds_read_b128 v[160:163], v19 offset:4096
	ds_read_b128 v[164:167], v19 offset:6144
	s_waitcnt lgkmcnt(14)
	v_mfma_f32_16x16x32_f16 v[56:59], v[136:139], v[120:123], v[56:59]
	s_waitcnt lgkmcnt(13)
	v_mfma_f32_16x16x32_f16 v[60:63], v[140:143], v[120:123], v[60:63]
	s_waitcnt lgkmcnt(12)
	v_mfma_f32_16x16x32_f16 v[64:67], v[144:147], v[120:123], v[64:67]
	s_waitcnt lgkmcnt(11)
	v_mfma_f32_16x16x32_f16 v[68:71], v[148:151], v[120:123], v[68:71]
	s_waitcnt lgkmcnt(10)
	v_mfma_f32_16x16x32_f16 v[72:75], v[136:139], v[124:127], v[72:75]
	v_mfma_f32_16x16x32_f16 v[76:79], v[140:143], v[124:127], v[76:79]
	v_mfma_f32_16x16x32_f16 v[80:83], v[144:147], v[124:127], v[80:83]
	v_mfma_f32_16x16x32_f16 v[84:87], v[148:151], v[124:127], v[84:87]
	s_waitcnt lgkmcnt(9)
	v_mfma_f32_16x16x32_f16 v[88:91], v[136:139], v[128:131], v[88:91]
	v_mfma_f32_16x16x32_f16 v[92:95], v[140:143], v[128:131], v[92:95]
	v_mfma_f32_16x16x32_f16 v[96:99], v[144:147], v[128:131], v[96:99]
	v_mfma_f32_16x16x32_f16 v[100:103], v[148:151], v[128:131], v[100:103]
	s_waitcnt lgkmcnt(8)
	v_mfma_f32_16x16x32_f16 v[104:107], v[136:139], v[132:135], v[104:107]
	v_mfma_f32_16x16x32_f16 v[108:111], v[140:143], v[132:135], v[108:111]
	v_mfma_f32_16x16x32_f16 v[112:115], v[144:147], v[132:135], v[112:115]
	v_mfma_f32_16x16x32_f16 v[116:119], v[148:151], v[132:135], v[116:119]
	s_waitcnt vmcnt(6) lgkmcnt(0)
	s_barrier
	s_add_u32 m0, s28, 0x18000
	s_nop 0
	global_load_lds_dwordx4 v10, s[4:5]
	s_add_u32 m0, s28, 0x1a000
	s_nop 0
	global_load_lds_dwordx4 v11, s[4:5]
	s_add_u32 m0, s28, 0x1c000
	s_nop 0
	global_load_lds_dwordx4 v12, s[4:5]
	s_add_u32 m0, s28, 0x1e000
	s_nop 0
	global_load_lds_dwordx4 v13, s[4:5]
	s_add_u32 m0, s28, 0x20000
	s_nop 0
	global_load_lds_dwordx4 v10, s[6:7]
	s_add_u32 m0, s28, 0x22000
	s_nop 0
	global_load_lds_dwordx4 v11, s[6:7]
	s_add_u32 s4, s4, s20
	s_addc_u32 s5, s5, 0
	s_add_u32 s6, s6, s20
	s_addc_u32 s7, s7, 0
	s_waitcnt lgkmcnt(7)
	ds_read_b128 v[120:123], v14
	ds_read_b128 v[136:139], v16
	ds_read_b128 v[140:143], v16 offset:2048
	ds_read_b128 v[144:147], v16 offset:4096
	ds_read_b128 v[148:151], v16 offset:6144
	ds_read_b128 v[124:127], v14 offset:2048
	ds_read_b128 v[128:131], v14 offset:4096
	ds_read_b128 v[132:135], v14 offset:6144
	s_waitcnt lgkmcnt(14)
	v_mfma_f32_16x16x32_f16 v[56:59], v[168:171], v[152:155], v[56:59]
	s_waitcnt lgkmcnt(13)
	v_mfma_f32_16x16x32_f16 v[60:63], v[172:175], v[152:155], v[60:63]
	s_waitcnt lgkmcnt(12)
	v_mfma_f32_16x16x32_f16 v[64:67], v[176:179], v[152:155], v[64:67]
	s_waitcnt lgkmcnt(11)
	v_mfma_f32_16x16x32_f16 v[68:71], v[180:183], v[152:155], v[68:71]
	s_waitcnt lgkmcnt(10)
	v_mfma_f32_16x16x32_f16 v[72:75], v[168:171], v[156:159], v[72:75]
	v_mfma_f32_16x16x32_f16 v[76:79], v[172:175], v[156:159], v[76:79]
	v_mfma_f32_16x16x32_f16 v[80:83], v[176:179], v[156:159], v[80:83]
	v_mfma_f32_16x16x32_f16 v[84:87], v[180:183], v[156:159], v[84:87]
	s_waitcnt lgkmcnt(9)
	v_mfma_f32_16x16x32_f16 v[88:91], v[168:171], v[160:163], v[88:91]
	v_mfma_f32_16x16x32_f16 v[92:95], v[172:175], v[160:163], v[92:95]
	v_mfma_f32_16x16x32_f16 v[96:99], v[176:179], v[160:163], v[96:99]
	v_mfma_f32_16x16x32_f16 v[100:103], v[180:183], v[160:163], v[100:103]
	s_waitcnt lgkmcnt(8)
	v_mfma_f32_16x16x32_f16 v[104:107], v[168:171], v[164:167], v[104:107]
	v_mfma_f32_16x16x32_f16 v[108:111], v[172:175], v[164:167], v[108:111]
	v_mfma_f32_16x16x32_f16 v[112:115], v[176:179], v[164:167], v[112:115]
	v_mfma_f32_16x16x32_f16 v[116:119], v[180:183], v[164:167], v[116:119]
	s_waitcnt lgkmcnt(7)
	ds_read_b128 v[152:155], v15
	ds_read_b128 v[168:171], v17
	ds_read_b128 v[172:175], v17 offset:2048
	ds_read_b128 v[176:179], v17 offset:4096
	ds_read_b128 v[180:183], v17 offset:6144
	ds_read_b128 v[156:159], v15 offset:2048
	ds_read_b128 v[160:163], v15 offset:4096
	ds_read_b128 v[164:167], v15 offset:6144
	s_waitcnt lgkmcnt(14)
	v_mfma_f32_16x16x32_f16 v[56:59], v[136:139], v[120:123], v[56:59]
	s_waitcnt lgkmcnt(13)
	v_mfma_f32_16x16x32_f16 v[60:63], v[140:143], v[120:123], v[60:63]
	s_waitcnt lgkmcnt(12)
	v_mfma_f32_16x16x32_f16 v[64:67], v[144:147], v[120:123], v[64:67]
	s_waitcnt lgkmcnt(11)
	v_mfma_f32_16x16x32_f16 v[68:71], v[148:151], v[120:123], v[68:71]
	s_waitcnt lgkmcnt(10)
	v_mfma_f32_16x16x32_f16 v[72:75], v[136:139], v[124:127], v[72:75]
	v_mfma_f32_16x16x32_f16 v[76:79], v[140:143], v[124:127], v[76:79]
	v_mfma_f32_16x16x32_f16 v[80:83], v[144:147], v[124:127], v[80:83]
	v_mfma_f32_16x16x32_f16 v[84:87], v[148:151], v[124:127], v[84:87]
	s_waitcnt lgkmcnt(9)
	v_mfma_f32_16x16x32_f16 v[88:91], v[136:139], v[128:131], v[88:91]
	v_mfma_f32_16x16x32_f16 v[92:95], v[140:143], v[128:131], v[92:95]
	v_mfma_f32_16x16x32_f16 v[96:99], v[144:147], v[128:131], v[96:99]
	v_mfma_f32_16x16x32_f16 v[100:103], v[148:151], v[128:131], v[100:103]
	s_waitcnt lgkmcnt(8)
	v_mfma_f32_16x16x32_f16 v[104:107], v[136:139], v[132:135], v[104:107]
	v_mfma_f32_16x16x32_f16 v[108:111], v[140:143], v[132:135], v[108:111]
	v_mfma_f32_16x16x32_f16 v[112:115], v[144:147], v[132:135], v[112:115]
	v_mfma_f32_16x16x32_f16 v[116:119], v[148:151], v[132:135], v[116:119]
	s_waitcnt vmcnt(6) lgkmcnt(0)
	s_barrier
	s_add_u32 m0, s28, 0x0
	s_nop 0
	global_load_lds_dwordx4 v10, s[4:5]
	s_add_u32 m0, s28, 0x2000
	s_nop 0
	global_load_lds_dwordx4 v11, s[4:5]
	s_add_u32 m0, s28, 0x4000
	s_nop 0
	global_load_lds_dwordx4 v12, s[4:5]
	s_add_u32 m0, s28, 0x6000
	s_nop 0
	global_load_lds_dwordx4 v13, s[4:5]
	s_add_u32 m0, s28, 0x8000
	s_nop 0
	global_load_lds_dwordx4 v10, s[6:7]
	s_add_u32 m0, s28, 0xa000
	s_nop 0
	global_load_lds_dwordx4 v11, s[6:7]
	s_add_u32 s4, s4, s20
	s_addc_u32 s5, s5, 0
	s_add_u32 s6, s6, s20
	s_addc_u32 s7, s7, 0
	s_waitcnt lgkmcnt(7)
	ds_read_b128 v[120:123], v14 offset:49152
	ds_read_b128 v[136:139], v16 offset:49152
	ds_read_b128 v[140:143], v16 offset:51200
	ds_read_b128 v[144:147], v16 offset:53248
	ds_read_b128 v[148:151], v16 offset:55296
	ds_read_b128 v[124:127], v14 offset:51200
	ds_read_b128 v[128:131], v14 offset:53248
	ds_read_b128 v[132:135], v14 offset:55296
	s_waitcnt lgkmcnt(14)
	v_mfma_f32_16x16x32_f16 v[56:59], v[168:171], v[152:155], v[56:59]
	s_waitcnt lgkmcnt(13)
	v_mfma_f32_16x16x32_f16 v[60:63], v[172:175], v[152:155], v[60:63]
	s_waitcnt lgkmcnt(12)
	v_mfma_f32_16x16x32_f16 v[64:67], v[176:179], v[152:155], v[64:67]
	s_waitcnt lgkmcnt(11)
	v_mfma_f32_16x16x32_f16 v[68:71], v[180:183], v[152:155], v[68:71]
	s_waitcnt lgkmcnt(10)
	v_mfma_f32_16x16x32_f16 v[72:75], v[168:171], v[156:159], v[72:75]
	v_mfma_f32_16x16x32_f16 v[76:79], v[172:175], v[156:159], v[76:79]
	v_mfma_f32_16x16x32_f16 v[80:83], v[176:179], v[156:159], v[80:83]
	v_mfma_f32_16x16x32_f16 v[84:87], v[180:183], v[156:159], v[84:87]
	s_waitcnt lgkmcnt(9)
	v_mfma_f32_16x16x32_f16 v[88:91], v[168:171], v[160:163], v[88:91]
	v_mfma_f32_16x16x32_f16 v[92:95], v[172:175], v[160:163], v[92:95]
	v_mfma_f32_16x16x32_f16 v[96:99], v[176:179], v[160:163], v[96:99]
	v_mfma_f32_16x16x32_f16 v[100:103], v[180:183], v[160:163], v[100:103]
	s_waitcnt lgkmcnt(8)
	v_mfma_f32_16x16x32_f16 v[104:107], v[168:171], v[164:167], v[104:107]
	v_mfma_f32_16x16x32_f16 v[108:111], v[172:175], v[164:167], v[108:111]
	v_mfma_f32_16x16x32_f16 v[112:115], v[176:179], v[164:167], v[112:115]
	v_mfma_f32_16x16x32_f16 v[116:119], v[180:183], v[164:167], v[116:119]
	s_waitcnt lgkmcnt(7)
	ds_read_b128 v[152:155], v15 offset:49152
	ds_read_b128 v[168:171], v17 offset:49152
	ds_read_b128 v[172:175], v17 offset:51200
	ds_read_b128 v[176:179], v17 offset:53248
	ds_read_b128 v[180:183], v17 offset:55296
	ds_read_b128 v[156:159], v15 offset:51200
	ds_read_b128 v[160:163], v15 offset:53248
	ds_read_b128 v[164:167], v15 offset:55296
	s_waitcnt lgkmcnt(14)
	v_mfma_f32_16x16x32_f16 v[56:59], v[136:139], v[120:123], v[56:59]
	s_waitcnt lgkmcnt(13)
	v_mfma_f32_16x16x32_f16 v[60:63], v[140:143], v[120:123], v[60:63]
	s_waitcnt lgkmcnt(12)
	v_mfma_f32_16x16x32_f16 v[64:67], v[144:147], v[120:123], v[64:67]
	s_waitcnt lgkmcnt(11)
	v_mfma_f32_16x16x32_f16 v[68:71], v[148:151], v[120:123], v[68:71]
	s_waitcnt lgkmcnt(10)
	v_mfma_f32_16x16x32_f16 v[72:75], v[136:139], v[124:127], v[72:75]
	v_mfma_f32_16x16x32_f16 v[76:79], v[140:143], v[124:127], v[76:79]
	v_mfma_f32_16x16x32_f16 v[80:83], v[144:147], v[124:127], v[80:83]
	v_mfma_f32_16x16x32_f16 v[84:87], v[148:151], v[124:127], v[84:87]
	s_waitcnt lgkmcnt(9)
	v_mfma_f32_16x16x32_f16 v[88:91], v[136:139], v[128:131], v[88:91]
	v_mfma_f32_16x16x32_f16 v[92:95], v[140:143], v[128:131], v[92:95]
	v_mfma_f32_16x16x32_f16 v[96:99], v[144:147], v[128:131], v[96:99]
	v_mfma_f32_16x16x32_f16 v[100:103], v[148:151], v[128:131], v[100:103]
	s_waitcnt lgkmcnt(8)
	v_mfma_f32_16x16x32_f16 v[104:107], v[136:139], v[132:135], v[104:107]
	v_mfma_f32_16x16x32_f16 v[108:111], v[140:143], v[132:135], v[108:111]
	v_mfma_f32_16x16x32_f16 v[112:115], v[144:147], v[132:135], v[112:115]
	v_mfma_f32_16x16x32_f16 v[116:119], v[148:151], v[132:135], v[116:119]
	s_waitcnt vmcnt(6) lgkmcnt(0)
	s_barrier
	s_add_u32 m0, s28, 0xc000
	s_nop 0
	global_load_lds_dwordx4 v10, s[4:5]
	s_add_u32 m0, s28, 0xe000
	s_nop 0
	global_load_lds_dwordx4 v11, s[4:5]
	s_add_u32 m0, s28, 0x10000
	s_nop 0
	global_load_lds_dwordx4 v12, s[4:5]
	s_add_u32 m0, s28, 0x12000
	s_nop 0
	global_load_lds_dwordx4 v13, s[4:5]
	s_add_u32 m0, s28, 0x14000
	s_nop 0
	global_load_lds_dwordx4 v10, s[6:7]
	s_add_u32 m0, s28, 0x16000
	s_nop 0
	global_load_lds_dwordx4 v11, s[6:7]
	s_add_u32 s4, s4, s20
	s_addc_u32 s5, s5, 0
	s_add_u32 s6, s6, s20
	s_addc_u32 s7, s7, 0
	s_waitcnt lgkmcnt(7)
	ds_read_b128 v[120:123], v18
	ds_read_b128 v[136:139], v20
	ds_read_b128 v[140:143], v20 offset:2048
	ds_read_b128 v[144:147], v20 offset:4096
	ds_read_b128 v[148:151], v20 offset:6144
	ds_read_b128 v[124:127], v18 offset:2048
	ds_read_b128 v[128:131], v18 offset:4096
	ds_read_b128 v[132:135], v18 offset:6144
	s_waitcnt lgkmcnt(14)
	v_mfma_f32_16x16x32_f16 v[56:59], v[168:171], v[152:155], v[56:59]
	s_waitcnt lgkmcnt(13)
	v_mfma_f32_16x16x32_f16 v[60:63], v[172:175], v[152:155], v[60:63]
	s_waitcnt lgkmcnt(12)
	v_mfma_f32_16x16x32_f16 v[64:67], v[176:179], v[152:155], v[64:67]
	s_waitcnt lgkmcnt(11)
	v_mfma_f32_16x16x32_f16 v[68:71], v[180:183], v[152:155], v[68:71]
	s_waitcnt lgkmcnt(10)
	v_mfma_f32_16x16x32_f16 v[72:75], v[168:171], v[156:159], v[72:75]
	v_mfma_f32_16x16x32_f16 v[76:79], v[172:175], v[156:159], v[76:79]
	v_mfma_f32_16x16x32_f16 v[80:83], v[176:179], v[156:159], v[80:83]
	v_mfma_f32_16x16x32_f16 v[84:87], v[180:183], v[156:159], v[84:87]
	s_waitcnt lgkmcnt(9)
	v_mfma_f32_16x16x32_f16 v[88:91], v[168:171], v[160:163], v[88:91]
	v_mfma_f32_16x16x32_f16 v[92:95], v[172:175], v[160:163], v[92:95]
	v_mfma_f32_16x16x32_f16 v[96:99], v[176:179], v[160:163], v[96:99]
	v_mfma_f32_16x16x32_f16 v[100:103], v[180:183], v[160:163], v[100:103]
	s_waitcnt lgkmcnt(8)
	v_mfma_f32_16x16x32_f16 v[104:107], v[168:171], v[164:167], v[104:107]
	v_mfma_f32_16x16x32_f16 v[108:111], v[172:175], v[164:167], v[108:111]
	v_mfma_f32_16x16x32_f16 v[112:115], v[176:179], v[164:167], v[112:115]
	v_mfma_f32_16x16x32_f16 v[116:119], v[180:183], v[164:167], v[116:119]
	s_waitcnt lgkmcnt(7)
	ds_read_b128 v[152:155], v19
	ds_read_b128 v[168:171], v21
	ds_read_b128 v[172:175], v21 offset:2048
	ds_read_b128 v[176:179], v21 offset:4096
	ds_read_b128 v[180:183], v21 offset:6144
	ds_read_b128 v[156:159], v19 offset:2048
	ds_read_b128 v[160:163], v19 offset:4096
	ds_read_b128 v[164:167], v19 offset:6144
	s_waitcnt lgkmcnt(14)
	v_mfma_f32_16x16x32_f16 v[56:59], v[136:139], v[120:123], v[56:59]
	s_waitcnt lgkmcnt(13)
	v_mfma_f32_16x16x32_f16 v[60:63], v[140:143], v[120:123], v[60:63]
	s_waitcnt lgkmcnt(12)
	v_mfma_f32_16x16x32_f16 v[64:67], v[144:147], v[120:123], v[64:67]
	s_waitcnt lgkmcnt(11)
	v_mfma_f32_16x16x32_f16 v[68:71], v[148:151], v[120:123], v[68:71]
	s_waitcnt lgkmcnt(10)
	v_mfma_f32_16x16x32_f16 v[72:75], v[136:139], v[124:127], v[72:75]
	v_mfma_f32_16x16x32_f16 v[76:79], v[140:143], v[124:127], v[76:79]
	v_mfma_f32_16x16x32_f16 v[80:83], v[144:147], v[124:127], v[80:83]
	v_mfma_f32_16x16x32_f16 v[84:87], v[148:151], v[124:127], v[84:87]
	s_waitcnt lgkmcnt(9)
	v_mfma_f32_16x16x32_f16 v[88:91], v[136:139], v[128:131], v[88:91]
	v_mfma_f32_16x16x32_f16 v[92:95], v[140:143], v[128:131], v[92:95]
	v_mfma_f32_16x16x32_f16 v[96:99], v[144:147], v[128:131], v[96:99]
	v_mfma_f32_16x16x32_f16 v[100:103], v[148:151], v[128:131], v[100:103]
	s_waitcnt lgkmcnt(8)
	v_mfma_f32_16x16x32_f16 v[104:107], v[136:139], v[132:135], v[104:107]
	v_mfma_f32_16x16x32_f16 v[108:111], v[140:143], v[132:135], v[108:111]
	v_mfma_f32_16x16x32_f16 v[112:115], v[144:147], v[132:135], v[112:115]
	v_mfma_f32_16x16x32_f16 v[116:119], v[148:151], v[132:135], v[116:119]
	s_waitcnt vmcnt(6) lgkmcnt(0)
	s_barrier
	s_add_u32 m0, s28, 0x18000
	s_nop 0
	global_load_lds_dwordx4 v10, s[4:5]
	s_add_u32 m0, s28, 0x1a000
	s_nop 0
	global_load_lds_dwordx4 v11, s[4:5]
	s_add_u32 m0, s28, 0x1c000
	s_nop 0
	global_load_lds_dwordx4 v12, s[4:5]
	s_add_u32 m0, s28, 0x1e000
	s_nop 0
	global_load_lds_dwordx4 v13, s[4:5]
	s_add_u32 m0, s28, 0x20000
	s_nop 0
	global_load_lds_dwordx4 v10, s[6:7]
	s_add_u32 m0, s28, 0x22000
	s_nop 0
	global_load_lds_dwordx4 v11, s[6:7]
	s_add_u32 s4, s4, s20
	s_addc_u32 s5, s5, 0
	s_add_u32 s6, s6, s20
	s_addc_u32 s7, s7, 0
	s_waitcnt lgkmcnt(7)
	ds_read_b128 v[120:123], v14
	ds_read_b128 v[136:139], v16
	ds_read_b128 v[140:143], v16 offset:2048
	ds_read_b128 v[144:147], v16 offset:4096
	ds_read_b128 v[148:151], v16 offset:6144
	ds_read_b128 v[124:127], v14 offset:2048
	ds_read_b128 v[128:131], v14 offset:4096
	ds_read_b128 v[132:135], v14 offset:6144
	s_waitcnt lgkmcnt(14)
	v_mfma_f32_16x16x32_f16 v[56:59], v[168:171], v[152:155], v[56:59]
	s_waitcnt lgkmcnt(13)
	v_mfma_f32_16x16x32_f16 v[60:63], v[172:175], v[152:155], v[60:63]
	s_waitcnt lgkmcnt(12)
	v_mfma_f32_16x16x32_f16 v[64:67], v[176:179], v[152:155], v[64:67]
	s_waitcnt lgkmcnt(11)
	v_mfma_f32_16x16x32_f16 v[68:71], v[180:183], v[152:155], v[68:71]
	s_waitcnt lgkmcnt(10)
	v_mfma_f32_16x16x32_f16 v[72:75], v[168:171], v[156:159], v[72:75]
	v_mfma_f32_16x16x32_f16 v[76:79], v[172:175], v[156:159], v[76:79]
	v_mfma_f32_16x16x32_f16 v[80:83], v[176:179], v[156:159], v[80:83]
	v_mfma_f32_16x16x32_f16 v[84:87], v[180:183], v[156:159], v[84:87]
	s_waitcnt lgkmcnt(9)
	v_mfma_f32_16x16x32_f16 v[88:91], v[168:171], v[160:163], v[88:91]
	v_mfma_f32_16x16x32_f16 v[92:95], v[172:175], v[160:163], v[92:95]
	v_mfma_f32_16x16x32_f16 v[96:99], v[176:179], v[160:163], v[96:99]
	v_mfma_f32_16x16x32_f16 v[100:103], v[180:183], v[160:163], v[100:103]
	s_waitcnt lgkmcnt(8)
	v_mfma_f32_16x16x32_f16 v[104:107], v[168:171], v[164:167], v[104:107]
	v_mfma_f32_16x16x32_f16 v[108:111], v[172:175], v[164:167], v[108:111]
	v_mfma_f32_16x16x32_f16 v[112:115], v[176:179], v[164:167], v[112:115]
	v_mfma_f32_16x16x32_f16 v[116:119], v[180:183], v[164:167], v[116:119]
	s_waitcnt lgkmcnt(7)
	ds_read_b128 v[152:155], v15
	ds_read_b128 v[168:171], v17
	ds_read_b128 v[172:175], v17 offset:2048
	ds_read_b128 v[176:179], v17 offset:4096
	ds_read_b128 v[180:183], v17 offset:6144
	ds_read_b128 v[156:159], v15 offset:2048
	ds_read_b128 v[160:163], v15 offset:4096
	ds_read_b128 v[164:167], v15 offset:6144
	s_waitcnt lgkmcnt(14)
	v_mfma_f32_16x16x32_f16 v[56:59], v[136:139], v[120:123], v[56:59]
	s_waitcnt lgkmcnt(13)
	v_mfma_f32_16x16x32_f16 v[60:63], v[140:143], v[120:123], v[60:63]
	s_waitcnt lgkmcnt(12)
	v_mfma_f32_16x16x32_f16 v[64:67], v[144:147], v[120:123], v[64:67]
	s_waitcnt lgkmcnt(11)
	v_mfma_f32_16x16x32_f16 v[68:71], v[148:151], v[120:123], v[68:71]
	s_waitcnt lgkmcnt(10)
	v_mfma_f32_16x16x32_f16 v[72:75], v[136:139], v[124:127], v[72:75]
	v_mfma_f32_16x16x32_f16 v[76:79], v[140:143], v[124:127], v[76:79]
	v_mfma_f32_16x16x32_f16 v[80:83], v[144:147], v[124:127], v[80:83]
	v_mfma_f32_16x16x32_f16 v[84:87], v[148:151], v[124:127], v[84:87]
	s_waitcnt lgkmcnt(9)
	v_mfma_f32_16x16x32_f16 v[88:91], v[136:139], v[128:131], v[88:91]
	v_mfma_f32_16x16x32_f16 v[92:95], v[140:143], v[128:131], v[92:95]
	v_mfma_f32_16x16x32_f16 v[96:99], v[144:147], v[128:131], v[96:99]
	v_mfma_f32_16x16x32_f16 v[100:103], v[148:151], v[128:131], v[100:103]
	s_waitcnt lgkmcnt(8)
	v_mfma_f32_16x16x32_f16 v[104:107], v[136:139], v[132:135], v[104:107]
	v_mfma_f32_16x16x32_f16 v[108:111], v[140:143], v[132:135], v[108:111]
	v_mfma_f32_16x16x32_f16 v[112:115], v[144:147], v[132:135], v[112:115]
	v_mfma_f32_16x16x32_f16 v[116:119], v[148:151], v[132:135], v[116:119]
	s_waitcnt vmcnt(6) lgkmcnt(0)
	s_barrier
	s_add_u32 m0, s28, 0x0
	s_nop 0
	global_load_lds_dwordx4 v10, s[4:5]
	s_add_u32 m0, s28, 0x2000
	s_nop 0
	global_load_lds_dwordx4 v11, s[4:5]
	s_add_u32 m0, s28, 0x4000
	s_nop 0
	global_load_lds_dwordx4 v12, s[4:5]
	s_add_u32 m0, s28, 0x6000
	s_nop 0
	global_load_lds_dwordx4 v13, s[4:5]
	s_add_u32 m0, s28, 0x8000
	s_nop 0
	global_load_lds_dwordx4 v10, s[6:7]
	s_add_u32 m0, s28, 0xa000
	s_nop 0
	global_load_lds_dwordx4 v11, s[6:7]
	s_add_u32 s4, s4, s20
	s_addc_u32 s5, s5, 0
	s_add_u32 s6, s6, s20
	s_addc_u32 s7, s7, 0
	s_waitcnt lgkmcnt(7)
	ds_read_b128 v[120:123], v14 offset:49152
	ds_read_b128 v[136:139], v16 offset:49152
	ds_read_b128 v[140:143], v16 offset:51200
	ds_read_b128 v[144:147], v16 offset:53248
	ds_read_b128 v[148:151], v16 offset:55296
	ds_read_b128 v[124:127], v14 offset:51200
	ds_read_b128 v[128:131], v14 offset:53248
	ds_read_b128 v[132:135], v14 offset:55296
	s_waitcnt lgkmcnt(14)
	v_mfma_f32_16x16x32_f16 v[56:59], v[168:171], v[152:155], v[56:59]
	s_waitcnt lgkmcnt(13)
	v_mfma_f32_16x16x32_f16 v[60:63], v[172:175], v[152:155], v[60:63]
	s_waitcnt lgkmcnt(12)
	v_mfma_f32_16x16x32_f16 v[64:67], v[176:179], v[152:155], v[64:67]
	s_waitcnt lgkmcnt(11)
	v_mfma_f32_16x16x32_f16 v[68:71], v[180:183], v[152:155], v[68:71]
	s_waitcnt lgkmcnt(10)
	v_mfma_f32_16x16x32_f16 v[72:75], v[168:171], v[156:159], v[72:75]
	v_mfma_f32_16x16x32_f16 v[76:79], v[172:175], v[156:159], v[76:79]
	v_mfma_f32_16x16x32_f16 v[80:83], v[176:179], v[156:159], v[80:83]
	v_mfma_f32_16x16x32_f16 v[84:87], v[180:183], v[156:159], v[84:87]
	s_waitcnt lgkmcnt(9)
	v_mfma_f32_16x16x32_f16 v[88:91], v[168:171], v[160:163], v[88:91]
	v_mfma_f32_16x16x32_f16 v[92:95], v[172:175], v[160:163], v[92:95]
	v_mfma_f32_16x16x32_f16 v[96:99], v[176:179], v[160:163], v[96:99]
	v_mfma_f32_16x16x32_f16 v[100:103], v[180:183], v[160:163], v[100:103]
	s_waitcnt lgkmcnt(8)
	v_mfma_f32_16x16x32_f16 v[104:107], v[168:171], v[164:167], v[104:107]
	v_mfma_f32_16x16x32_f16 v[108:111], v[172:175], v[164:167], v[108:111]
	v_mfma_f32_16x16x32_f16 v[112:115], v[176:179], v[164:167], v[112:115]
	v_mfma_f32_16x16x32_f16 v[116:119], v[180:183], v[164:167], v[116:119]
	s_waitcnt lgkmcnt(7)
	ds_read_b128 v[152:155], v15 offset:49152
	ds_read_b128 v[168:171], v17 offset:49152
	ds_read_b128 v[172:175], v17 offset:51200
	ds_read_b128 v[176:179], v17 offset:53248
	ds_read_b128 v[180:183], v17 offset:55296
	ds_read_b128 v[156:159], v15 offset:51200
	ds_read_b128 v[160:163], v15 offset:53248
	ds_read_b128 v[164:167], v15 offset:55296
	s_waitcnt lgkmcnt(14)
	v_mfma_f32_16x16x32_f16 v[56:59], v[136:139], v[120:123], v[56:59]
	s_waitcnt lgkmcnt(13)
	v_mfma_f32_16x16x32_f16 v[60:63], v[140:143], v[120:123], v[60:63]
	s_waitcnt lgkmcnt(12)
	v_mfma_f32_16x16x32_f16 v[64:67], v[144:147], v[120:123], v[64:67]
	s_waitcnt lgkmcnt(11)
	v_mfma_f32_16x16x32_f16 v[68:71], v[148:151], v[120:123], v[68:71]
	s_waitcnt lgkmcnt(10)
	v_mfma_f32_16x16x32_f16 v[72:75], v[136:139], v[124:127], v[72:75]
	v_mfma_f32_16x16x32_f16 v[76:79], v[140:143], v[124:127], v[76:79]
	v_mfma_f32_16x16x32_f16 v[80:83], v[144:147], v[124:127], v[80:83]
	v_mfma_f32_16x16x32_f16 v[84:87], v[148:151], v[124:127], v[84:87]
	s_waitcnt lgkmcnt(9)
	v_mfma_f32_16x16x32_f16 v[88:91], v[136:139], v[128:131], v[88:91]
	v_mfma_f32_16x16x32_f16 v[92:95], v[140:143], v[128:131], v[92:95]
	v_mfma_f32_16x16x32_f16 v[96:99], v[144:147], v[128:131], v[96:99]
	v_mfma_f32_16x16x32_f16 v[100:103], v[148:151], v[128:131], v[100:103]
	s_waitcnt lgkmcnt(8)
	v_mfma_f32_16x16x32_f16 v[104:107], v[136:139], v[132:135], v[104:107]
	v_mfma_f32_16x16x32_f16 v[108:111], v[140:143], v[132:135], v[108:111]
	v_mfma_f32_16x16x32_f16 v[112:115], v[144:147], v[132:135], v[112:115]
	v_mfma_f32_16x16x32_f16 v[116:119], v[148:151], v[132:135], v[116:119]
	s_waitcnt vmcnt(6) lgkmcnt(0)
	s_barrier
	s_add_u32 m0, s28, 0xc000
	s_nop 0
	global_load_lds_dwordx4 v10, s[4:5]
	s_add_u32 m0, s28, 0xe000
	s_nop 0
	global_load_lds_dwordx4 v11, s[4:5]
	s_add_u32 m0, s28, 0x10000
	s_nop 0
	global_load_lds_dwordx4 v12, s[4:5]
	s_add_u32 m0, s28, 0x12000
	s_nop 0
	global_load_lds_dwordx4 v13, s[4:5]
	s_add_u32 m0, s28, 0x14000
	s_nop 0
	global_load_lds_dwordx4 v10, s[6:7]
	s_add_u32 m0, s28, 0x16000
	s_nop 0
	global_load_lds_dwordx4 v11, s[6:7]
	s_add_u32 s4, s4, s20
	s_addc_u32 s5, s5, 0
	s_add_u32 s6, s6, s20
	s_addc_u32 s7, s7, 0
	s_waitcnt lgkmcnt(7)
	ds_read_b128 v[120:123], v18
	ds_read_b128 v[136:139], v20
	ds_read_b128 v[140:143], v20 offset:2048
	ds_read_b128 v[144:147], v20 offset:4096
	ds_read_b128 v[148:151], v20 offset:6144
	ds_read_b128 v[124:127], v18 offset:2048
	ds_read_b128 v[128:131], v18 offset:4096
	ds_read_b128 v[132:135], v18 offset:6144
	s_waitcnt lgkmcnt(14)
	v_mfma_f32_16x16x32_f16 v[56:59], v[168:171], v[152:155], v[56:59]
	s_waitcnt lgkmcnt(13)
	v_mfma_f32_16x16x32_f16 v[60:63], v[172:175], v[152:155], v[60:63]
	s_waitcnt lgkmcnt(12)
	v_mfma_f32_16x16x32_f16 v[64:67], v[176:179], v[152:155], v[64:67]
	s_waitcnt lgkmcnt(11)
	v_mfma_f32_16x16x32_f16 v[68:71], v[180:183], v[152:155], v[68:71]
	s_waitcnt lgkmcnt(10)
	v_mfma_f32_16x16x32_f16 v[72:75], v[168:171], v[156:159], v[72:75]
	v_mfma_f32_16x16x32_f16 v[76:79], v[172:175], v[156:159], v[76:79]
	v_mfma_f32_16x16x32_f16 v[80:83], v[176:179], v[156:159], v[80:83]
	v_mfma_f32_16x16x32_f16 v[84:87], v[180:183], v[156:159], v[84:87]
	s_waitcnt lgkmcnt(9)
	v_mfma_f32_16x16x32_f16 v[88:91], v[168:171], v[160:163], v[88:91]
	v_mfma_f32_16x16x32_f16 v[92:95], v[172:175], v[160:163], v[92:95]
	v_mfma_f32_16x16x32_f16 v[96:99], v[176:179], v[160:163], v[96:99]
	v_mfma_f32_16x16x32_f16 v[100:103], v[180:183], v[160:163], v[100:103]
	s_waitcnt lgkmcnt(8)
	v_mfma_f32_16x16x32_f16 v[104:107], v[168:171], v[164:167], v[104:107]
	v_mfma_f32_16x16x32_f16 v[108:111], v[172:175], v[164:167], v[108:111]
	v_mfma_f32_16x16x32_f16 v[112:115], v[176:179], v[164:167], v[112:115]
	v_mfma_f32_16x16x32_f16 v[116:119], v[180:183], v[164:167], v[116:119]
	s_waitcnt lgkmcnt(7)
	ds_read_b128 v[152:155], v19
	ds_read_b128 v[168:171], v21
	ds_read_b128 v[172:175], v21 offset:2048
	ds_read_b128 v[176:179], v21 offset:4096
	ds_read_b128 v[180:183], v21 offset:6144
	ds_read_b128 v[156:159], v19 offset:2048
	ds_read_b128 v[160:163], v19 offset:4096
	ds_read_b128 v[164:167], v19 offset:6144
	s_waitcnt lgkmcnt(14)
	v_mfma_f32_16x16x32_f16 v[56:59], v[136:139], v[120:123], v[56:59]
	s_waitcnt lgkmcnt(13)
	v_mfma_f32_16x16x32_f16 v[60:63], v[140:143], v[120:123], v[60:63]
	s_waitcnt lgkmcnt(12)
	v_mfma_f32_16x16x32_f16 v[64:67], v[144:147], v[120:123], v[64:67]
	s_waitcnt lgkmcnt(11)
	v_mfma_f32_16x16x32_f16 v[68:71], v[148:151], v[120:123], v[68:71]
	s_waitcnt lgkmcnt(10)
	v_mfma_f32_16x16x32_f16 v[72:75], v[136:139], v[124:127], v[72:75]
	v_mfma_f32_16x16x32_f16 v[76:79], v[140:143], v[124:127], v[76:79]
	v_mfma_f32_16x16x32_f16 v[80:83], v[144:147], v[124:127], v[80:83]
	v_mfma_f32_16x16x32_f16 v[84:87], v[148:151], v[124:127], v[84:87]
	s_waitcnt lgkmcnt(9)
	v_mfma_f32_16x16x32_f16 v[88:91], v[136:139], v[128:131], v[88:91]
	v_mfma_f32_16x16x32_f16 v[92:95], v[140:143], v[128:131], v[92:95]
	v_mfma_f32_16x16x32_f16 v[96:99], v[144:147], v[128:131], v[96:99]
	v_mfma_f32_16x16x32_f16 v[100:103], v[148:151], v[128:131], v[100:103]
	s_waitcnt lgkmcnt(8)
	v_mfma_f32_16x16x32_f16 v[104:107], v[136:139], v[132:135], v[104:107]
	v_mfma_f32_16x16x32_f16 v[108:111], v[140:143], v[132:135], v[108:111]
	v_mfma_f32_16x16x32_f16 v[112:115], v[144:147], v[132:135], v[112:115]
	v_mfma_f32_16x16x32_f16 v[116:119], v[148:151], v[132:135], v[116:119]
	s_waitcnt vmcnt(6) lgkmcnt(0)
	s_barrier
	s_add_u32 m0, s28, 0x18000
	s_nop 0
	global_load_lds_dwordx4 v10, s[4:5]
	s_add_u32 m0, s28, 0x1a000
	s_nop 0
	global_load_lds_dwordx4 v11, s[4:5]
	s_add_u32 m0, s28, 0x1c000
	s_nop 0
	global_load_lds_dwordx4 v12, s[4:5]
	s_add_u32 m0, s28, 0x1e000
	s_nop 0
	global_load_lds_dwordx4 v13, s[4:5]
	s_add_u32 m0, s28, 0x20000
	s_nop 0
	global_load_lds_dwordx4 v10, s[6:7]
	s_add_u32 m0, s28, 0x22000
	s_nop 0
	global_load_lds_dwordx4 v11, s[6:7]
	s_add_u32 s4, s4, s20
	s_addc_u32 s5, s5, 0
	s_add_u32 s6, s6, s20
	s_addc_u32 s7, s7, 0
	s_waitcnt lgkmcnt(7)
	ds_read_b128 v[120:123], v14
	ds_read_b128 v[136:139], v16
	ds_read_b128 v[140:143], v16 offset:2048
	ds_read_b128 v[144:147], v16 offset:4096
	ds_read_b128 v[148:151], v16 offset:6144
	ds_read_b128 v[124:127], v14 offset:2048
	ds_read_b128 v[128:131], v14 offset:4096
	ds_read_b128 v[132:135], v14 offset:6144
	s_waitcnt lgkmcnt(14)
	v_mfma_f32_16x16x32_f16 v[56:59], v[168:171], v[152:155], v[56:59]
	s_waitcnt lgkmcnt(13)
	v_mfma_f32_16x16x32_f16 v[60:63], v[172:175], v[152:155], v[60:63]
	s_waitcnt lgkmcnt(12)
	v_mfma_f32_16x16x32_f16 v[64:67], v[176:179], v[152:155], v[64:67]
	s_waitcnt lgkmcnt(11)
	v_mfma_f32_16x16x32_f16 v[68:71], v[180:183], v[152:155], v[68:71]
	s_waitcnt lgkmcnt(10)
	v_mfma_f32_16x16x32_f16 v[72:75], v[168:171], v[156:159], v[72:75]
	v_mfma_f32_16x16x32_f16 v[76:79], v[172:175], v[156:159], v[76:79]
	v_mfma_f32_16x16x32_f16 v[80:83], v[176:179], v[156:159], v[80:83]
	v_mfma_f32_16x16x32_f16 v[84:87], v[180:183], v[156:159], v[84:87]
	s_waitcnt lgkmcnt(9)
	v_mfma_f32_16x16x32_f16 v[88:91], v[168:171], v[160:163], v[88:91]
	v_mfma_f32_16x16x32_f16 v[92:95], v[172:175], v[160:163], v[92:95]
	v_mfma_f32_16x16x32_f16 v[96:99], v[176:179], v[160:163], v[96:99]
	v_mfma_f32_16x16x32_f16 v[100:103], v[180:183], v[160:163], v[100:103]
	s_waitcnt lgkmcnt(8)
	v_mfma_f32_16x16x32_f16 v[104:107], v[168:171], v[164:167], v[104:107]
	v_mfma_f32_16x16x32_f16 v[108:111], v[172:175], v[164:167], v[108:111]
	v_mfma_f32_16x16x32_f16 v[112:115], v[176:179], v[164:167], v[112:115]
	v_mfma_f32_16x16x32_f16 v[116:119], v[180:183], v[164:167], v[116:119]
	s_waitcnt lgkmcnt(7)
	ds_read_b128 v[152:155], v15
	ds_read_b128 v[168:171], v17
	ds_read_b128 v[172:175], v17 offset:2048
	ds_read_b128 v[176:179], v17 offset:4096
	ds_read_b128 v[180:183], v17 offset:6144
	ds_read_b128 v[156:159], v15 offset:2048
	ds_read_b128 v[160:163], v15 offset:4096
	ds_read_b128 v[164:167], v15 offset:6144
	s_waitcnt lgkmcnt(14)
	v_mfma_f32_16x16x32_f16 v[56:59], v[136:139], v[120:123], v[56:59]
	s_waitcnt lgkmcnt(13)
	v_mfma_f32_16x16x32_f16 v[60:63], v[140:143], v[120:123], v[60:63]
	s_waitcnt lgkmcnt(12)
	v_mfma_f32_16x16x32_f16 v[64:67], v[144:147], v[120:123], v[64:67]
	s_waitcnt lgkmcnt(11)
	v_mfma_f32_16x16x32_f16 v[68:71], v[148:151], v[120:123], v[68:71]
	s_waitcnt lgkmcnt(10)
	v_mfma_f32_16x16x32_f16 v[72:75], v[136:139], v[124:127], v[72:75]
	v_mfma_f32_16x16x32_f16 v[76:79], v[140:143], v[124:127], v[76:79]
	v_mfma_f32_16x16x32_f16 v[80:83], v[144:147], v[124:127], v[80:83]
	v_mfma_f32_16x16x32_f16 v[84:87], v[148:151], v[124:127], v[84:87]
	s_waitcnt lgkmcnt(9)
	v_mfma_f32_16x16x32_f16 v[88:91], v[136:139], v[128:131], v[88:91]
	v_mfma_f32_16x16x32_f16 v[92:95], v[140:143], v[128:131], v[92:95]
	v_mfma_f32_16x16x32_f16 v[96:99], v[144:147], v[128:131], v[96:99]
	v_mfma_f32_16x16x32_f16 v[100:103], v[148:151], v[128:131], v[100:103]
	s_waitcnt lgkmcnt(8)
	v_mfma_f32_16x16x32_f16 v[104:107], v[136:139], v[132:135], v[104:107]
	v_mfma_f32_16x16x32_f16 v[108:111], v[140:143], v[132:135], v[108:111]
	v_mfma_f32_16x16x32_f16 v[112:115], v[144:147], v[132:135], v[112:115]
	v_mfma_f32_16x16x32_f16 v[116:119], v[148:151], v[132:135], v[116:119]
	s_waitcnt vmcnt(6) lgkmcnt(0)
	s_barrier
	s_add_u32 m0, s28, 0x0
	s_nop 0
	global_load_lds_dwordx4 v10, s[4:5]
	s_add_u32 m0, s28, 0x2000
	s_nop 0
	global_load_lds_dwordx4 v11, s[4:5]
	s_add_u32 m0, s28, 0x4000
	s_nop 0
	global_load_lds_dwordx4 v12, s[4:5]
	s_add_u32 m0, s28, 0x6000
	s_nop 0
	global_load_lds_dwordx4 v13, s[4:5]
	s_add_u32 m0, s28, 0x8000
	s_nop 0
	global_load_lds_dwordx4 v10, s[6:7]
	s_add_u32 m0, s28, 0xa000
	s_nop 0
	global_load_lds_dwordx4 v11, s[6:7]
	s_add_u32 s4, s4, s20
	s_addc_u32 s5, s5, 0
	s_add_u32 s6, s6, s20
	s_addc_u32 s7, s7, 0
	s_waitcnt lgkmcnt(7)
	ds_read_b128 v[120:123], v14 offset:49152
	ds_read_b128 v[136:139], v16 offset:49152
	ds_read_b128 v[140:143], v16 offset:51200
	ds_read_b128 v[144:147], v16 offset:53248
	ds_read_b128 v[148:151], v16 offset:55296
	ds_read_b128 v[124:127], v14 offset:51200
	ds_read_b128 v[128:131], v14 offset:53248
	ds_read_b128 v[132:135], v14 offset:55296
	s_waitcnt lgkmcnt(14)
	v_mfma_f32_16x16x32_f16 v[56:59], v[168:171], v[152:155], v[56:59]
	s_waitcnt lgkmcnt(13)
	v_mfma_f32_16x16x32_f16 v[60:63], v[172:175], v[152:155], v[60:63]
	s_waitcnt lgkmcnt(12)
	v_mfma_f32_16x16x32_f16 v[64:67], v[176:179], v[152:155], v[64:67]
	s_waitcnt lgkmcnt(11)
	v_mfma_f32_16x16x32_f16 v[68:71], v[180:183], v[152:155], v[68:71]
	s_waitcnt lgkmcnt(10)
	v_mfma_f32_16x16x32_f16 v[72:75], v[168:171], v[156:159], v[72:75]
	v_mfma_f32_16x16x32_f16 v[76:79], v[172:175], v[156:159], v[76:79]
	v_mfma_f32_16x16x32_f16 v[80:83], v[176:179], v[156:159], v[80:83]
	v_mfma_f32_16x16x32_f16 v[84:87], v[180:183], v[156:159], v[84:87]
	s_waitcnt lgkmcnt(9)
	v_mfma_f32_16x16x32_f16 v[88:91], v[168:171], v[160:163], v[88:91]
	v_mfma_f32_16x16x32_f16 v[92:95], v[172:175], v[160:163], v[92:95]
	v_mfma_f32_16x16x32_f16 v[96:99], v[176:179], v[160:163], v[96:99]
	v_mfma_f32_16x16x32_f16 v[100:103], v[180:183], v[160:163], v[100:103]
	s_waitcnt lgkmcnt(8)
	v_mfma_f32_16x16x32_f16 v[104:107], v[168:171], v[164:167], v[104:107]
	v_mfma_f32_16x16x32_f16 v[108:111], v[172:175], v[164:167], v[108:111]
	v_mfma_f32_16x16x32_f16 v[112:115], v[176:179], v[164:167], v[112:115]
	v_mfma_f32_16x16x32_f16 v[116:119], v[180:183], v[164:167], v[116:119]
	s_waitcnt lgkmcnt(7)
	ds_read_b128 v[152:155], v15 offset:49152
	ds_read_b128 v[168:171], v17 offset:49152
	ds_read_b128 v[172:175], v17 offset:51200
	ds_read_b128 v[176:179], v17 offset:53248
	ds_read_b128 v[180:183], v17 offset:55296
	ds_read_b128 v[156:159], v15 offset:51200
	ds_read_b128 v[160:163], v15 offset:53248
	ds_read_b128 v[164:167], v15 offset:55296
	s_waitcnt lgkmcnt(14)
	v_mfma_f32_16x16x32_f16 v[56:59], v[136:139], v[120:123], v[56:59]
	s_waitcnt lgkmcnt(13)
	v_mfma_f32_16x16x32_f16 v[60:63], v[140:143], v[120:123], v[60:63]
	s_waitcnt lgkmcnt(12)
	v_mfma_f32_16x16x32_f16 v[64:67], v[144:147], v[120:123], v[64:67]
	s_waitcnt lgkmcnt(11)
	v_mfma_f32_16x16x32_f16 v[68:71], v[148:151], v[120:123], v[68:71]
	s_waitcnt lgkmcnt(10)
	v_mfma_f32_16x16x32_f16 v[72:75], v[136:139], v[124:127], v[72:75]
	v_mfma_f32_16x16x32_f16 v[76:79], v[140:143], v[124:127], v[76:79]
	v_mfma_f32_16x16x32_f16 v[80:83], v[144:147], v[124:127], v[80:83]
	v_mfma_f32_16x16x32_f16 v[84:87], v[148:151], v[124:127], v[84:87]
	s_waitcnt lgkmcnt(9)
	v_mfma_f32_16x16x32_f16 v[88:91], v[136:139], v[128:131], v[88:91]
	v_mfma_f32_16x16x32_f16 v[92:95], v[140:143], v[128:131], v[92:95]
	v_mfma_f32_16x16x32_f16 v[96:99], v[144:147], v[128:131], v[96:99]
	v_mfma_f32_16x16x32_f16 v[100:103], v[148:151], v[128:131], v[100:103]
	s_waitcnt lgkmcnt(8)
	v_mfma_f32_16x16x32_f16 v[104:107], v[136:139], v[132:135], v[104:107]
	v_mfma_f32_16x16x32_f16 v[108:111], v[140:143], v[132:135], v[108:111]
	v_mfma_f32_16x16x32_f16 v[112:115], v[144:147], v[132:135], v[112:115]
	v_mfma_f32_16x16x32_f16 v[116:119], v[148:151], v[132:135], v[116:119]
	s_waitcnt vmcnt(6) lgkmcnt(0)
	s_barrier
	s_add_u32 m0, s28, 0xc000
	s_nop 0
	global_load_lds_dwordx4 v10, s[4:5]
	s_add_u32 m0, s28, 0xe000
	s_nop 0
	global_load_lds_dwordx4 v11, s[4:5]
	s_add_u32 m0, s28, 0x10000
	s_nop 0
	global_load_lds_dwordx4 v12, s[4:5]
	s_add_u32 m0, s28, 0x12000
	s_nop 0
	global_load_lds_dwordx4 v13, s[4:5]
	s_add_u32 m0, s28, 0x14000
	s_nop 0
	global_load_lds_dwordx4 v10, s[6:7]
	s_add_u32 m0, s28, 0x16000
	s_nop 0
	global_load_lds_dwordx4 v11, s[6:7]
	s_add_u32 s4, s4, s20
	s_addc_u32 s5, s5, 0
	s_add_u32 s6, s6, s20
	s_addc_u32 s7, s7, 0
	s_waitcnt lgkmcnt(7)
	ds_read_b128 v[120:123], v18
	ds_read_b128 v[136:139], v20
	ds_read_b128 v[140:143], v20 offset:2048
	ds_read_b128 v[144:147], v20 offset:4096
	ds_read_b128 v[148:151], v20 offset:6144
	ds_read_b128 v[124:127], v18 offset:2048
	ds_read_b128 v[128:131], v18 offset:4096
	ds_read_b128 v[132:135], v18 offset:6144
	s_waitcnt lgkmcnt(14)
	v_mfma_f32_16x16x32_f16 v[56:59], v[168:171], v[152:155], v[56:59]
	s_waitcnt lgkmcnt(13)
	v_mfma_f32_16x16x32_f16 v[60:63], v[172:175], v[152:155], v[60:63]
	s_waitcnt lgkmcnt(12)
	v_mfma_f32_16x16x32_f16 v[64:67], v[176:179], v[152:155], v[64:67]
	s_waitcnt lgkmcnt(11)
	v_mfma_f32_16x16x32_f16 v[68:71], v[180:183], v[152:155], v[68:71]
	s_waitcnt lgkmcnt(10)
	v_mfma_f32_16x16x32_f16 v[72:75], v[168:171], v[156:159], v[72:75]
	v_mfma_f32_16x16x32_f16 v[76:79], v[172:175], v[156:159], v[76:79]
	v_mfma_f32_16x16x32_f16 v[80:83], v[176:179], v[156:159], v[80:83]
	v_mfma_f32_16x16x32_f16 v[84:87], v[180:183], v[156:159], v[84:87]
	s_waitcnt lgkmcnt(9)
	v_mfma_f32_16x16x32_f16 v[88:91], v[168:171], v[160:163], v[88:91]
	v_mfma_f32_16x16x32_f16 v[92:95], v[172:175], v[160:163], v[92:95]
	v_mfma_f32_16x16x32_f16 v[96:99], v[176:179], v[160:163], v[96:99]
	v_mfma_f32_16x16x32_f16 v[100:103], v[180:183], v[160:163], v[100:103]
	s_waitcnt lgkmcnt(8)
	v_mfma_f32_16x16x32_f16 v[104:107], v[168:171], v[164:167], v[104:107]
	v_mfma_f32_16x16x32_f16 v[108:111], v[172:175], v[164:167], v[108:111]
	v_mfma_f32_16x16x32_f16 v[112:115], v[176:179], v[164:167], v[112:115]
	v_mfma_f32_16x16x32_f16 v[116:119], v[180:183], v[164:167], v[116:119]
	s_waitcnt lgkmcnt(7)
	ds_read_b128 v[152:155], v19
	ds_read_b128 v[168:171], v21
	ds_read_b128 v[172:175], v21 offset:2048
	ds_read_b128 v[176:179], v21 offset:4096
	ds_read_b128 v[180:183], v21 offset:6144
	ds_read_b128 v[156:159], v19 offset:2048
	ds_read_b128 v[160:163], v19 offset:4096
	ds_read_b128 v[164:167], v19 offset:6144
	s_waitcnt lgkmcnt(14)
	v_mfma_f32_16x16x32_f16 v[56:59], v[136:139], v[120:123], v[56:59]
	s_waitcnt lgkmcnt(13)
	v_mfma_f32_16x16x32_f16 v[60:63], v[140:143], v[120:123], v[60:63]
	s_waitcnt lgkmcnt(12)
	v_mfma_f32_16x16x32_f16 v[64:67], v[144:147], v[120:123], v[64:67]
	s_waitcnt lgkmcnt(11)
	v_mfma_f32_16x16x32_f16 v[68:71], v[148:151], v[120:123], v[68:71]
	s_waitcnt lgkmcnt(10)
	v_mfma_f32_16x16x32_f16 v[72:75], v[136:139], v[124:127], v[72:75]
	v_mfma_f32_16x16x32_f16 v[76:79], v[140:143], v[124:127], v[76:79]
	v_mfma_f32_16x16x32_f16 v[80:83], v[144:147], v[124:127], v[80:83]
	v_mfma_f32_16x16x32_f16 v[84:87], v[148:151], v[124:127], v[84:87]
	s_waitcnt lgkmcnt(9)
	v_mfma_f32_16x16x32_f16 v[88:91], v[136:139], v[128:131], v[88:91]
	v_mfma_f32_16x16x32_f16 v[92:95], v[140:143], v[128:131], v[92:95]
	v_mfma_f32_16x16x32_f16 v[96:99], v[144:147], v[128:131], v[96:99]
	v_mfma_f32_16x16x32_f16 v[100:103], v[148:151], v[128:131], v[100:103]
	s_waitcnt lgkmcnt(8)
	v_mfma_f32_16x16x32_f16 v[104:107], v[136:139], v[132:135], v[104:107]
	v_mfma_f32_16x16x32_f16 v[108:111], v[140:143], v[132:135], v[108:111]
	v_mfma_f32_16x16x32_f16 v[112:115], v[144:147], v[132:135], v[112:115]
	v_mfma_f32_16x16x32_f16 v[116:119], v[148:151], v[132:135], v[116:119]
	s_waitcnt vmcnt(6) lgkmcnt(0)
	s_barrier
	s_add_u32 m0, s28, 0x18000
	s_nop 0
	global_load_lds_dwordx4 v10, s[4:5]
	s_add_u32 m0, s28, 0x1a000
	s_nop 0
	global_load_lds_dwordx4 v11, s[4:5]
	s_add_u32 m0, s28, 0x1c000
	s_nop 0
	global_load_lds_dwordx4 v12, s[4:5]
	s_add_u32 m0, s28, 0x1e000
	s_nop 0
	global_load_lds_dwordx4 v13, s[4:5]
	s_add_u32 m0, s28, 0x20000
	s_nop 0
	global_load_lds_dwordx4 v10, s[6:7]
	s_add_u32 m0, s28, 0x22000
	s_nop 0
	global_load_lds_dwordx4 v11, s[6:7]
	s_add_u32 s4, s4, s20
	s_addc_u32 s5, s5, 0
	s_add_u32 s6, s6, s20
	s_addc_u32 s7, s7, 0
	s_waitcnt lgkmcnt(7)
	ds_read_b128 v[120:123], v14
	ds_read_b128 v[136:139], v16
	ds_read_b128 v[140:143], v16 offset:2048
	ds_read_b128 v[144:147], v16 offset:4096
	ds_read_b128 v[148:151], v16 offset:6144
	ds_read_b128 v[124:127], v14 offset:2048
	ds_read_b128 v[128:131], v14 offset:4096
	ds_read_b128 v[132:135], v14 offset:6144
	s_waitcnt lgkmcnt(14)
	v_mfma_f32_16x16x32_f16 v[56:59], v[168:171], v[152:155], v[56:59]
	s_waitcnt lgkmcnt(13)
	v_mfma_f32_16x16x32_f16 v[60:63], v[172:175], v[152:155], v[60:63]
	s_waitcnt lgkmcnt(12)
	v_mfma_f32_16x16x32_f16 v[64:67], v[176:179], v[152:155], v[64:67]
	s_waitcnt lgkmcnt(11)
	v_mfma_f32_16x16x32_f16 v[68:71], v[180:183], v[152:155], v[68:71]
	s_waitcnt lgkmcnt(10)
	v_mfma_f32_16x16x32_f16 v[72:75], v[168:171], v[156:159], v[72:75]
	v_mfma_f32_16x16x32_f16 v[76:79], v[172:175], v[156:159], v[76:79]
	v_mfma_f32_16x16x32_f16 v[80:83], v[176:179], v[156:159], v[80:83]
	v_mfma_f32_16x16x32_f16 v[84:87], v[180:183], v[156:159], v[84:87]
	s_waitcnt lgkmcnt(9)
	v_mfma_f32_16x16x32_f16 v[88:91], v[168:171], v[160:163], v[88:91]
	v_mfma_f32_16x16x32_f16 v[92:95], v[172:175], v[160:163], v[92:95]
	v_mfma_f32_16x16x32_f16 v[96:99], v[176:179], v[160:163], v[96:99]
	v_mfma_f32_16x16x32_f16 v[100:103], v[180:183], v[160:163], v[100:103]
	s_waitcnt lgkmcnt(8)
	v_mfma_f32_16x16x32_f16 v[104:107], v[168:171], v[164:167], v[104:107]
	v_mfma_f32_16x16x32_f16 v[108:111], v[172:175], v[164:167], v[108:111]
	v_mfma_f32_16x16x32_f16 v[112:115], v[176:179], v[164:167], v[112:115]
	v_mfma_f32_16x16x32_f16 v[116:119], v[180:183], v[164:167], v[116:119]
	s_waitcnt lgkmcnt(7)
	ds_read_b128 v[152:155], v15
	ds_read_b128 v[168:171], v17
	ds_read_b128 v[172:175], v17 offset:2048
	ds_read_b128 v[176:179], v17 offset:4096
	ds_read_b128 v[180:183], v17 offset:6144
	ds_read_b128 v[156:159], v15 offset:2048
	ds_read_b128 v[160:163], v15 offset:4096
	ds_read_b128 v[164:167], v15 offset:6144
	s_waitcnt lgkmcnt(14)
	v_mfma_f32_16x16x32_f16 v[56:59], v[136:139], v[120:123], v[56:59]
	s_waitcnt lgkmcnt(13)
	v_mfma_f32_16x16x32_f16 v[60:63], v[140:143], v[120:123], v[60:63]
	s_waitcnt lgkmcnt(12)
	v_mfma_f32_16x16x32_f16 v[64:67], v[144:147], v[120:123], v[64:67]
	s_waitcnt lgkmcnt(11)
	v_mfma_f32_16x16x32_f16 v[68:71], v[148:151], v[120:123], v[68:71]
	s_waitcnt lgkmcnt(10)
	v_mfma_f32_16x16x32_f16 v[72:75], v[136:139], v[124:127], v[72:75]
	v_mfma_f32_16x16x32_f16 v[76:79], v[140:143], v[124:127], v[76:79]
	v_mfma_f32_16x16x32_f16 v[80:83], v[144:147], v[124:127], v[80:83]
	v_mfma_f32_16x16x32_f16 v[84:87], v[148:151], v[124:127], v[84:87]
	s_waitcnt lgkmcnt(9)
	v_mfma_f32_16x16x32_f16 v[88:91], v[136:139], v[128:131], v[88:91]
	v_mfma_f32_16x16x32_f16 v[92:95], v[140:143], v[128:131], v[92:95]
	v_mfma_f32_16x16x32_f16 v[96:99], v[144:147], v[128:131], v[96:99]
	v_mfma_f32_16x16x32_f16 v[100:103], v[148:151], v[128:131], v[100:103]
	s_waitcnt lgkmcnt(8)
	v_mfma_f32_16x16x32_f16 v[104:107], v[136:139], v[132:135], v[104:107]
	v_mfma_f32_16x16x32_f16 v[108:111], v[140:143], v[132:135], v[108:111]
	v_mfma_f32_16x16x32_f16 v[112:115], v[144:147], v[132:135], v[112:115]
	v_mfma_f32_16x16x32_f16 v[116:119], v[148:151], v[132:135], v[116:119]
	s_waitcnt vmcnt(6) lgkmcnt(0)
	s_barrier
	s_add_u32 m0, s28, 0x0
	s_nop 0
	global_load_lds_dwordx4 v10, s[4:5]
	s_add_u32 m0, s28, 0x2000
	s_nop 0
	global_load_lds_dwordx4 v11, s[4:5]
	s_add_u32 m0, s28, 0x4000
	s_nop 0
	global_load_lds_dwordx4 v12, s[4:5]
	s_add_u32 m0, s28, 0x6000
	s_nop 0
	global_load_lds_dwordx4 v13, s[4:5]
	s_add_u32 m0, s28, 0x8000
	s_nop 0
	global_load_lds_dwordx4 v10, s[6:7]
	s_add_u32 m0, s28, 0xa000
	s_nop 0
	global_load_lds_dwordx4 v11, s[6:7]
	s_add_u32 s4, s4, s20
	s_addc_u32 s5, s5, 0
	s_add_u32 s6, s6, s20
	s_addc_u32 s7, s7, 0
	s_waitcnt lgkmcnt(7)
	ds_read_b128 v[120:123], v14 offset:49152
	ds_read_b128 v[136:139], v16 offset:49152
	ds_read_b128 v[140:143], v16 offset:51200
	ds_read_b128 v[144:147], v16 offset:53248
	ds_read_b128 v[148:151], v16 offset:55296
	ds_read_b128 v[124:127], v14 offset:51200
	ds_read_b128 v[128:131], v14 offset:53248
	ds_read_b128 v[132:135], v14 offset:55296
	s_waitcnt lgkmcnt(14)
	v_mfma_f32_16x16x32_f16 v[56:59], v[168:171], v[152:155], v[56:59]
	s_waitcnt lgkmcnt(13)
	v_mfma_f32_16x16x32_f16 v[60:63], v[172:175], v[152:155], v[60:63]
	s_waitcnt lgkmcnt(12)
	v_mfma_f32_16x16x32_f16 v[64:67], v[176:179], v[152:155], v[64:67]
	s_waitcnt lgkmcnt(11)
	v_mfma_f32_16x16x32_f16 v[68:71], v[180:183], v[152:155], v[68:71]
	s_waitcnt lgkmcnt(10)
	v_mfma_f32_16x16x32_f16 v[72:75], v[168:171], v[156:159], v[72:75]
	v_mfma_f32_16x16x32_f16 v[76:79], v[172:175], v[156:159], v[76:79]
	v_mfma_f32_16x16x32_f16 v[80:83], v[176:179], v[156:159], v[80:83]
	v_mfma_f32_16x16x32_f16 v[84:87], v[180:183], v[156:159], v[84:87]
	s_waitcnt lgkmcnt(9)
	v_mfma_f32_16x16x32_f16 v[88:91], v[168:171], v[160:163], v[88:91]
	v_mfma_f32_16x16x32_f16 v[92:95], v[172:175], v[160:163], v[92:95]
	v_mfma_f32_16x16x32_f16 v[96:99], v[176:179], v[160:163], v[96:99]
	v_mfma_f32_16x16x32_f16 v[100:103], v[180:183], v[160:163], v[100:103]
	s_waitcnt lgkmcnt(8)
	v_mfma_f32_16x16x32_f16 v[104:107], v[168:171], v[164:167], v[104:107]
	v_mfma_f32_16x16x32_f16 v[108:111], v[172:175], v[164:167], v[108:111]
	v_mfma_f32_16x16x32_f16 v[112:115], v[176:179], v[164:167], v[112:115]
	v_mfma_f32_16x16x32_f16 v[116:119], v[180:183], v[164:167], v[116:119]
	s_waitcnt lgkmcnt(7)
	ds_read_b128 v[152:155], v15 offset:49152
	ds_read_b128 v[168:171], v17 offset:49152
	ds_read_b128 v[172:175], v17 offset:51200
	ds_read_b128 v[176:179], v17 offset:53248
	ds_read_b128 v[180:183], v17 offset:55296
	ds_read_b128 v[156:159], v15 offset:51200
	ds_read_b128 v[160:163], v15 offset:53248
	ds_read_b128 v[164:167], v15 offset:55296
	s_waitcnt lgkmcnt(14)
	v_mfma_f32_16x16x32_f16 v[56:59], v[136:139], v[120:123], v[56:59]
	s_waitcnt lgkmcnt(13)
	v_mfma_f32_16x16x32_f16 v[60:63], v[140:143], v[120:123], v[60:63]
	s_waitcnt lgkmcnt(12)
	v_mfma_f32_16x16x32_f16 v[64:67], v[144:147], v[120:123], v[64:67]
	s_waitcnt lgkmcnt(11)
	v_mfma_f32_16x16x32_f16 v[68:71], v[148:151], v[120:123], v[68:71]
	s_waitcnt lgkmcnt(10)
	v_mfma_f32_16x16x32_f16 v[72:75], v[136:139], v[124:127], v[72:75]
	v_mfma_f32_16x16x32_f16 v[76:79], v[140:143], v[124:127], v[76:79]
	v_mfma_f32_16x16x32_f16 v[80:83], v[144:147], v[124:127], v[80:83]
	v_mfma_f32_16x16x32_f16 v[84:87], v[148:151], v[124:127], v[84:87]
	s_waitcnt lgkmcnt(9)
	v_mfma_f32_16x16x32_f16 v[88:91], v[136:139], v[128:131], v[88:91]
	v_mfma_f32_16x16x32_f16 v[92:95], v[140:143], v[128:131], v[92:95]
	v_mfma_f32_16x16x32_f16 v[96:99], v[144:147], v[128:131], v[96:99]
	v_mfma_f32_16x16x32_f16 v[100:103], v[148:151], v[128:131], v[100:103]
	s_waitcnt lgkmcnt(8)
	v_mfma_f32_16x16x32_f16 v[104:107], v[136:139], v[132:135], v[104:107]
	v_mfma_f32_16x16x32_f16 v[108:111], v[140:143], v[132:135], v[108:111]
	v_mfma_f32_16x16x32_f16 v[112:115], v[144:147], v[132:135], v[112:115]
	v_mfma_f32_16x16x32_f16 v[116:119], v[148:151], v[132:135], v[116:119]
	s_waitcnt vmcnt(6) lgkmcnt(0)
	s_barrier
	s_waitcnt lgkmcnt(7)
	ds_read_b128 v[120:123], v18
	ds_read_b128 v[136:139], v20
	ds_read_b128 v[140:143], v20 offset:2048
	ds_read_b128 v[144:147], v20 offset:4096
	ds_read_b128 v[148:151], v20 offset:6144
	ds_read_b128 v[124:127], v18 offset:2048
	ds_read_b128 v[128:131], v18 offset:4096
	ds_read_b128 v[132:135], v18 offset:6144
	s_waitcnt lgkmcnt(14)
	v_mfma_f32_16x16x32_f16 v[56:59], v[168:171], v[152:155], v[56:59]
	s_waitcnt lgkmcnt(13)
	v_mfma_f32_16x16x32_f16 v[60:63], v[172:175], v[152:155], v[60:63]
	s_waitcnt lgkmcnt(12)
	v_mfma_f32_16x16x32_f16 v[64:67], v[176:179], v[152:155], v[64:67]
	s_waitcnt lgkmcnt(11)
	v_mfma_f32_16x16x32_f16 v[68:71], v[180:183], v[152:155], v[68:71]
	s_waitcnt lgkmcnt(10)
	v_mfma_f32_16x16x32_f16 v[72:75], v[168:171], v[156:159], v[72:75]
	v_mfma_f32_16x16x32_f16 v[76:79], v[172:175], v[156:159], v[76:79]
	v_mfma_f32_16x16x32_f16 v[80:83], v[176:179], v[156:159], v[80:83]
	v_mfma_f32_16x16x32_f16 v[84:87], v[180:183], v[156:159], v[84:87]
	s_waitcnt lgkmcnt(9)
	v_mfma_f32_16x16x32_f16 v[88:91], v[168:171], v[160:163], v[88:91]
	v_mfma_f32_16x16x32_f16 v[92:95], v[172:175], v[160:163], v[92:95]
	v_mfma_f32_16x16x32_f16 v[96:99], v[176:179], v[160:163], v[96:99]
	v_mfma_f32_16x16x32_f16 v[100:103], v[180:183], v[160:163], v[100:103]
	s_waitcnt lgkmcnt(8)
	v_mfma_f32_16x16x32_f16 v[104:107], v[168:171], v[164:167], v[104:107]
	v_mfma_f32_16x16x32_f16 v[108:111], v[172:175], v[164:167], v[108:111]
	v_mfma_f32_16x16x32_f16 v[112:115], v[176:179], v[164:167], v[112:115]
	v_mfma_f32_16x16x32_f16 v[116:119], v[180:183], v[164:167], v[116:119]
	s_waitcnt lgkmcnt(7)
	ds_read_b128 v[152:155], v19
	ds_read_b128 v[168:171], v21
	ds_read_b128 v[172:175], v21 offset:2048
	ds_read_b128 v[176:179], v21 offset:4096
	ds_read_b128 v[180:183], v21 offset:6144
	ds_read_b128 v[156:159], v19 offset:2048
	ds_read_b128 v[160:163], v19 offset:4096
	ds_read_b128 v[164:167], v19 offset:6144
	s_waitcnt lgkmcnt(14)
	v_mfma_f32_16x16x32_f16 v[56:59], v[136:139], v[120:123], v[56:59]
	s_waitcnt lgkmcnt(13)
	v_mfma_f32_16x16x32_f16 v[60:63], v[140:143], v[120:123], v[60:63]
	s_waitcnt lgkmcnt(12)
	v_mfma_f32_16x16x32_f16 v[64:67], v[144:147], v[120:123], v[64:67]
	s_waitcnt lgkmcnt(11)
	v_mfma_f32_16x16x32_f16 v[68:71], v[148:151], v[120:123], v[68:71]
	s_waitcnt lgkmcnt(10)
	v_mfma_f32_16x16x32_f16 v[72:75], v[136:139], v[124:127], v[72:75]
	v_mfma_f32_16x16x32_f16 v[76:79], v[140:143], v[124:127], v[76:79]
	v_mfma_f32_16x16x32_f16 v[80:83], v[144:147], v[124:127], v[80:83]
	v_mfma_f32_16x16x32_f16 v[84:87], v[148:151], v[124:127], v[84:87]
	s_waitcnt lgkmcnt(9)
	v_mfma_f32_16x16x32_f16 v[88:91], v[136:139], v[128:131], v[88:91]
	v_mfma_f32_16x16x32_f16 v[92:95], v[140:143], v[128:131], v[92:95]
	v_mfma_f32_16x16x32_f16 v[96:99], v[144:147], v[128:131], v[96:99]
	v_mfma_f32_16x16x32_f16 v[100:103], v[148:151], v[128:131], v[100:103]
	s_waitcnt lgkmcnt(8)
	v_mfma_f32_16x16x32_f16 v[104:107], v[136:139], v[132:135], v[104:107]
	v_mfma_f32_16x16x32_f16 v[108:111], v[140:143], v[132:135], v[108:111]
	v_mfma_f32_16x16x32_f16 v[112:115], v[144:147], v[132:135], v[112:115]
	v_mfma_f32_16x16x32_f16 v[116:119], v[148:151], v[132:135], v[116:119]
	s_waitcnt vmcnt(0) lgkmcnt(0)
	s_barrier
	s_waitcnt lgkmcnt(7)
	ds_read_b128 v[120:123], v14
	ds_read_b128 v[136:139], v16
	ds_read_b128 v[140:143], v16 offset:2048
	ds_read_b128 v[144:147], v16 offset:4096
	ds_read_b128 v[148:151], v16 offset:6144
	ds_read_b128 v[124:127], v14 offset:2048
	ds_read_b128 v[128:131], v14 offset:4096
	ds_read_b128 v[132:135], v14 offset:6144
	s_waitcnt lgkmcnt(14)
	v_mfma_f32_16x16x32_f16 v[56:59], v[168:171], v[152:155], v[56:59]
	s_waitcnt lgkmcnt(13)
	v_mfma_f32_16x16x32_f16 v[60:63], v[172:175], v[152:155], v[60:63]
	s_waitcnt lgkmcnt(12)
	v_mfma_f32_16x16x32_f16 v[64:67], v[176:179], v[152:155], v[64:67]
	s_waitcnt lgkmcnt(11)
	v_mfma_f32_16x16x32_f16 v[68:71], v[180:183], v[152:155], v[68:71]
	s_waitcnt lgkmcnt(10)
	v_mfma_f32_16x16x32_f16 v[72:75], v[168:171], v[156:159], v[72:75]
	v_mfma_f32_16x16x32_f16 v[76:79], v[172:175], v[156:159], v[76:79]
	v_mfma_f32_16x16x32_f16 v[80:83], v[176:179], v[156:159], v[80:83]
	v_mfma_f32_16x16x32_f16 v[84:87], v[180:183], v[156:159], v[84:87]
	s_waitcnt lgkmcnt(9)
	v_mfma_f32_16x16x32_f16 v[88:91], v[168:171], v[160:163], v[88:91]
	v_mfma_f32_16x16x32_f16 v[92:95], v[172:175], v[160:163], v[92:95]
	v_mfma_f32_16x16x32_f16 v[96:99], v[176:179], v[160:163], v[96:99]
	v_mfma_f32_16x16x32_f16 v[100:103], v[180:183], v[160:163], v[100:103]
	s_waitcnt lgkmcnt(8)
	v_mfma_f32_16x16x32_f16 v[104:107], v[168:171], v[164:167], v[104:107]
	v_mfma_f32_16x16x32_f16 v[108:111], v[172:175], v[164:167], v[108:111]
	v_mfma_f32_16x16x32_f16 v[112:115], v[176:179], v[164:167], v[112:115]
	v_mfma_f32_16x16x32_f16 v[116:119], v[180:183], v[164:167], v[116:119]
	s_waitcnt lgkmcnt(7)
	ds_read_b128 v[152:155], v15
	ds_read_b128 v[168:171], v17
	ds_read_b128 v[172:175], v17 offset:2048
	ds_read_b128 v[176:179], v17 offset:4096
	ds_read_b128 v[180:183], v17 offset:6144
	ds_read_b128 v[156:159], v15 offset:2048
	ds_read_b128 v[160:163], v15 offset:4096
	ds_read_b128 v[164:167], v15 offset:6144
	s_waitcnt lgkmcnt(14)
	v_mfma_f32_16x16x32_f16 v[56:59], v[136:139], v[120:123], v[56:59]
	s_waitcnt lgkmcnt(13)
	v_mfma_f32_16x16x32_f16 v[60:63], v[140:143], v[120:123], v[60:63]
	s_waitcnt lgkmcnt(12)
	v_mfma_f32_16x16x32_f16 v[64:67], v[144:147], v[120:123], v[64:67]
	s_waitcnt lgkmcnt(11)
	v_mfma_f32_16x16x32_f16 v[68:71], v[148:151], v[120:123], v[68:71]
	s_waitcnt lgkmcnt(10)
	v_mfma_f32_16x16x32_f16 v[72:75], v[136:139], v[124:127], v[72:75]
	v_mfma_f32_16x16x32_f16 v[76:79], v[140:143], v[124:127], v[76:79]
	v_mfma_f32_16x16x32_f16 v[80:83], v[144:147], v[124:127], v[80:83]
	v_mfma_f32_16x16x32_f16 v[84:87], v[148:151], v[124:127], v[84:87]
	s_waitcnt lgkmcnt(9)
	v_mfma_f32_16x16x32_f16 v[88:91], v[136:139], v[128:131], v[88:91]
	v_mfma_f32_16x16x32_f16 v[92:95], v[140:143], v[128:131], v[92:95]
	v_mfma_f32_16x16x32_f16 v[96:99], v[144:147], v[128:131], v[96:99]
	v_mfma_f32_16x16x32_f16 v[100:103], v[148:151], v[128:131], v[100:103]
	s_waitcnt lgkmcnt(8)
	v_mfma_f32_16x16x32_f16 v[104:107], v[136:139], v[132:135], v[104:107]
	v_mfma_f32_16x16x32_f16 v[108:111], v[140:143], v[132:135], v[108:111]
	v_mfma_f32_16x16x32_f16 v[112:115], v[144:147], v[132:135], v[112:115]
	v_mfma_f32_16x16x32_f16 v[116:119], v[148:151], v[132:135], v[116:119]
	s_waitcnt lgkmcnt(6)
	v_mfma_f32_16x16x32_f16 v[56:59], v[168:171], v[152:155], v[56:59]
	s_waitcnt lgkmcnt(5)
	v_mfma_f32_16x16x32_f16 v[60:63], v[172:175], v[152:155], v[60:63]
	s_waitcnt lgkmcnt(4)
	v_mfma_f32_16x16x32_f16 v[64:67], v[176:179], v[152:155], v[64:67]
	s_waitcnt lgkmcnt(3)
	v_mfma_f32_16x16x32_f16 v[68:71], v[180:183], v[152:155], v[68:71]
	s_waitcnt lgkmcnt(2)
	v_mfma_f32_16x16x32_f16 v[72:75], v[168:171], v[156:159], v[72:75]
	v_mfma_f32_16x16x32_f16 v[76:79], v[172:175], v[156:159], v[76:79]
	v_mfma_f32_16x16x32_f16 v[80:83], v[176:179], v[156:159], v[80:83]
	v_mfma_f32_16x16x32_f16 v[84:87], v[180:183], v[156:159], v[84:87]
	s_waitcnt lgkmcnt(1)
	v_mfma_f32_16x16x32_f16 v[88:91], v[168:171], v[160:163], v[88:91]
	v_mfma_f32_16x16x32_f16 v[92:95], v[172:175], v[160:163], v[92:95]
	v_mfma_f32_16x16x32_f16 v[96:99], v[176:179], v[160:163], v[96:99]
	v_mfma_f32_16x16x32_f16 v[100:103], v[180:183], v[160:163], v[100:103]
	s_waitcnt lgkmcnt(0)
	v_mfma_f32_16x16x32_f16 v[104:107], v[168:171], v[164:167], v[104:107]
	v_mfma_f32_16x16x32_f16 v[108:111], v[172:175], v[164:167], v[108:111]
	v_mfma_f32_16x16x32_f16 v[112:115], v[176:179], v[164:167], v[112:115]
	v_mfma_f32_16x16x32_f16 v[116:119], v[180:183], v[164:167], v[116:119]
	s_nop 7
	s_nop 1
	v_mov_b32_e32 v187, s19
	v_add_f32_e32 v56, v56, v24
	v_add_f32_e32 v57, v57, v25
	v_add_f32_e32 v58, v58, v26
	v_add_f32_e32 v59, v59, v27
	v_add_f32_e32 v60, v60, v28
	v_add_f32_e32 v61, v61, v29
	v_add_f32_e32 v62, v62, v30
	v_add_f32_e32 v63, v63, v31
	v_add_f32_e32 v64, v64, v32
	v_add_f32_e32 v65, v65, v33
	v_add_f32_e32 v66, v66, v34
	v_add_f32_e32 v67, v67, v35
	v_add_f32_e32 v68, v68, v36
	v_add_f32_e32 v69, v69, v37
	v_add_f32_e32 v70, v70, v38
	v_add_f32_e32 v71, v71, v39
	v_mul_f32_e32 v184, v56, v56
	v_fmac_f32_e32 v184, v57, v57
	v_fmac_f32_e32 v184, v58, v58
	v_fmac_f32_e32 v184, v59, v59
	v_fmac_f32_e32 v184, v60, v60
	v_fmac_f32_e32 v184, v61, v61
	v_fmac_f32_e32 v184, v62, v62
	v_fmac_f32_e32 v184, v63, v63
	v_fmac_f32_e32 v184, v64, v64
	v_fmac_f32_e32 v184, v65, v65
	v_fmac_f32_e32 v184, v66, v66
	v_fmac_f32_e32 v184, v67, v67
	v_fmac_f32_e32 v184, v68, v68
	v_fmac_f32_e32 v184, v69, v69
	v_fmac_f32_e32 v184, v70, v70
	v_fmac_f32_e32 v184, v71, v71
	v_mov_b32_e32 v185, v184
	s_nop 1
	v_permlane16_swap_b32_e32 v184, v185
	v_add_f32_e32 v184, v184, v185
	v_mov_b32_e32 v185, v184
	s_nop 1
	v_permlane32_swap_b32_e32 v184, v185
	v_add_f32_e32 v184, v184, v185
	v_mov_b32_e32 v186, 0x358637bd
	v_fmac_f32_e32 v186, 0x3c800000, v184
	v_rsq_f32_e32 v186, v186
	s_nop 0
	v_mul_f32_e32 v186, v187, v186
	v_mul_f32_e32 v56, v56, v186
	v_mul_f32_e32 v57, v57, v186
	v_mul_f32_e32 v58, v58, v186
	v_mul_f32_e32 v59, v59, v186
	v_mul_f32_e32 v56, v56, v40
	v_mul_f32_e32 v57, v57, v41
	v_mul_f32_e32 v58, v58, v42
	v_mul_f32_e32 v59, v59, v43
	v_cvt_pk_f16_f32 v56, v56, v57
	v_cvt_pk_f16_f32 v57, v58, v59
	global_store_dwordx2 v22, v[56:57], s[22:23] offset:0
	v_mul_f32_e32 v60, v60, v186
	v_mul_f32_e32 v61, v61, v186
	v_mul_f32_e32 v62, v62, v186
	v_mul_f32_e32 v63, v63, v186
	v_mul_f32_e32 v60, v60, v44
	v_mul_f32_e32 v61, v61, v45
	v_mul_f32_e32 v62, v62, v46
	v_mul_f32_e32 v63, v63, v47
	v_cvt_pk_f16_f32 v60, v60, v61
	v_cvt_pk_f16_f32 v61, v62, v63
	global_store_dwordx2 v22, v[60:61], s[22:23] offset:1024
	v_mul_f32_e32 v64, v64, v186
	v_mul_f32_e32 v65, v65, v186
	v_mul_f32_e32 v66, v66, v186
	v_mul_f32_e32 v67, v67, v186
	v_mul_f32_e32 v64, v64, v48
	v_mul_f32_e32 v65, v65, v49
	v_mul_f32_e32 v66, v66, v50
	v_mul_f32_e32 v67, v67, v51
	v_cvt_pk_f16_f32 v64, v64, v65
	v_cvt_pk_f16_f32 v65, v66, v67
	global_store_dwordx2 v22, v[64:65], s[22:23] offset:2048
	v_mul_f32_e32 v68, v68, v186
	v_mul_f32_e32 v69, v69, v186
	v_mul_f32_e32 v70, v70, v186
	v_mul_f32_e32 v71, v71, v186
	v_mul_f32_e32 v68, v68, v52
	v_mul_f32_e32 v69, v69, v53
	v_mul_f32_e32 v70, v70, v54
	v_mul_f32_e32 v71, v71, v55
	v_cvt_pk_f16_f32 v68, v68, v69
	v_cvt_pk_f16_f32 v69, v70, v71
	global_store_dwordx2 v22, v[68:69], s[22:23] offset:3072
	v_add_f32_e32 v72, v72, v24
	v_add_f32_e32 v73, v73, v25
	v_add_f32_e32 v74, v74, v26
	v_add_f32_e32 v75, v75, v27
	v_add_f32_e32 v76, v76, v28
	v_add_f32_e32 v77, v77, v29
	v_add_f32_e32 v78, v78, v30
	v_add_f32_e32 v79, v79, v31
	v_add_f32_e32 v80, v80, v32
	v_add_f32_e32 v81, v81, v33
	v_add_f32_e32 v82, v82, v34
	v_add_f32_e32 v83, v83, v35
	v_add_f32_e32 v84, v84, v36
	v_add_f32_e32 v85, v85, v37
	v_add_f32_e32 v86, v86, v38
	v_add_f32_e32 v87, v87, v39
	v_mul_f32_e32 v184, v72, v72
	v_fmac_f32_e32 v184, v73, v73
	v_fmac_f32_e32 v184, v74, v74
	v_fmac_f32_e32 v184, v75, v75
	v_fmac_f32_e32 v184, v76, v76
	v_fmac_f32_e32 v184, v77, v77
	v_fmac_f32_e32 v184, v78, v78
	v_fmac_f32_e32 v184, v79, v79
	v_fmac_f32_e32 v184, v80, v80
	v_fmac_f32_e32 v184, v81, v81
	v_fmac_f32_e32 v184, v82, v82
	v_fmac_f32_e32 v184, v83, v83
	v_fmac_f32_e32 v184, v84, v84
	v_fmac_f32_e32 v184, v85, v85
	v_fmac_f32_e32 v184, v86, v86
	v_fmac_f32_e32 v184, v87, v87
	v_mov_b32_e32 v185, v184
	s_nop 1
	v_permlane16_swap_b32_e32 v184, v185
	v_add_f32_e32 v184, v184, v185
	v_mov_b32_e32 v185, v184
	s_nop 1
	v_permlane32_swap_b32_e32 v184, v185
	v_add_f32_e32 v184, v184, v185
	v_mov_b32_e32 v186, 0x358637bd
	v_fmac_f32_e32 v186, 0x3c800000, v184
	v_rsq_f32_e32 v186, v186
	s_nop 0
	v_mul_f32_e32 v186, v187, v186
	v_mul_f32_e32 v72, v72, v186
	v_mul_f32_e32 v73, v73, v186
	v_mul_f32_e32 v74, v74, v186
	v_mul_f32_e32 v75, v75, v186
	v_mul_f32_e32 v72, v72, v40
	v_mul_f32_e32 v73, v73, v41
	v_mul_f32_e32 v74, v74, v42
	v_mul_f32_e32 v75, v75, v43
	v_cvt_pk_f16_f32 v72, v72, v73
	v_cvt_pk_f16_f32 v73, v74, v75
	global_store_dwordx2 v22, v[72:73], s[22:23] offset:256
	v_mul_f32_e32 v76, v76, v186
	v_mul_f32_e32 v77, v77, v186
	v_mul_f32_e32 v78, v78, v186
	v_mul_f32_e32 v79, v79, v186
	v_mul_f32_e32 v76, v76, v44
	v_mul_f32_e32 v77, v77, v45
	v_mul_f32_e32 v78, v78, v46
	v_mul_f32_e32 v79, v79, v47
	v_cvt_pk_f16_f32 v76, v76, v77
	v_cvt_pk_f16_f32 v77, v78, v79
	global_store_dwordx2 v22, v[76:77], s[22:23] offset:1280
	v_mul_f32_e32 v80, v80, v186
	v_mul_f32_e32 v81, v81, v186
	v_mul_f32_e32 v82, v82, v186
	v_mul_f32_e32 v83, v83, v186
	v_mul_f32_e32 v80, v80, v48
	v_mul_f32_e32 v81, v81, v49
	v_mul_f32_e32 v82, v82, v50
	v_mul_f32_e32 v83, v83, v51
	v_cvt_pk_f16_f32 v80, v80, v81
	v_cvt_pk_f16_f32 v81, v82, v83
	global_store_dwordx2 v22, v[80:81], s[22:23] offset:2304
	v_mul_f32_e32 v84, v84, v186
	v_mul_f32_e32 v85, v85, v186
	v_mul_f32_e32 v86, v86, v186
	v_mul_f32_e32 v87, v87, v186
	v_mul_f32_e32 v84, v84, v52
	v_mul_f32_e32 v85, v85, v53
	v_mul_f32_e32 v86, v86, v54
	v_mul_f32_e32 v87, v87, v55
	v_cvt_pk_f16_f32 v84, v84, v85
	v_cvt_pk_f16_f32 v85, v86, v87
	global_store_dwordx2 v22, v[84:85], s[22:23] offset:3328
	v_add_f32_e32 v88, v88, v24
	v_add_f32_e32 v89, v89, v25
	v_add_f32_e32 v90, v90, v26
	v_add_f32_e32 v91, v91, v27
	v_add_f32_e32 v92, v92, v28
	v_add_f32_e32 v93, v93, v29
	v_add_f32_e32 v94, v94, v30
	v_add_f32_e32 v95, v95, v31
	v_add_f32_e32 v96, v96, v32
	v_add_f32_e32 v97, v97, v33
	v_add_f32_e32 v98, v98, v34
	v_add_f32_e32 v99, v99, v35
	v_add_f32_e32 v100, v100, v36
	v_add_f32_e32 v101, v101, v37
	v_add_f32_e32 v102, v102, v38
	v_add_f32_e32 v103, v103, v39
	v_mul_f32_e32 v184, v88, v88
	v_fmac_f32_e32 v184, v89, v89
	v_fmac_f32_e32 v184, v90, v90
	v_fmac_f32_e32 v184, v91, v91
	v_fmac_f32_e32 v184, v92, v92
	v_fmac_f32_e32 v184, v93, v93
	v_fmac_f32_e32 v184, v94, v94
	v_fmac_f32_e32 v184, v95, v95
	v_fmac_f32_e32 v184, v96, v96
	v_fmac_f32_e32 v184, v97, v97
	v_fmac_f32_e32 v184, v98, v98
	v_fmac_f32_e32 v184, v99, v99
	v_fmac_f32_e32 v184, v100, v100
	v_fmac_f32_e32 v184, v101, v101
	v_fmac_f32_e32 v184, v102, v102
	v_fmac_f32_e32 v184, v103, v103
	v_mov_b32_e32 v185, v184
	s_nop 1
	v_permlane16_swap_b32_e32 v184, v185
	v_add_f32_e32 v184, v184, v185
	v_mov_b32_e32 v185, v184
	s_nop 1
	v_permlane32_swap_b32_e32 v184, v185
	v_add_f32_e32 v184, v184, v185
	v_mov_b32_e32 v186, 0x358637bd
	v_fmac_f32_e32 v186, 0x3c800000, v184
	v_rsq_f32_e32 v186, v186
	s_nop 0
	v_mul_f32_e32 v186, v187, v186
	v_mul_f32_e32 v88, v88, v186
	v_mul_f32_e32 v89, v89, v186
	v_mul_f32_e32 v90, v90, v186
	v_mul_f32_e32 v91, v91, v186
	v_mul_f32_e32 v88, v88, v40
	v_mul_f32_e32 v89, v89, v41
	v_mul_f32_e32 v90, v90, v42
	v_mul_f32_e32 v91, v91, v43
	v_cvt_pk_f16_f32 v88, v88, v89
	v_cvt_pk_f16_f32 v89, v90, v91
	global_store_dwordx2 v23, v[88:89], s[22:23] offset:0
	v_mul_f32_e32 v92, v92, v186
	v_mul_f32_e32 v93, v93, v186
	v_mul_f32_e32 v94, v94, v186
	v_mul_f32_e32 v95, v95, v186
	v_mul_f32_e32 v92, v92, v44
	v_mul_f32_e32 v93, v93, v45
	v_mul_f32_e32 v94, v94, v46
	v_mul_f32_e32 v95, v95, v47
	v_cvt_pk_f16_f32 v92, v92, v93
	v_cvt_pk_f16_f32 v93, v94, v95
	global_store_dwordx2 v23, v[92:93], s[22:23] offset:1024
	v_mul_f32_e32 v96, v96, v186
	v_mul_f32_e32 v97, v97, v186
	v_mul_f32_e32 v98, v98, v186
	v_mul_f32_e32 v99, v99, v186
	v_mul_f32_e32 v96, v96, v48
	v_mul_f32_e32 v97, v97, v49
	v_mul_f32_e32 v98, v98, v50
	v_mul_f32_e32 v99, v99, v51
	v_cvt_pk_f16_f32 v96, v96, v97
	v_cvt_pk_f16_f32 v97, v98, v99
	global_store_dwordx2 v23, v[96:97], s[22:23] offset:2048
	v_mul_f32_e32 v100, v100, v186
	v_mul_f32_e32 v101, v101, v186
	v_mul_f32_e32 v102, v102, v186
	v_mul_f32_e32 v103, v103, v186
	v_mul_f32_e32 v100, v100, v52
	v_mul_f32_e32 v101, v101, v53
	v_mul_f32_e32 v102, v102, v54
	v_mul_f32_e32 v103, v103, v55
	v_cvt_pk_f16_f32 v100, v100, v101
	v_cvt_pk_f16_f32 v101, v102, v103
	global_store_dwordx2 v23, v[100:101], s[22:23] offset:3072
	v_add_f32_e32 v104, v104, v24
	v_add_f32_e32 v105, v105, v25
	v_add_f32_e32 v106, v106, v26
	v_add_f32_e32 v107, v107, v27
	v_add_f32_e32 v108, v108, v28
	v_add_f32_e32 v109, v109, v29
	v_add_f32_e32 v110, v110, v30
	v_add_f32_e32 v111, v111, v31
	v_add_f32_e32 v112, v112, v32
	v_add_f32_e32 v113, v113, v33
	v_add_f32_e32 v114, v114, v34
	v_add_f32_e32 v115, v115, v35
	v_add_f32_e32 v116, v116, v36
	v_add_f32_e32 v117, v117, v37
	v_add_f32_e32 v118, v118, v38
	v_add_f32_e32 v119, v119, v39
	v_mul_f32_e32 v184, v104, v104
	v_fmac_f32_e32 v184, v105, v105
	v_fmac_f32_e32 v184, v106, v106
	v_fmac_f32_e32 v184, v107, v107
	v_fmac_f32_e32 v184, v108, v108
	v_fmac_f32_e32 v184, v109, v109
	v_fmac_f32_e32 v184, v110, v110
	v_fmac_f32_e32 v184, v111, v111
	v_fmac_f32_e32 v184, v112, v112
	v_fmac_f32_e32 v184, v113, v113
	v_fmac_f32_e32 v184, v114, v114
	v_fmac_f32_e32 v184, v115, v115
	v_fmac_f32_e32 v184, v116, v116
	v_fmac_f32_e32 v184, v117, v117
	v_fmac_f32_e32 v184, v118, v118
	v_fmac_f32_e32 v184, v119, v119
	v_mov_b32_e32 v185, v184
	s_nop 1
	v_permlane16_swap_b32_e32 v184, v185
	v_add_f32_e32 v184, v184, v185
	v_mov_b32_e32 v185, v184
	s_nop 1
	v_permlane32_swap_b32_e32 v184, v185
	v_add_f32_e32 v184, v184, v185
	v_mov_b32_e32 v186, 0x358637bd
	v_fmac_f32_e32 v186, 0x3c800000, v184
	v_rsq_f32_e32 v186, v186
	s_nop 0
	v_mul_f32_e32 v186, v187, v186
	v_mul_f32_e32 v104, v104, v186
	v_mul_f32_e32 v105, v105, v186
	v_mul_f32_e32 v106, v106, v186
	v_mul_f32_e32 v107, v107, v186
	v_mul_f32_e32 v104, v104, v40
	v_mul_f32_e32 v105, v105, v41
	v_mul_f32_e32 v106, v106, v42
	v_mul_f32_e32 v107, v107, v43
	v_cvt_pk_f16_f32 v104, v104, v105
	v_cvt_pk_f16_f32 v105, v106, v107
	global_store_dwordx2 v23, v[104:105], s[22:23] offset:256
	v_mul_f32_e32 v108, v108, v186
	v_mul_f32_e32 v109, v109, v186
	v_mul_f32_e32 v110, v110, v186
	v_mul_f32_e32 v111, v111, v186
	v_mul_f32_e32 v108, v108, v44
	v_mul_f32_e32 v109, v109, v45
	v_mul_f32_e32 v110, v110, v46
	v_mul_f32_e32 v111, v111, v47
	v_cvt_pk_f16_f32 v108, v108, v109
	v_cvt_pk_f16_f32 v109, v110, v111
	global_store_dwordx2 v23, v[108:109], s[22:23] offset:1280
	v_mul_f32_e32 v112, v112, v186
	v_mul_f32_e32 v113, v113, v186
	v_mul_f32_e32 v114, v114, v186
	v_mul_f32_e32 v115, v115, v186
	v_mul_f32_e32 v112, v112, v48
	v_mul_f32_e32 v113, v113, v49
	v_mul_f32_e32 v114, v114, v50
	v_mul_f32_e32 v115, v115, v51
	v_cvt_pk_f16_f32 v112, v112, v113
	v_cvt_pk_f16_f32 v113, v114, v115
	global_store_dwordx2 v23, v[112:113], s[22:23] offset:2304
	v_mul_f32_e32 v116, v116, v186
	v_mul_f32_e32 v117, v117, v186
	v_mul_f32_e32 v118, v118, v186
	v_mul_f32_e32 v119, v119, v186
	v_mul_f32_e32 v116, v116, v52
	v_mul_f32_e32 v117, v117, v53
	v_mul_f32_e32 v118, v118, v54
	v_mul_f32_e32 v119, v119, v55
	v_cvt_pk_f16_f32 v116, v116, v117
	v_cvt_pk_f16_f32 v117, v118, v119
	global_store_dwordx2 v23, v[116:117], s[22:23] offset:3328
	s_endpgm
.Lpf_v:
	v_lshlrev_b32_e32 v5, 2, v3
	global_load_dword v24, v5, s[14:15] offset:0
	global_load_dword v25, v5, s[14:15] offset:64
	global_load_dword v26, v5, s[14:15] offset:128
	global_load_dword v27, v5, s[14:15] offset:192
	s_lshl_b32 s8, s27, 7
	s_lshr_b32 s24, s10, 4
	s_add_u32 s8, s8, s24
	s_lshl_b32 s24, s25, 2
	s_add_u32 s8, s8, s24
	s_lshl_b32 s8, s8, 11
	s_add_u32 s22, s22, s8
	s_addc_u32 s23, s23, 0
	s_add_u32 m0, s28, 0x0
	s_nop 0
	global_load_lds_dwordx4 v10, s[4:5]
	s_add_u32 m0, s28, 0x2000
	s_nop 0
	global_load_lds_dwordx4 v11, s[4:5]
	s_add_u32 m0, s28, 0x4000
	s_nop 0
	global_load_lds_dwordx4 v12, s[4:5]
	s_add_u32 m0, s28, 0x6000
	s_nop 0
	global_load_lds_dwordx4 v13, s[4:5]
	s_add_u32 m0, s28, 0x8000
	s_nop 0
	global_load_lds_dwordx4 v10, s[6:7]
	s_add_u32 m0, s28, 0xa000
	s_nop 0
	global_load_lds_dwordx4 v11, s[6:7]
	s_add_u32 s4, s4, s20
	s_addc_u32 s5, s5, 0
	s_add_u32 s6, s6, s20
	s_addc_u32 s7, s7, 0
	s_add_u32 m0, s28, 0xc000
	s_nop 0
	global_load_lds_dwordx4 v10, s[4:5]
	s_add_u32 m0, s28, 0xe000
	s_nop 0
	global_load_lds_dwordx4 v11, s[4:5]
	s_add_u32 m0, s28, 0x10000
	s_nop 0
	global_load_lds_dwordx4 v12, s[4:5]
	s_add_u32 m0, s28, 0x12000
	s_nop 0
	global_load_lds_dwordx4 v13, s[4:5]
	s_add_u32 m0, s28, 0x14000
	s_nop 0
	global_load_lds_dwordx4 v10, s[6:7]
	s_add_u32 m0, s28, 0x16000
	s_nop 0
	global_load_lds_dwordx4 v11, s[6:7]
	s_add_u32 s4, s4, s20
	s_addc_u32 s5, s5, 0
	s_add_u32 s6, s6, s20
	s_addc_u32 s7, s7, 0
	s_add_u32 m0, s28, 0x18000
	s_nop 0
	global_load_lds_dwordx4 v10, s[4:5]
	s_add_u32 m0, s28, 0x1a000
	s_nop 0
	global_load_lds_dwordx4 v11, s[4:5]
	s_add_u32 m0, s28, 0x1c000
	s_nop 0
	global_load_lds_dwordx4 v12, s[4:5]
	s_add_u32 m0, s28, 0x1e000
	s_nop 0
	global_load_lds_dwordx4 v13, s[4:5]
	s_add_u32 m0, s28, 0x20000
	s_nop 0
	global_load_lds_dwordx4 v10, s[6:7]
	s_add_u32 m0, s28, 0x22000
	s_nop 0
	global_load_lds_dwordx4 v11, s[6:7]
	s_add_u32 s4, s4, s20
	s_addc_u32 s5, s5, 0
	s_add_u32 s6, s6, s20
	s_addc_u32 s7, s7, 0
	s_waitcnt vmcnt(12)
	s_barrier
	s_waitcnt lgkmcnt(7)
	ds_read_b128 v[120:123], v14
	ds_read_b128 v[136:139], v16
	ds_read_b128 v[140:143], v16 offset:2048
	ds_read_b128 v[144:147], v16 offset:4096
	ds_read_b128 v[148:151], v16 offset:6144
	ds_read_b128 v[124:127], v14 offset:2048
	ds_read_b128 v[128:131], v14 offset:4096
	ds_read_b128 v[132:135], v14 offset:6144
	s_waitcnt lgkmcnt(7)
	ds_read_b128 v[152:155], v15
	ds_read_b128 v[168:171], v17
	ds_read_b128 v[172:175], v17 offset:2048
	ds_read_b128 v[176:179], v17 offset:4096
	ds_read_b128 v[180:183], v17 offset:6144
	ds_read_b128 v[156:159], v15 offset:2048
	ds_read_b128 v[160:163], v15 offset:4096
	ds_read_b128 v[164:167], v15 offset:6144
	s_waitcnt lgkmcnt(14)
	v_mfma_f32_16x16x32_f16 v[56:59], v[120:123], v[136:139], 0
	s_waitcnt lgkmcnt(13)
	v_mfma_f32_16x16x32_f16 v[60:63], v[120:123], v[140:143], 0
	s_waitcnt lgkmcnt(12)
	v_mfma_f32_16x16x32_f16 v[64:67], v[120:123], v[144:147], 0
	s_waitcnt lgkmcnt(11)
	v_mfma_f32_16x16x32_f16 v[68:71], v[120:123], v[148:151], 0
	s_waitcnt lgkmcnt(10)
	v_mfma_f32_16x16x32_f16 v[72:75], v[124:127], v[136:139], 0
	v_mfma_f32_16x16x32_f16 v[76:79], v[124:127], v[140:143], 0
	v_mfma_f32_16x16x32_f16 v[80:83], v[124:127], v[144:147], 0
	v_mfma_f32_16x16x32_f16 v[84:87], v[124:127], v[148:151], 0
	s_waitcnt lgkmcnt(9)
	v_mfma_f32_16x16x32_f16 v[88:91], v[128:131], v[136:139], 0
	v_mfma_f32_16x16x32_f16 v[92:95], v[128:131], v[140:143], 0
	v_mfma_f32_16x16x32_f16 v[96:99], v[128:131], v[144:147], 0
	v_mfma_f32_16x16x32_f16 v[100:103], v[128:131], v[148:151], 0
	s_waitcnt lgkmcnt(8)
	v_mfma_f32_16x16x32_f16 v[104:107], v[132:135], v[136:139], 0
	v_mfma_f32_16x16x32_f16 v[108:111], v[132:135], v[140:143], 0
	v_mfma_f32_16x16x32_f16 v[112:115], v[132:135], v[144:147], 0
	v_mfma_f32_16x16x32_f16 v[116:119], v[132:135], v[148:151], 0
	s_waitcnt vmcnt(6) lgkmcnt(0)
	s_barrier
	s_add_u32 m0, s28, 0x0
	s_nop 0
	global_load_lds_dwordx4 v10, s[4:5]
	s_add_u32 m0, s28, 0x2000
	s_nop 0
	global_load_lds_dwordx4 v11, s[4:5]
	s_add_u32 m0, s28, 0x4000
	s_nop 0
	global_load_lds_dwordx4 v12, s[4:5]
	s_add_u32 m0, s28, 0x6000
	s_nop 0
	global_load_lds_dwordx4 v13, s[4:5]
	s_add_u32 m0, s28, 0x8000
	s_nop 0
	global_load_lds_dwordx4 v10, s[6:7]
	s_add_u32 m0, s28, 0xa000
	s_nop 0
	global_load_lds_dwordx4 v11, s[6:7]
	s_add_u32 s4, s4, s20
	s_addc_u32 s5, s5, 0
	s_add_u32 s6, s6, s20
	s_addc_u32 s7, s7, 0
	s_waitcnt lgkmcnt(7)
	ds_read_b128 v[120:123], v14 offset:49152
	ds_read_b128 v[136:139], v16 offset:49152
	ds_read_b128 v[140:143], v16 offset:51200
	ds_read_b128 v[144:147], v16 offset:53248
	ds_read_b128 v[148:151], v16 offset:55296
	ds_read_b128 v[124:127], v14 offset:51200
	ds_read_b128 v[128:131], v14 offset:53248
	ds_read_b128 v[132:135], v14 offset:55296
	s_waitcnt lgkmcnt(14)
	v_mfma_f32_16x16x32_f16 v[56:59], v[152:155], v[168:171], v[56:59]
	s_waitcnt lgkmcnt(13)
	v_mfma_f32_16x16x32_f16 v[60:63], v[152:155], v[172:175], v[60:63]
	s_waitcnt lgkmcnt(12)
	v_mfma_f32_16x16x32_f16 v[64:67], v[152:155], v[176:179], v[64:67]
	s_waitcnt lgkmcnt(11)
	v_mfma_f32_16x16x32_f16 v[68:71], v[152:155], v[180:183], v[68:71]
	s_waitcnt lgkmcnt(10)
	v_mfma_f32_16x16x32_f16 v[72:75], v[156:159], v[168:171], v[72:75]
	v_mfma_f32_16x16x32_f16 v[76:79], v[156:159], v[172:175], v[76:79]
	v_mfma_f32_16x16x32_f16 v[80:83], v[156:159], v[176:179], v[80:83]
	v_mfma_f32_16x16x32_f16 v[84:87], v[156:159], v[180:183], v[84:87]
	s_waitcnt lgkmcnt(9)
	v_mfma_f32_16x16x32_f16 v[88:91], v[160:163], v[168:171], v[88:91]
	v_mfma_f32_16x16x32_f16 v[92:95], v[160:163], v[172:175], v[92:95]
	v_mfma_f32_16x16x32_f16 v[96:99], v[160:163], v[176:179], v[96:99]
	v_mfma_f32_16x16x32_f16 v[100:103], v[160:163], v[180:183], v[100:103]
	s_waitcnt lgkmcnt(8)
	v_mfma_f32_16x16x32_f16 v[104:107], v[164:167], v[168:171], v[104:107]
	v_mfma_f32_16x16x32_f16 v[108:111], v[164:167], v[172:175], v[108:111]
	v_mfma_f32_16x16x32_f16 v[112:115], v[164:167], v[176:179], v[112:115]
	v_mfma_f32_16x16x32_f16 v[116:119], v[164:167], v[180:183], v[116:119]
	s_waitcnt lgkmcnt(7)
	ds_read_b128 v[152:155], v15 offset:49152
	ds_read_b128 v[168:171], v17 offset:49152
	ds_read_b128 v[172:175], v17 offset:51200
	ds_read_b128 v[176:179], v17 offset:53248
	ds_read_b128 v[180:183], v17 offset:55296
	ds_read_b128 v[156:159], v15 offset:51200
	ds_read_b128 v[160:163], v15 offset:53248
	ds_read_b128 v[164:167], v15 offset:55296
	s_waitcnt lgkmcnt(14)
	v_mfma_f32_16x16x32_f16 v[56:59], v[120:123], v[136:139], v[56:59]
	s_waitcnt lgkmcnt(13)
	v_mfma_f32_16x16x32_f16 v[60:63], v[120:123], v[140:143], v[60:63]
	s_waitcnt lgkmcnt(12)
	v_mfma_f32_16x16x32_f16 v[64:67], v[120:123], v[144:147], v[64:67]
	s_waitcnt lgkmcnt(11)
	v_mfma_f32_16x16x32_f16 v[68:71], v[120:123], v[148:151], v[68:71]
	s_waitcnt lgkmcnt(10)
	v_mfma_f32_16x16x32_f16 v[72:75], v[124:127], v[136:139], v[72:75]
	v_mfma_f32_16x16x32_f16 v[76:79], v[124:127], v[140:143], v[76:79]
	v_mfma_f32_16x16x32_f16 v[80:83], v[124:127], v[144:147], v[80:83]
	v_mfma_f32_16x16x32_f16 v[84:87], v[124:127], v[148:151], v[84:87]
	s_waitcnt lgkmcnt(9)
	v_mfma_f32_16x16x32_f16 v[88:91], v[128:131], v[136:139], v[88:91]
	v_mfma_f32_16x16x32_f16 v[92:95], v[128:131], v[140:143], v[92:95]
	v_mfma_f32_16x16x32_f16 v[96:99], v[128:131], v[144:147], v[96:99]
	v_mfma_f32_16x16x32_f16 v[100:103], v[128:131], v[148:151], v[100:103]
	s_waitcnt lgkmcnt(8)
	v_mfma_f32_16x16x32_f16 v[104:107], v[132:135], v[136:139], v[104:107]
	v_mfma_f32_16x16x32_f16 v[108:111], v[132:135], v[140:143], v[108:111]
	v_mfma_f32_16x16x32_f16 v[112:115], v[132:135], v[144:147], v[112:115]
	v_mfma_f32_16x16x32_f16 v[116:119], v[132:135], v[148:151], v[116:119]
	s_waitcnt vmcnt(6) lgkmcnt(0)
	s_barrier
	s_add_u32 m0, s28, 0xc000
	s_nop 0
	global_load_lds_dwordx4 v10, s[4:5]
	s_add_u32 m0, s28, 0xe000
	s_nop 0
	global_load_lds_dwordx4 v11, s[4:5]
	s_add_u32 m0, s28, 0x10000
	s_nop 0
	global_load_lds_dwordx4 v12, s[4:5]
	s_add_u32 m0, s28, 0x12000
	s_nop 0
	global_load_lds_dwordx4 v13, s[4:5]
	s_add_u32 m0, s28, 0x14000
	s_nop 0
	global_load_lds_dwordx4 v10, s[6:7]
	s_add_u32 m0, s28, 0x16000
	s_nop 0
	global_load_lds_dwordx4 v11, s[6:7]
	s_add_u32 s4, s4, s20
	s_addc_u32 s5, s5, 0
	s_add_u32 s6, s6, s20
	s_addc_u32 s7, s7, 0
	s_waitcnt lgkmcnt(7)
	ds_read_b128 v[120:123], v18
	ds_read_b128 v[136:139], v20
	ds_read_b128 v[140:143], v20 offset:2048
	ds_read_b128 v[144:147], v20 offset:4096
	ds_read_b128 v[148:151], v20 offset:6144
	ds_read_b128 v[124:127], v18 offset:2048
	ds_read_b128 v[128:131], v18 offset:4096
	ds_read_b128 v[132:135], v18 offset:6144
	s_waitcnt lgkmcnt(14)
	v_mfma_f32_16x16x32_f16 v[56:59], v[152:155], v[168:171], v[56:59]
	s_waitcnt lgkmcnt(13)
	v_mfma_f32_16x16x32_f16 v[60:63], v[152:155], v[172:175], v[60:63]
	s_waitcnt lgkmcnt(12)
	v_mfma_f32_16x16x32_f16 v[64:67], v[152:155], v[176:179], v[64:67]
	s_waitcnt lgkmcnt(11)
	v_mfma_f32_16x16x32_f16 v[68:71], v[152:155], v[180:183], v[68:71]
	s_waitcnt lgkmcnt(10)
	v_mfma_f32_16x16x32_f16 v[72:75], v[156:159], v[168:171], v[72:75]
	v_mfma_f32_16x16x32_f16 v[76:79], v[156:159], v[172:175], v[76:79]
	v_mfma_f32_16x16x32_f16 v[80:83], v[156:159], v[176:179], v[80:83]
	v_mfma_f32_16x16x32_f16 v[84:87], v[156:159], v[180:183], v[84:87]
	s_waitcnt lgkmcnt(9)
	v_mfma_f32_16x16x32_f16 v[88:91], v[160:163], v[168:171], v[88:91]
	v_mfma_f32_16x16x32_f16 v[92:95], v[160:163], v[172:175], v[92:95]
	v_mfma_f32_16x16x32_f16 v[96:99], v[160:163], v[176:179], v[96:99]
	v_mfma_f32_16x16x32_f16 v[100:103], v[160:163], v[180:183], v[100:103]
	s_waitcnt lgkmcnt(8)
	v_mfma_f32_16x16x32_f16 v[104:107], v[164:167], v[168:171], v[104:107]
	v_mfma_f32_16x16x32_f16 v[108:111], v[164:167], v[172:175], v[108:111]
	v_mfma_f32_16x16x32_f16 v[112:115], v[164:167], v[176:179], v[112:115]
	v_mfma_f32_16x16x32_f16 v[116:119], v[164:167], v[180:183], v[116:119]
	s_waitcnt lgkmcnt(7)
	ds_read_b128 v[152:155], v19
	ds_read_b128 v[168:171], v21
	ds_read_b128 v[172:175], v21 offset:2048
	ds_read_b128 v[176:179], v21 offset:4096
	ds_read_b128 v[180:183], v21 offset:6144
	ds_read_b128 v[156:159], v19 offset:2048
	ds_read_b128 v[160:163], v19 offset:4096
	ds_read_b128 v[164:167], v19 offset:6144
	s_waitcnt lgkmcnt(14)
	v_mfma_f32_16x16x32_f16 v[56:59], v[120:123], v[136:139], v[56:59]
	s_waitcnt lgkmcnt(13)
	v_mfma_f32_16x16x32_f16 v[60:63], v[120:123], v[140:143], v[60:63]
	s_waitcnt lgkmcnt(12)
	v_mfma_f32_16x16x32_f16 v[64:67], v[120:123], v[144:147], v[64:67]
	s_waitcnt lgkmcnt(11)
	v_mfma_f32_16x16x32_f16 v[68:71], v[120:123], v[148:151], v[68:71]
	s_waitcnt lgkmcnt(10)
	v_mfma_f32_16x16x32_f16 v[72:75], v[124:127], v[136:139], v[72:75]
	v_mfma_f32_16x16x32_f16 v[76:79], v[124:127], v[140:143], v[76:79]
	v_mfma_f32_16x16x32_f16 v[80:83], v[124:127], v[144:147], v[80:83]
	v_mfma_f32_16x16x32_f16 v[84:87], v[124:127], v[148:151], v[84:87]
	s_waitcnt lgkmcnt(9)
	v_mfma_f32_16x16x32_f16 v[88:91], v[128:131], v[136:139], v[88:91]
	v_mfma_f32_16x16x32_f16 v[92:95], v[128:131], v[140:143], v[92:95]
	v_mfma_f32_16x16x32_f16 v[96:99], v[128:131], v[144:147], v[96:99]
	v_mfma_f32_16x16x32_f16 v[100:103], v[128:131], v[148:151], v[100:103]
	s_waitcnt lgkmcnt(8)
	v_mfma_f32_16x16x32_f16 v[104:107], v[132:135], v[136:139], v[104:107]
	v_mfma_f32_16x16x32_f16 v[108:111], v[132:135], v[140:143], v[108:111]
	v_mfma_f32_16x16x32_f16 v[112:115], v[132:135], v[144:147], v[112:115]
	v_mfma_f32_16x16x32_f16 v[116:119], v[132:135], v[148:151], v[116:119]
	s_waitcnt vmcnt(6) lgkmcnt(0)
	s_barrier
	s_add_u32 m0, s28, 0x18000
	s_nop 0
	global_load_lds_dwordx4 v10, s[4:5]
	s_add_u32 m0, s28, 0x1a000
	s_nop 0
	global_load_lds_dwordx4 v11, s[4:5]
	s_add_u32 m0, s28, 0x1c000
	s_nop 0
	global_load_lds_dwordx4 v12, s[4:5]
	s_add_u32 m0, s28, 0x1e000
	s_nop 0
	global_load_lds_dwordx4 v13, s[4:5]
	s_add_u32 m0, s28, 0x20000
	s_nop 0
	global_load_lds_dwordx4 v10, s[6:7]
	s_add_u32 m0, s28, 0x22000
	s_nop 0
	global_load_lds_dwordx4 v11, s[6:7]
	s_add_u32 s4, s4, s20
	s_addc_u32 s5, s5, 0
	s_add_u32 s6, s6, s20
	s_addc_u32 s7, s7, 0
	s_waitcnt lgkmcnt(7)
	ds_read_b128 v[120:123], v14
	ds_read_b128 v[136:139], v16
	ds_read_b128 v[140:143], v16 offset:2048
	ds_read_b128 v[144:147], v16 offset:4096
	ds_read_b128 v[148:151], v16 offset:6144
	ds_read_b128 v[124:127], v14 offset:2048
	ds_read_b128 v[128:131], v14 offset:4096
	ds_read_b128 v[132:135], v14 offset:6144
	s_waitcnt lgkmcnt(14)
	v_mfma_f32_16x16x32_f16 v[56:59], v[152:155], v[168:171], v[56:59]
	s_waitcnt lgkmcnt(13)
	v_mfma_f32_16x16x32_f16 v[60:63], v[152:155], v[172:175], v[60:63]
	s_waitcnt lgkmcnt(12)
	v_mfma_f32_16x16x32_f16 v[64:67], v[152:155], v[176:179], v[64:67]
	s_waitcnt lgkmcnt(11)
	v_mfma_f32_16x16x32_f16 v[68:71], v[152:155], v[180:183], v[68:71]
	s_waitcnt lgkmcnt(10)
	v_mfma_f32_16x16x32_f16 v[72:75], v[156:159], v[168:171], v[72:75]
	v_mfma_f32_16x16x32_f16 v[76:79], v[156:159], v[172:175], v[76:79]
	v_mfma_f32_16x16x32_f16 v[80:83], v[156:159], v[176:179], v[80:83]
	v_mfma_f32_16x16x32_f16 v[84:87], v[156:159], v[180:183], v[84:87]
	s_waitcnt lgkmcnt(9)
	v_mfma_f32_16x16x32_f16 v[88:91], v[160:163], v[168:171], v[88:91]
	v_mfma_f32_16x16x32_f16 v[92:95], v[160:163], v[172:175], v[92:95]
	v_mfma_f32_16x16x32_f16 v[96:99], v[160:163], v[176:179], v[96:99]
	v_mfma_f32_16x16x32_f16 v[100:103], v[160:163], v[180:183], v[100:103]
	s_waitcnt lgkmcnt(8)
	v_mfma_f32_16x16x32_f16 v[104:107], v[164:167], v[168:171], v[104:107]
	v_mfma_f32_16x16x32_f16 v[108:111], v[164:167], v[172:175], v[108:111]
	v_mfma_f32_16x16x32_f16 v[112:115], v[164:167], v[176:179], v[112:115]
	v_mfma_f32_16x16x32_f16 v[116:119], v[164:167], v[180:183], v[116:119]
	s_waitcnt lgkmcnt(7)
	ds_read_b128 v[152:155], v15
	ds_read_b128 v[168:171], v17
	ds_read_b128 v[172:175], v17 offset:2048
	ds_read_b128 v[176:179], v17 offset:4096
	ds_read_b128 v[180:183], v17 offset:6144
	ds_read_b128 v[156:159], v15 offset:2048
	ds_read_b128 v[160:163], v15 offset:4096
	ds_read_b128 v[164:167], v15 offset:6144
	s_waitcnt lgkmcnt(14)
	v_mfma_f32_16x16x32_f16 v[56:59], v[120:123], v[136:139], v[56:59]
	s_waitcnt lgkmcnt(13)
	v_mfma_f32_16x16x32_f16 v[60:63], v[120:123], v[140:143], v[60:63]
	s_waitcnt lgkmcnt(12)
	v_mfma_f32_16x16x32_f16 v[64:67], v[120:123], v[144:147], v[64:67]
	s_waitcnt lgkmcnt(11)
	v_mfma_f32_16x16x32_f16 v[68:71], v[120:123], v[148:151], v[68:71]
	s_waitcnt lgkmcnt(10)
	v_mfma_f32_16x16x32_f16 v[72:75], v[124:127], v[136:139], v[72:75]
	v_mfma_f32_16x16x32_f16 v[76:79], v[124:127], v[140:143], v[76:79]
	v_mfma_f32_16x16x32_f16 v[80:83], v[124:127], v[144:147], v[80:83]
	v_mfma_f32_16x16x32_f16 v[84:87], v[124:127], v[148:151], v[84:87]
	s_waitcnt lgkmcnt(9)
	v_mfma_f32_16x16x32_f16 v[88:91], v[128:131], v[136:139], v[88:91]
	v_mfma_f32_16x16x32_f16 v[92:95], v[128:131], v[140:143], v[92:95]
	v_mfma_f32_16x16x32_f16 v[96:99], v[128:131], v[144:147], v[96:99]
	v_mfma_f32_16x16x32_f16 v[100:103], v[128:131], v[148:151], v[100:103]
	s_waitcnt lgkmcnt(8)
	v_mfma_f32_16x16x32_f16 v[104:107], v[132:135], v[136:139], v[104:107]
	v_mfma_f32_16x16x32_f16 v[108:111], v[132:135], v[140:143], v[108:111]
	v_mfma_f32_16x16x32_f16 v[112:115], v[132:135], v[144:147], v[112:115]
	v_mfma_f32_16x16x32_f16 v[116:119], v[132:135], v[148:151], v[116:119]
	s_waitcnt vmcnt(6) lgkmcnt(0)
	s_barrier
	s_add_u32 m0, s28, 0x0
	s_nop 0
	global_load_lds_dwordx4 v10, s[4:5]
	s_add_u32 m0, s28, 0x2000
	s_nop 0
	global_load_lds_dwordx4 v11, s[4:5]
	s_add_u32 m0, s28, 0x4000
	s_nop 0
	global_load_lds_dwordx4 v12, s[4:5]
	s_add_u32 m0, s28, 0x6000
	s_nop 0
	global_load_lds_dwordx4 v13, s[4:5]
	s_add_u32 m0, s28, 0x8000
	s_nop 0
	global_load_lds_dwordx4 v10, s[6:7]
	s_add_u32 m0, s28, 0xa000
	s_nop 0
	global_load_lds_dwordx4 v11, s[6:7]
	s_add_u32 s4, s4, s20
	s_addc_u32 s5, s5, 0
	s_add_u32 s6, s6, s20
	s_addc_u32 s7, s7, 0
	s_waitcnt lgkmcnt(7)
	ds_read_b128 v[120:123], v14 offset:49152
	ds_read_b128 v[136:139], v16 offset:49152
	ds_read_b128 v[140:143], v16 offset:51200
	ds_read_b128 v[144:147], v16 offset:53248
	ds_read_b128 v[148:151], v16 offset:55296
	ds_read_b128 v[124:127], v14 offset:51200
	ds_read_b128 v[128:131], v14 offset:53248
	ds_read_b128 v[132:135], v14 offset:55296
	s_waitcnt lgkmcnt(14)
	v_mfma_f32_16x16x32_f16 v[56:59], v[152:155], v[168:171], v[56:59]
	s_waitcnt lgkmcnt(13)
	v_mfma_f32_16x16x32_f16 v[60:63], v[152:155], v[172:175], v[60:63]
	s_waitcnt lgkmcnt(12)
	v_mfma_f32_16x16x32_f16 v[64:67], v[152:155], v[176:179], v[64:67]
	s_waitcnt lgkmcnt(11)
	v_mfma_f32_16x16x32_f16 v[68:71], v[152:155], v[180:183], v[68:71]
	s_waitcnt lgkmcnt(10)
	v_mfma_f32_16x16x32_f16 v[72:75], v[156:159], v[168:171], v[72:75]
	v_mfma_f32_16x16x32_f16 v[76:79], v[156:159], v[172:175], v[76:79]
	v_mfma_f32_16x16x32_f16 v[80:83], v[156:159], v[176:179], v[80:83]
	v_mfma_f32_16x16x32_f16 v[84:87], v[156:159], v[180:183], v[84:87]
	s_waitcnt lgkmcnt(9)
	v_mfma_f32_16x16x32_f16 v[88:91], v[160:163], v[168:171], v[88:91]
	v_mfma_f32_16x16x32_f16 v[92:95], v[160:163], v[172:175], v[92:95]
	v_mfma_f32_16x16x32_f16 v[96:99], v[160:163], v[176:179], v[96:99]
	v_mfma_f32_16x16x32_f16 v[100:103], v[160:163], v[180:183], v[100:103]
	s_waitcnt lgkmcnt(8)
	v_mfma_f32_16x16x32_f16 v[104:107], v[164:167], v[168:171], v[104:107]
	v_mfma_f32_16x16x32_f16 v[108:111], v[164:167], v[172:175], v[108:111]
	v_mfma_f32_16x16x32_f16 v[112:115], v[164:167], v[176:179], v[112:115]
	v_mfma_f32_16x16x32_f16 v[116:119], v[164:167], v[180:183], v[116:119]
	s_waitcnt lgkmcnt(7)
	ds_read_b128 v[152:155], v15 offset:49152
	ds_read_b128 v[168:171], v17 offset:49152
	ds_read_b128 v[172:175], v17 offset:51200
	ds_read_b128 v[176:179], v17 offset:53248
	ds_read_b128 v[180:183], v17 offset:55296
	ds_read_b128 v[156:159], v15 offset:51200
	ds_read_b128 v[160:163], v15 offset:53248
	ds_read_b128 v[164:167], v15 offset:55296
	s_waitcnt lgkmcnt(14)
	v_mfma_f32_16x16x32_f16 v[56:59], v[120:123], v[136:139], v[56:59]
	s_waitcnt lgkmcnt(13)
	v_mfma_f32_16x16x32_f16 v[60:63], v[120:123], v[140:143], v[60:63]
	s_waitcnt lgkmcnt(12)
	v_mfma_f32_16x16x32_f16 v[64:67], v[120:123], v[144:147], v[64:67]
	s_waitcnt lgkmcnt(11)
	v_mfma_f32_16x16x32_f16 v[68:71], v[120:123], v[148:151], v[68:71]
	s_waitcnt lgkmcnt(10)
	v_mfma_f32_16x16x32_f16 v[72:75], v[124:127], v[136:139], v[72:75]
	v_mfma_f32_16x16x32_f16 v[76:79], v[124:127], v[140:143], v[76:79]
	v_mfma_f32_16x16x32_f16 v[80:83], v[124:127], v[144:147], v[80:83]
	v_mfma_f32_16x16x32_f16 v[84:87], v[124:127], v[148:151], v[84:87]
	s_waitcnt lgkmcnt(9)
	v_mfma_f32_16x16x32_f16 v[88:91], v[128:131], v[136:139], v[88:91]
	v_mfma_f32_16x16x32_f16 v[92:95], v[128:131], v[140:143], v[92:95]
	v_mfma_f32_16x16x32_f16 v[96:99], v[128:131], v[144:147], v[96:99]
	v_mfma_f32_16x16x32_f16 v[100:103], v[128:131], v[148:151], v[100:103]
	s_waitcnt lgkmcnt(8)
	v_mfma_f32_16x16x32_f16 v[104:107], v[132:135], v[136:139], v[104:107]
	v_mfma_f32_16x16x32_f16 v[108:111], v[132:135], v[140:143], v[108:111]
	v_mfma_f32_16x16x32_f16 v[112:115], v[132:135], v[144:147], v[112:115]
	v_mfma_f32_16x16x32_f16 v[116:119], v[132:135], v[148:151], v[116:119]
	s_waitcnt vmcnt(6) lgkmcnt(0)
	s_barrier
	s_add_u32 m0, s28, 0xc000
	s_nop 0
	global_load_lds_dwordx4 v10, s[4:5]
	s_add_u32 m0, s28, 0xe000
	s_nop 0
	global_load_lds_dwordx4 v11, s[4:5]
	s_add_u32 m0, s28, 0x10000
	s_nop 0
	global_load_lds_dwordx4 v12, s[4:5]
	s_add_u32 m0, s28, 0x12000
	s_nop 0
	global_load_lds_dwordx4 v13, s[4:5]
	s_add_u32 m0, s28, 0x14000
	s_nop 0
	global_load_lds_dwordx4 v10, s[6:7]
	s_add_u32 m0, s28, 0x16000
	s_nop 0
	global_load_lds_dwordx4 v11, s[6:7]
	s_add_u32 s4, s4, s20
	s_addc_u32 s5, s5, 0
	s_add_u32 s6, s6, s20
	s_addc_u32 s7, s7, 0
	s_waitcnt lgkmcnt(7)
	ds_read_b128 v[120:123], v18
	ds_read_b128 v[136:139], v20
	ds_read_b128 v[140:143], v20 offset:2048
	ds_read_b128 v[144:147], v20 offset:4096
	ds_read_b128 v[148:151], v20 offset:6144
	ds_read_b128 v[124:127], v18 offset:2048
	ds_read_b128 v[128:131], v18 offset:4096
	ds_read_b128 v[132:135], v18 offset:6144
	s_waitcnt lgkmcnt(14)
	v_mfma_f32_16x16x32_f16 v[56:59], v[152:155], v[168:171], v[56:59]
	s_waitcnt lgkmcnt(13)
	v_mfma_f32_16x16x32_f16 v[60:63], v[152:155], v[172:175], v[60:63]
	s_waitcnt lgkmcnt(12)
	v_mfma_f32_16x16x32_f16 v[64:67], v[152:155], v[176:179], v[64:67]
	s_waitcnt lgkmcnt(11)
	v_mfma_f32_16x16x32_f16 v[68:71], v[152:155], v[180:183], v[68:71]
	s_waitcnt lgkmcnt(10)
	v_mfma_f32_16x16x32_f16 v[72:75], v[156:159], v[168:171], v[72:75]
	v_mfma_f32_16x16x32_f16 v[76:79], v[156:159], v[172:175], v[76:79]
	v_mfma_f32_16x16x32_f16 v[80:83], v[156:159], v[176:179], v[80:83]
	v_mfma_f32_16x16x32_f16 v[84:87], v[156:159], v[180:183], v[84:87]
	s_waitcnt lgkmcnt(9)
	v_mfma_f32_16x16x32_f16 v[88:91], v[160:163], v[168:171], v[88:91]
	v_mfma_f32_16x16x32_f16 v[92:95], v[160:163], v[172:175], v[92:95]
	v_mfma_f32_16x16x32_f16 v[96:99], v[160:163], v[176:179], v[96:99]
	v_mfma_f32_16x16x32_f16 v[100:103], v[160:163], v[180:183], v[100:103]
	s_waitcnt lgkmcnt(8)
	v_mfma_f32_16x16x32_f16 v[104:107], v[164:167], v[168:171], v[104:107]
	v_mfma_f32_16x16x32_f16 v[108:111], v[164:167], v[172:175], v[108:111]
	v_mfma_f32_16x16x32_f16 v[112:115], v[164:167], v[176:179], v[112:115]
	v_mfma_f32_16x16x32_f16 v[116:119], v[164:167], v[180:183], v[116:119]
	s_waitcnt lgkmcnt(7)
	ds_read_b128 v[152:155], v19
	ds_read_b128 v[168:171], v21
	ds_read_b128 v[172:175], v21 offset:2048
	ds_read_b128 v[176:179], v21 offset:4096
	ds_read_b128 v[180:183], v21 offset:6144
	ds_read_b128 v[156:159], v19 offset:2048
	ds_read_b128 v[160:163], v19 offset:4096
	ds_read_b128 v[164:167], v19 offset:6144
	s_waitcnt lgkmcnt(14)
	v_mfma_f32_16x16x32_f16 v[56:59], v[120:123], v[136:139], v[56:59]
	s_waitcnt lgkmcnt(13)
	v_mfma_f32_16x16x32_f16 v[60:63], v[120:123], v[140:143], v[60:63]
	s_waitcnt lgkmcnt(12)
	v_mfma_f32_16x16x32_f16 v[64:67], v[120:123], v[144:147], v[64:67]
	s_waitcnt lgkmcnt(11)
	v_mfma_f32_16x16x32_f16 v[68:71], v[120:123], v[148:151], v[68:71]
	s_waitcnt lgkmcnt(10)
	v_mfma_f32_16x16x32_f16 v[72:75], v[124:127], v[136:139], v[72:75]
	v_mfma_f32_16x16x32_f16 v[76:79], v[124:127], v[140:143], v[76:79]
	v_mfma_f32_16x16x32_f16 v[80:83], v[124:127], v[144:147], v[80:83]
	v_mfma_f32_16x16x32_f16 v[84:87], v[124:127], v[148:151], v[84:87]
	s_waitcnt lgkmcnt(9)
	v_mfma_f32_16x16x32_f16 v[88:91], v[128:131], v[136:139], v[88:91]
	v_mfma_f32_16x16x32_f16 v[92:95], v[128:131], v[140:143], v[92:95]
	v_mfma_f32_16x16x32_f16 v[96:99], v[128:131], v[144:147], v[96:99]
	v_mfma_f32_16x16x32_f16 v[100:103], v[128:131], v[148:151], v[100:103]
	s_waitcnt lgkmcnt(8)
	v_mfma_f32_16x16x32_f16 v[104:107], v[132:135], v[136:139], v[104:107]
	v_mfma_f32_16x16x32_f16 v[108:111], v[132:135], v[140:143], v[108:111]
	v_mfma_f32_16x16x32_f16 v[112:115], v[132:135], v[144:147], v[112:115]
	v_mfma_f32_16x16x32_f16 v[116:119], v[132:135], v[148:151], v[116:119]
	s_waitcnt vmcnt(6) lgkmcnt(0)
	s_barrier
	s_add_u32 m0, s28, 0x18000
	s_nop 0
	global_load_lds_dwordx4 v10, s[4:5]
	s_add_u32 m0, s28, 0x1a000
	s_nop 0
	global_load_lds_dwordx4 v11, s[4:5]
	s_add_u32 m0, s28, 0x1c000
	s_nop 0
	global_load_lds_dwordx4 v12, s[4:5]
	s_add_u32 m0, s28, 0x1e000
	s_nop 0
	global_load_lds_dwordx4 v13, s[4:5]
	s_add_u32 m0, s28, 0x20000
	s_nop 0
	global_load_lds_dwordx4 v10, s[6:7]
	s_add_u32 m0, s28, 0x22000
	s_nop 0
	global_load_lds_dwordx4 v11, s[6:7]
	s_add_u32 s4, s4, s20
	s_addc_u32 s5, s5, 0
	s_add_u32 s6, s6, s20
	s_addc_u32 s7, s7, 0
	s_waitcnt lgkmcnt(7)
	ds_read_b128 v[120:123], v14
	ds_read_b128 v[136:139], v16
	ds_read_b128 v[140:143], v16 offset:2048
	ds_read_b128 v[144:147], v16 offset:4096
	ds_read_b128 v[148:151], v16 offset:6144
	ds_read_b128 v[124:127], v14 offset:2048
	ds_read_b128 v[128:131], v14 offset:4096
	ds_read_b128 v[132:135], v14 offset:6144
	s_waitcnt lgkmcnt(14)
	v_mfma_f32_16x16x32_f16 v[56:59], v[152:155], v[168:171], v[56:59]
	s_waitcnt lgkmcnt(13)
	v_mfma_f32_16x16x32_f16 v[60:63], v[152:155], v[172:175], v[60:63]
	s_waitcnt lgkmcnt(12)
	v_mfma_f32_16x16x32_f16 v[64:67], v[152:155], v[176:179], v[64:67]
	s_waitcnt lgkmcnt(11)
	v_mfma_f32_16x16x32_f16 v[68:71], v[152:155], v[180:183], v[68:71]
	s_waitcnt lgkmcnt(10)
	v_mfma_f32_16x16x32_f16 v[72:75], v[156:159], v[168:171], v[72:75]
	v_mfma_f32_16x16x32_f16 v[76:79], v[156:159], v[172:175], v[76:79]
	v_mfma_f32_16x16x32_f16 v[80:83], v[156:159], v[176:179], v[80:83]
	v_mfma_f32_16x16x32_f16 v[84:87], v[156:159], v[180:183], v[84:87]
	s_waitcnt lgkmcnt(9)
	v_mfma_f32_16x16x32_f16 v[88:91], v[160:163], v[168:171], v[88:91]
	v_mfma_f32_16x16x32_f16 v[92:95], v[160:163], v[172:175], v[92:95]
	v_mfma_f32_16x16x32_f16 v[96:99], v[160:163], v[176:179], v[96:99]
	v_mfma_f32_16x16x32_f16 v[100:103], v[160:163], v[180:183], v[100:103]
	s_waitcnt lgkmcnt(8)
	v_mfma_f32_16x16x32_f16 v[104:107], v[164:167], v[168:171], v[104:107]
	v_mfma_f32_16x16x32_f16 v[108:111], v[164:167], v[172:175], v[108:111]
	v_mfma_f32_16x16x32_f16 v[112:115], v[164:167], v[176:179], v[112:115]
	v_mfma_f32_16x16x32_f16 v[116:119], v[164:167], v[180:183], v[116:119]
	s_waitcnt lgkmcnt(7)
	ds_read_b128 v[152:155], v15
	ds_read_b128 v[168:171], v17
	ds_read_b128 v[172:175], v17 offset:2048
	ds_read_b128 v[176:179], v17 offset:4096
	ds_read_b128 v[180:183], v17 offset:6144
	ds_read_b128 v[156:159], v15 offset:2048
	ds_read_b128 v[160:163], v15 offset:4096
	ds_read_b128 v[164:167], v15 offset:6144
	s_waitcnt lgkmcnt(14)
	v_mfma_f32_16x16x32_f16 v[56:59], v[120:123], v[136:139], v[56:59]
	s_waitcnt lgkmcnt(13)
	v_mfma_f32_16x16x32_f16 v[60:63], v[120:123], v[140:143], v[60:63]
	s_waitcnt lgkmcnt(12)
	v_mfma_f32_16x16x32_f16 v[64:67], v[120:123], v[144:147], v[64:67]
	s_waitcnt lgkmcnt(11)
	v_mfma_f32_16x16x32_f16 v[68:71], v[120:123], v[148:151], v[68:71]
	s_waitcnt lgkmcnt(10)
	v_mfma_f32_16x16x32_f16 v[72:75], v[124:127], v[136:139], v[72:75]
	v_mfma_f32_16x16x32_f16 v[76:79], v[124:127], v[140:143], v[76:79]
	v_mfma_f32_16x16x32_f16 v[80:83], v[124:127], v[144:147], v[80:83]
	v_mfma_f32_16x16x32_f16 v[84:87], v[124:127], v[148:151], v[84:87]
	s_waitcnt lgkmcnt(9)
	v_mfma_f32_16x16x32_f16 v[88:91], v[128:131], v[136:139], v[88:91]
	v_mfma_f32_16x16x32_f16 v[92:95], v[128:131], v[140:143], v[92:95]
	v_mfma_f32_16x16x32_f16 v[96:99], v[128:131], v[144:147], v[96:99]
	v_mfma_f32_16x16x32_f16 v[100:103], v[128:131], v[148:151], v[100:103]
	s_waitcnt lgkmcnt(8)
	v_mfma_f32_16x16x32_f16 v[104:107], v[132:135], v[136:139], v[104:107]
	v_mfma_f32_16x16x32_f16 v[108:111], v[132:135], v[140:143], v[108:111]
	v_mfma_f32_16x16x32_f16 v[112:115], v[132:135], v[144:147], v[112:115]
	v_mfma_f32_16x16x32_f16 v[116:119], v[132:135], v[148:151], v[116:119]
	s_waitcnt vmcnt(6) lgkmcnt(0)
	s_barrier
	s_add_u32 m0, s28, 0x0
	s_nop 0
	global_load_lds_dwordx4 v10, s[4:5]
	s_add_u32 m0, s28, 0x2000
	s_nop 0
	global_load_lds_dwordx4 v11, s[4:5]
	s_add_u32 m0, s28, 0x4000
	s_nop 0
	global_load_lds_dwordx4 v12, s[4:5]
	s_add_u32 m0, s28, 0x6000
	s_nop 0
	global_load_lds_dwordx4 v13, s[4:5]
	s_add_u32 m0, s28, 0x8000
	s_nop 0
	global_load_lds_dwordx4 v10, s[6:7]
	s_add_u32 m0, s28, 0xa000
	s_nop 0
	global_load_lds_dwordx4 v11, s[6:7]
	s_add_u32 s4, s4, s20
	s_addc_u32 s5, s5, 0
	s_add_u32 s6, s6, s20
	s_addc_u32 s7, s7, 0
	s_waitcnt lgkmcnt(7)
	ds_read_b128 v[120:123], v14 offset:49152
	ds_read_b128 v[136:139], v16 offset:49152
	ds_read_b128 v[140:143], v16 offset:51200
	ds_read_b128 v[144:147], v16 offset:53248
	ds_read_b128 v[148:151], v16 offset:55296
	ds_read_b128 v[124:127], v14 offset:51200
	ds_read_b128 v[128:131], v14 offset:53248
	ds_read_b128 v[132:135], v14 offset:55296
	s_waitcnt lgkmcnt(14)
	v_mfma_f32_16x16x32_f16 v[56:59], v[152:155], v[168:171], v[56:59]
	s_waitcnt lgkmcnt(13)
	v_mfma_f32_16x16x32_f16 v[60:63], v[152:155], v[172:175], v[60:63]
	s_waitcnt lgkmcnt(12)
	v_mfma_f32_16x16x32_f16 v[64:67], v[152:155], v[176:179], v[64:67]
	s_waitcnt lgkmcnt(11)
	v_mfma_f32_16x16x32_f16 v[68:71], v[152:155], v[180:183], v[68:71]
	s_waitcnt lgkmcnt(10)
	v_mfma_f32_16x16x32_f16 v[72:75], v[156:159], v[168:171], v[72:75]
	v_mfma_f32_16x16x32_f16 v[76:79], v[156:159], v[172:175], v[76:79]
	v_mfma_f32_16x16x32_f16 v[80:83], v[156:159], v[176:179], v[80:83]
	v_mfma_f32_16x16x32_f16 v[84:87], v[156:159], v[180:183], v[84:87]
	s_waitcnt lgkmcnt(9)
	v_mfma_f32_16x16x32_f16 v[88:91], v[160:163], v[168:171], v[88:91]
	v_mfma_f32_16x16x32_f16 v[92:95], v[160:163], v[172:175], v[92:95]
	v_mfma_f32_16x16x32_f16 v[96:99], v[160:163], v[176:179], v[96:99]
	v_mfma_f32_16x16x32_f16 v[100:103], v[160:163], v[180:183], v[100:103]
	s_waitcnt lgkmcnt(8)
	v_mfma_f32_16x16x32_f16 v[104:107], v[164:167], v[168:171], v[104:107]
	v_mfma_f32_16x16x32_f16 v[108:111], v[164:167], v[172:175], v[108:111]
	v_mfma_f32_16x16x32_f16 v[112:115], v[164:167], v[176:179], v[112:115]
	v_mfma_f32_16x16x32_f16 v[116:119], v[164:167], v[180:183], v[116:119]
	s_waitcnt lgkmcnt(7)
	ds_read_b128 v[152:155], v15 offset:49152
	ds_read_b128 v[168:171], v17 offset:49152
	ds_read_b128 v[172:175], v17 offset:51200
	ds_read_b128 v[176:179], v17 offset:53248
	ds_read_b128 v[180:183], v17 offset:55296
	ds_read_b128 v[156:159], v15 offset:51200
	ds_read_b128 v[160:163], v15 offset:53248
	ds_read_b128 v[164:167], v15 offset:55296
	s_waitcnt lgkmcnt(14)
	v_mfma_f32_16x16x32_f16 v[56:59], v[120:123], v[136:139], v[56:59]
	s_waitcnt lgkmcnt(13)
	v_mfma_f32_16x16x32_f16 v[60:63], v[120:123], v[140:143], v[60:63]
	s_waitcnt lgkmcnt(12)
	v_mfma_f32_16x16x32_f16 v[64:67], v[120:123], v[144:147], v[64:67]
	s_waitcnt lgkmcnt(11)
	v_mfma_f32_16x16x32_f16 v[68:71], v[120:123], v[148:151], v[68:71]
	s_waitcnt lgkmcnt(10)
	v_mfma_f32_16x16x32_f16 v[72:75], v[124:127], v[136:139], v[72:75]
	v_mfma_f32_16x16x32_f16 v[76:79], v[124:127], v[140:143], v[76:79]
	v_mfma_f32_16x16x32_f16 v[80:83], v[124:127], v[144:147], v[80:83]
	v_mfma_f32_16x16x32_f16 v[84:87], v[124:127], v[148:151], v[84:87]
	s_waitcnt lgkmcnt(9)
	v_mfma_f32_16x16x32_f16 v[88:91], v[128:131], v[136:139], v[88:91]
	v_mfma_f32_16x16x32_f16 v[92:95], v[128:131], v[140:143], v[92:95]
	v_mfma_f32_16x16x32_f16 v[96:99], v[128:131], v[144:147], v[96:99]
	v_mfma_f32_16x16x32_f16 v[100:103], v[128:131], v[148:151], v[100:103]
	s_waitcnt lgkmcnt(8)
	v_mfma_f32_16x16x32_f16 v[104:107], v[132:135], v[136:139], v[104:107]
	v_mfma_f32_16x16x32_f16 v[108:111], v[132:135], v[140:143], v[108:111]
	v_mfma_f32_16x16x32_f16 v[112:115], v[132:135], v[144:147], v[112:115]
	v_mfma_f32_16x16x32_f16 v[116:119], v[132:135], v[148:151], v[116:119]
	s_waitcnt vmcnt(6) lgkmcnt(0)
	s_barrier
	s_add_u32 m0, s28, 0xc000
	s_nop 0
	global_load_lds_dwordx4 v10, s[4:5]
	s_add_u32 m0, s28, 0xe000
	s_nop 0
	global_load_lds_dwordx4 v11, s[4:5]
	s_add_u32 m0, s28, 0x10000
	s_nop 0
	global_load_lds_dwordx4 v12, s[4:5]
	s_add_u32 m0, s28, 0x12000
	s_nop 0
	global_load_lds_dwordx4 v13, s[4:5]
	s_add_u32 m0, s28, 0x14000
	s_nop 0
	global_load_lds_dwordx4 v10, s[6:7]
	s_add_u32 m0, s28, 0x16000
	s_nop 0
	global_load_lds_dwordx4 v11, s[6:7]
	s_add_u32 s4, s4, s20
	s_addc_u32 s5, s5, 0
	s_add_u32 s6, s6, s20
	s_addc_u32 s7, s7, 0
	s_waitcnt lgkmcnt(7)
	ds_read_b128 v[120:123], v18
	ds_read_b128 v[136:139], v20
	ds_read_b128 v[140:143], v20 offset:2048
	ds_read_b128 v[144:147], v20 offset:4096
	ds_read_b128 v[148:151], v20 offset:6144
	ds_read_b128 v[124:127], v18 offset:2048
	ds_read_b128 v[128:131], v18 offset:4096
	ds_read_b128 v[132:135], v18 offset:6144
	s_waitcnt lgkmcnt(14)
	v_mfma_f32_16x16x32_f16 v[56:59], v[152:155], v[168:171], v[56:59]
	s_waitcnt lgkmcnt(13)
	v_mfma_f32_16x16x32_f16 v[60:63], v[152:155], v[172:175], v[60:63]
	s_waitcnt lgkmcnt(12)
	v_mfma_f32_16x16x32_f16 v[64:67], v[152:155], v[176:179], v[64:67]
	s_waitcnt lgkmcnt(11)
	v_mfma_f32_16x16x32_f16 v[68:71], v[152:155], v[180:183], v[68:71]
	s_waitcnt lgkmcnt(10)
	v_mfma_f32_16x16x32_f16 v[72:75], v[156:159], v[168:171], v[72:75]
	v_mfma_f32_16x16x32_f16 v[76:79], v[156:159], v[172:175], v[76:79]
	v_mfma_f32_16x16x32_f16 v[80:83], v[156:159], v[176:179], v[80:83]
	v_mfma_f32_16x16x32_f16 v[84:87], v[156:159], v[180:183], v[84:87]
	s_waitcnt lgkmcnt(9)
	v_mfma_f32_16x16x32_f16 v[88:91], v[160:163], v[168:171], v[88:91]
	v_mfma_f32_16x16x32_f16 v[92:95], v[160:163], v[172:175], v[92:95]
	v_mfma_f32_16x16x32_f16 v[96:99], v[160:163], v[176:179], v[96:99]
	v_mfma_f32_16x16x32_f16 v[100:103], v[160:163], v[180:183], v[100:103]
	s_waitcnt lgkmcnt(8)
	v_mfma_f32_16x16x32_f16 v[104:107], v[164:167], v[168:171], v[104:107]
	v_mfma_f32_16x16x32_f16 v[108:111], v[164:167], v[172:175], v[108:111]
	v_mfma_f32_16x16x32_f16 v[112:115], v[164:167], v[176:179], v[112:115]
	v_mfma_f32_16x16x32_f16 v[116:119], v[164:167], v[180:183], v[116:119]
	s_waitcnt lgkmcnt(7)
	ds_read_b128 v[152:155], v19
	ds_read_b128 v[168:171], v21
	ds_read_b128 v[172:175], v21 offset:2048
	ds_read_b128 v[176:179], v21 offset:4096
	ds_read_b128 v[180:183], v21 offset:6144
	ds_read_b128 v[156:159], v19 offset:2048
	ds_read_b128 v[160:163], v19 offset:4096
	ds_read_b128 v[164:167], v19 offset:6144
	s_waitcnt lgkmcnt(14)
	v_mfma_f32_16x16x32_f16 v[56:59], v[120:123], v[136:139], v[56:59]
	s_waitcnt lgkmcnt(13)
	v_mfma_f32_16x16x32_f16 v[60:63], v[120:123], v[140:143], v[60:63]
	s_waitcnt lgkmcnt(12)
	v_mfma_f32_16x16x32_f16 v[64:67], v[120:123], v[144:147], v[64:67]
	s_waitcnt lgkmcnt(11)
	v_mfma_f32_16x16x32_f16 v[68:71], v[120:123], v[148:151], v[68:71]
	s_waitcnt lgkmcnt(10)
	v_mfma_f32_16x16x32_f16 v[72:75], v[124:127], v[136:139], v[72:75]
	v_mfma_f32_16x16x32_f16 v[76:79], v[124:127], v[140:143], v[76:79]
	v_mfma_f32_16x16x32_f16 v[80:83], v[124:127], v[144:147], v[80:83]
	v_mfma_f32_16x16x32_f16 v[84:87], v[124:127], v[148:151], v[84:87]
	s_waitcnt lgkmcnt(9)
	v_mfma_f32_16x16x32_f16 v[88:91], v[128:131], v[136:139], v[88:91]
	v_mfma_f32_16x16x32_f16 v[92:95], v[128:131], v[140:143], v[92:95]
	v_mfma_f32_16x16x32_f16 v[96:99], v[128:131], v[144:147], v[96:99]
	v_mfma_f32_16x16x32_f16 v[100:103], v[128:131], v[148:151], v[100:103]
	s_waitcnt lgkmcnt(8)
	v_mfma_f32_16x16x32_f16 v[104:107], v[132:135], v[136:139], v[104:107]
	v_mfma_f32_16x16x32_f16 v[108:111], v[132:135], v[140:143], v[108:111]
	v_mfma_f32_16x16x32_f16 v[112:115], v[132:135], v[144:147], v[112:115]
	v_mfma_f32_16x16x32_f16 v[116:119], v[132:135], v[148:151], v[116:119]
	s_waitcnt vmcnt(6) lgkmcnt(0)
	s_barrier
	s_add_u32 m0, s28, 0x18000
	s_nop 0
	global_load_lds_dwordx4 v10, s[4:5]
	s_add_u32 m0, s28, 0x1a000
	s_nop 0
	global_load_lds_dwordx4 v11, s[4:5]
	s_add_u32 m0, s28, 0x1c000
	s_nop 0
	global_load_lds_dwordx4 v12, s[4:5]
	s_add_u32 m0, s28, 0x1e000
	s_nop 0
	global_load_lds_dwordx4 v13, s[4:5]
	s_add_u32 m0, s28, 0x20000
	s_nop 0
	global_load_lds_dwordx4 v10, s[6:7]
	s_add_u32 m0, s28, 0x22000
	s_nop 0
	global_load_lds_dwordx4 v11, s[6:7]
	s_add_u32 s4, s4, s20
	s_addc_u32 s5, s5, 0
	s_add_u32 s6, s6, s20
	s_addc_u32 s7, s7, 0
	s_waitcnt lgkmcnt(7)
	ds_read_b128 v[120:123], v14
	ds_read_b128 v[136:139], v16
	ds_read_b128 v[140:143], v16 offset:2048
	ds_read_b128 v[144:147], v16 offset:4096
	ds_read_b128 v[148:151], v16 offset:6144
	ds_read_b128 v[124:127], v14 offset:2048
	ds_read_b128 v[128:131], v14 offset:4096
	ds_read_b128 v[132:135], v14 offset:6144
	s_waitcnt lgkmcnt(14)
	v_mfma_f32_16x16x32_f16 v[56:59], v[152:155], v[168:171], v[56:59]
	s_waitcnt lgkmcnt(13)
	v_mfma_f32_16x16x32_f16 v[60:63], v[152:155], v[172:175], v[60:63]
	s_waitcnt lgkmcnt(12)
	v_mfma_f32_16x16x32_f16 v[64:67], v[152:155], v[176:179], v[64:67]
	s_waitcnt lgkmcnt(11)
	v_mfma_f32_16x16x32_f16 v[68:71], v[152:155], v[180:183], v[68:71]
	s_waitcnt lgkmcnt(10)
	v_mfma_f32_16x16x32_f16 v[72:75], v[156:159], v[168:171], v[72:75]
	v_mfma_f32_16x16x32_f16 v[76:79], v[156:159], v[172:175], v[76:79]
	v_mfma_f32_16x16x32_f16 v[80:83], v[156:159], v[176:179], v[80:83]
	v_mfma_f32_16x16x32_f16 v[84:87], v[156:159], v[180:183], v[84:87]
	s_waitcnt lgkmcnt(9)
	v_mfma_f32_16x16x32_f16 v[88:91], v[160:163], v[168:171], v[88:91]
	v_mfma_f32_16x16x32_f16 v[92:95], v[160:163], v[172:175], v[92:95]
	v_mfma_f32_16x16x32_f16 v[96:99], v[160:163], v[176:179], v[96:99]
	v_mfma_f32_16x16x32_f16 v[100:103], v[160:163], v[180:183], v[100:103]
	s_waitcnt lgkmcnt(8)
	v_mfma_f32_16x16x32_f16 v[104:107], v[164:167], v[168:171], v[104:107]
	v_mfma_f32_16x16x32_f16 v[108:111], v[164:167], v[172:175], v[108:111]
	v_mfma_f32_16x16x32_f16 v[112:115], v[164:167], v[176:179], v[112:115]
	v_mfma_f32_16x16x32_f16 v[116:119], v[164:167], v[180:183], v[116:119]
	s_waitcnt lgkmcnt(7)
	ds_read_b128 v[152:155], v15
	ds_read_b128 v[168:171], v17
	ds_read_b128 v[172:175], v17 offset:2048
	ds_read_b128 v[176:179], v17 offset:4096
	ds_read_b128 v[180:183], v17 offset:6144
	ds_read_b128 v[156:159], v15 offset:2048
	ds_read_b128 v[160:163], v15 offset:4096
	ds_read_b128 v[164:167], v15 offset:6144
	s_waitcnt lgkmcnt(14)
	v_mfma_f32_16x16x32_f16 v[56:59], v[120:123], v[136:139], v[56:59]
	s_waitcnt lgkmcnt(13)
	v_mfma_f32_16x16x32_f16 v[60:63], v[120:123], v[140:143], v[60:63]
	s_waitcnt lgkmcnt(12)
	v_mfma_f32_16x16x32_f16 v[64:67], v[120:123], v[144:147], v[64:67]
	s_waitcnt lgkmcnt(11)
	v_mfma_f32_16x16x32_f16 v[68:71], v[120:123], v[148:151], v[68:71]
	s_waitcnt lgkmcnt(10)
	v_mfma_f32_16x16x32_f16 v[72:75], v[124:127], v[136:139], v[72:75]
	v_mfma_f32_16x16x32_f16 v[76:79], v[124:127], v[140:143], v[76:79]
	v_mfma_f32_16x16x32_f16 v[80:83], v[124:127], v[144:147], v[80:83]
	v_mfma_f32_16x16x32_f16 v[84:87], v[124:127], v[148:151], v[84:87]
	s_waitcnt lgkmcnt(9)
	v_mfma_f32_16x16x32_f16 v[88:91], v[128:131], v[136:139], v[88:91]
	v_mfma_f32_16x16x32_f16 v[92:95], v[128:131], v[140:143], v[92:95]
	v_mfma_f32_16x16x32_f16 v[96:99], v[128:131], v[144:147], v[96:99]
	v_mfma_f32_16x16x32_f16 v[100:103], v[128:131], v[148:151], v[100:103]
	s_waitcnt lgkmcnt(8)
	v_mfma_f32_16x16x32_f16 v[104:107], v[132:135], v[136:139], v[104:107]
	v_mfma_f32_16x16x32_f16 v[108:111], v[132:135], v[140:143], v[108:111]
	v_mfma_f32_16x16x32_f16 v[112:115], v[132:135], v[144:147], v[112:115]
	v_mfma_f32_16x16x32_f16 v[116:119], v[132:135], v[148:151], v[116:119]
	s_waitcnt vmcnt(6) lgkmcnt(0)
	s_barrier
	s_add_u32 m0, s28, 0x0
	s_nop 0
	global_load_lds_dwordx4 v10, s[4:5]
	s_add_u32 m0, s28, 0x2000
	s_nop 0
	global_load_lds_dwordx4 v11, s[4:5]
	s_add_u32 m0, s28, 0x4000
	s_nop 0
	global_load_lds_dwordx4 v12, s[4:5]
	s_add_u32 m0, s28, 0x6000
	s_nop 0
	global_load_lds_dwordx4 v13, s[4:5]
	s_add_u32 m0, s28, 0x8000
	s_nop 0
	global_load_lds_dwordx4 v10, s[6:7]
	s_add_u32 m0, s28, 0xa000
	s_nop 0
	global_load_lds_dwordx4 v11, s[6:7]
	s_add_u32 s4, s4, s20
	s_addc_u32 s5, s5, 0
	s_add_u32 s6, s6, s20
	s_addc_u32 s7, s7, 0
	s_waitcnt lgkmcnt(7)
	ds_read_b128 v[120:123], v14 offset:49152
	ds_read_b128 v[136:139], v16 offset:49152
	ds_read_b128 v[140:143], v16 offset:51200
	ds_read_b128 v[144:147], v16 offset:53248
	ds_read_b128 v[148:151], v16 offset:55296
	ds_read_b128 v[124:127], v14 offset:51200
	ds_read_b128 v[128:131], v14 offset:53248
	ds_read_b128 v[132:135], v14 offset:55296
	s_waitcnt lgkmcnt(14)
	v_mfma_f32_16x16x32_f16 v[56:59], v[152:155], v[168:171], v[56:59]
	s_waitcnt lgkmcnt(13)
	v_mfma_f32_16x16x32_f16 v[60:63], v[152:155], v[172:175], v[60:63]
	s_waitcnt lgkmcnt(12)
	v_mfma_f32_16x16x32_f16 v[64:67], v[152:155], v[176:179], v[64:67]
	s_waitcnt lgkmcnt(11)
	v_mfma_f32_16x16x32_f16 v[68:71], v[152:155], v[180:183], v[68:71]
	s_waitcnt lgkmcnt(10)
	v_mfma_f32_16x16x32_f16 v[72:75], v[156:159], v[168:171], v[72:75]
	v_mfma_f32_16x16x32_f16 v[76:79], v[156:159], v[172:175], v[76:79]
	v_mfma_f32_16x16x32_f16 v[80:83], v[156:159], v[176:179], v[80:83]
	v_mfma_f32_16x16x32_f16 v[84:87], v[156:159], v[180:183], v[84:87]
	s_waitcnt lgkmcnt(9)
	v_mfma_f32_16x16x32_f16 v[88:91], v[160:163], v[168:171], v[88:91]
	v_mfma_f32_16x16x32_f16 v[92:95], v[160:163], v[172:175], v[92:95]
	v_mfma_f32_16x16x32_f16 v[96:99], v[160:163], v[176:179], v[96:99]
	v_mfma_f32_16x16x32_f16 v[100:103], v[160:163], v[180:183], v[100:103]
	s_waitcnt lgkmcnt(8)
	v_mfma_f32_16x16x32_f16 v[104:107], v[164:167], v[168:171], v[104:107]
	v_mfma_f32_16x16x32_f16 v[108:111], v[164:167], v[172:175], v[108:111]
	v_mfma_f32_16x16x32_f16 v[112:115], v[164:167], v[176:179], v[112:115]
	v_mfma_f32_16x16x32_f16 v[116:119], v[164:167], v[180:183], v[116:119]
	s_waitcnt lgkmcnt(7)
	ds_read_b128 v[152:155], v15 offset:49152
	ds_read_b128 v[168:171], v17 offset:49152
	ds_read_b128 v[172:175], v17 offset:51200
	ds_read_b128 v[176:179], v17 offset:53248
	ds_read_b128 v[180:183], v17 offset:55296
	ds_read_b128 v[156:159], v15 offset:51200
	ds_read_b128 v[160:163], v15 offset:53248
	ds_read_b128 v[164:167], v15 offset:55296
	s_waitcnt lgkmcnt(14)
	v_mfma_f32_16x16x32_f16 v[56:59], v[120:123], v[136:139], v[56:59]
	s_waitcnt lgkmcnt(13)
	v_mfma_f32_16x16x32_f16 v[60:63], v[120:123], v[140:143], v[60:63]
	s_waitcnt lgkmcnt(12)
	v_mfma_f32_16x16x32_f16 v[64:67], v[120:123], v[144:147], v[64:67]
	s_waitcnt lgkmcnt(11)
	v_mfma_f32_16x16x32_f16 v[68:71], v[120:123], v[148:151], v[68:71]
	s_waitcnt lgkmcnt(10)
	v_mfma_f32_16x16x32_f16 v[72:75], v[124:127], v[136:139], v[72:75]
	v_mfma_f32_16x16x32_f16 v[76:79], v[124:127], v[140:143], v[76:79]
	v_mfma_f32_16x16x32_f16 v[80:83], v[124:127], v[144:147], v[80:83]
	v_mfma_f32_16x16x32_f16 v[84:87], v[124:127], v[148:151], v[84:87]
	s_waitcnt lgkmcnt(9)
	v_mfma_f32_16x16x32_f16 v[88:91], v[128:131], v[136:139], v[88:91]
	v_mfma_f32_16x16x32_f16 v[92:95], v[128:131], v[140:143], v[92:95]
	v_mfma_f32_16x16x32_f16 v[96:99], v[128:131], v[144:147], v[96:99]
	v_mfma_f32_16x16x32_f16 v[100:103], v[128:131], v[148:151], v[100:103]
	s_waitcnt lgkmcnt(8)
	v_mfma_f32_16x16x32_f16 v[104:107], v[132:135], v[136:139], v[104:107]
	v_mfma_f32_16x16x32_f16 v[108:111], v[132:135], v[140:143], v[108:111]
	v_mfma_f32_16x16x32_f16 v[112:115], v[132:135], v[144:147], v[112:115]
	v_mfma_f32_16x16x32_f16 v[116:119], v[132:135], v[148:151], v[116:119]
	s_waitcnt vmcnt(6) lgkmcnt(0)
	s_barrier
	s_add_u32 m0, s28, 0xc000
	s_nop 0
	global_load_lds_dwordx4 v10, s[4:5]
	s_add_u32 m0, s28, 0xe000
	s_nop 0
	global_load_lds_dwordx4 v11, s[4:5]
	s_add_u32 m0, s28, 0x10000
	s_nop 0
	global_load_lds_dwordx4 v12, s[4:5]
	s_add_u32 m0, s28, 0x12000
	s_nop 0
	global_load_lds_dwordx4 v13, s[4:5]
	s_add_u32 m0, s28, 0x14000
	s_nop 0
	global_load_lds_dwordx4 v10, s[6:7]
	s_add_u32 m0, s28, 0x16000
	s_nop 0
	global_load_lds_dwordx4 v11, s[6:7]
	s_add_u32 s4, s4, s20
	s_addc_u32 s5, s5, 0
	s_add_u32 s6, s6, s20
	s_addc_u32 s7, s7, 0
	s_waitcnt lgkmcnt(7)
	ds_read_b128 v[120:123], v18
	ds_read_b128 v[136:139], v20
	ds_read_b128 v[140:143], v20 offset:2048
	ds_read_b128 v[144:147], v20 offset:4096
	ds_read_b128 v[148:151], v20 offset:6144
	ds_read_b128 v[124:127], v18 offset:2048
	ds_read_b128 v[128:131], v18 offset:4096
	ds_read_b128 v[132:135], v18 offset:6144
	s_waitcnt lgkmcnt(14)
	v_mfma_f32_16x16x32_f16 v[56:59], v[152:155], v[168:171], v[56:59]
	s_waitcnt lgkmcnt(13)
	v_mfma_f32_16x16x32_f16 v[60:63], v[152:155], v[172:175], v[60:63]
	s_waitcnt lgkmcnt(12)
	v_mfma_f32_16x16x32_f16 v[64:67], v[152:155], v[176:179], v[64:67]
	s_waitcnt lgkmcnt(11)
	v_mfma_f32_16x16x32_f16 v[68:71], v[152:155], v[180:183], v[68:71]
	s_waitcnt lgkmcnt(10)
	v_mfma_f32_16x16x32_f16 v[72:75], v[156:159], v[168:171], v[72:75]
	v_mfma_f32_16x16x32_f16 v[76:79], v[156:159], v[172:175], v[76:79]
	v_mfma_f32_16x16x32_f16 v[80:83], v[156:159], v[176:179], v[80:83]
	v_mfma_f32_16x16x32_f16 v[84:87], v[156:159], v[180:183], v[84:87]
	s_waitcnt lgkmcnt(9)
	v_mfma_f32_16x16x32_f16 v[88:91], v[160:163], v[168:171], v[88:91]
	v_mfma_f32_16x16x32_f16 v[92:95], v[160:163], v[172:175], v[92:95]
	v_mfma_f32_16x16x32_f16 v[96:99], v[160:163], v[176:179], v[96:99]
	v_mfma_f32_16x16x32_f16 v[100:103], v[160:163], v[180:183], v[100:103]
	s_waitcnt lgkmcnt(8)
	v_mfma_f32_16x16x32_f16 v[104:107], v[164:167], v[168:171], v[104:107]
	v_mfma_f32_16x16x32_f16 v[108:111], v[164:167], v[172:175], v[108:111]
	v_mfma_f32_16x16x32_f16 v[112:115], v[164:167], v[176:179], v[112:115]
	v_mfma_f32_16x16x32_f16 v[116:119], v[164:167], v[180:183], v[116:119]
	s_waitcnt lgkmcnt(7)
	ds_read_b128 v[152:155], v19
	ds_read_b128 v[168:171], v21
	ds_read_b128 v[172:175], v21 offset:2048
	ds_read_b128 v[176:179], v21 offset:4096
	ds_read_b128 v[180:183], v21 offset:6144
	ds_read_b128 v[156:159], v19 offset:2048
	ds_read_b128 v[160:163], v19 offset:4096
	ds_read_b128 v[164:167], v19 offset:6144
	s_waitcnt lgkmcnt(14)
	v_mfma_f32_16x16x32_f16 v[56:59], v[120:123], v[136:139], v[56:59]
	s_waitcnt lgkmcnt(13)
	v_mfma_f32_16x16x32_f16 v[60:63], v[120:123], v[140:143], v[60:63]
	s_waitcnt lgkmcnt(12)
	v_mfma_f32_16x16x32_f16 v[64:67], v[120:123], v[144:147], v[64:67]
	s_waitcnt lgkmcnt(11)
	v_mfma_f32_16x16x32_f16 v[68:71], v[120:123], v[148:151], v[68:71]
	s_waitcnt lgkmcnt(10)
	v_mfma_f32_16x16x32_f16 v[72:75], v[124:127], v[136:139], v[72:75]
	v_mfma_f32_16x16x32_f16 v[76:79], v[124:127], v[140:143], v[76:79]
	v_mfma_f32_16x16x32_f16 v[80:83], v[124:127], v[144:147], v[80:83]
	v_mfma_f32_16x16x32_f16 v[84:87], v[124:127], v[148:151], v[84:87]
	s_waitcnt lgkmcnt(9)
	v_mfma_f32_16x16x32_f16 v[88:91], v[128:131], v[136:139], v[88:91]
	v_mfma_f32_16x16x32_f16 v[92:95], v[128:131], v[140:143], v[92:95]
	v_mfma_f32_16x16x32_f16 v[96:99], v[128:131], v[144:147], v[96:99]
	v_mfma_f32_16x16x32_f16 v[100:103], v[128:131], v[148:151], v[100:103]
	s_waitcnt lgkmcnt(8)
	v_mfma_f32_16x16x32_f16 v[104:107], v[132:135], v[136:139], v[104:107]
	v_mfma_f32_16x16x32_f16 v[108:111], v[132:135], v[140:143], v[108:111]
	v_mfma_f32_16x16x32_f16 v[112:115], v[132:135], v[144:147], v[112:115]
	v_mfma_f32_16x16x32_f16 v[116:119], v[132:135], v[148:151], v[116:119]
	s_waitcnt vmcnt(6) lgkmcnt(0)
	s_barrier
	s_add_u32 m0, s28, 0x18000
	s_nop 0
	global_load_lds_dwordx4 v10, s[4:5]
	s_add_u32 m0, s28, 0x1a000
	s_nop 0
	global_load_lds_dwordx4 v11, s[4:5]
	s_add_u32 m0, s28, 0x1c000
	s_nop 0
	global_load_lds_dwordx4 v12, s[4:5]
	s_add_u32 m0, s28, 0x1e000
	s_nop 0
	global_load_lds_dwordx4 v13, s[4:5]
	s_add_u32 m0, s28, 0x20000
	s_nop 0
	global_load_lds_dwordx4 v10, s[6:7]
	s_add_u32 m0, s28, 0x22000
	s_nop 0
	global_load_lds_dwordx4 v11, s[6:7]
	s_add_u32 s4, s4, s20
	s_addc_u32 s5, s5, 0
	s_add_u32 s6, s6, s20
	s_addc_u32 s7, s7, 0
	s_waitcnt lgkmcnt(7)
	ds_read_b128 v[120:123], v14
	ds_read_b128 v[136:139], v16
	ds_read_b128 v[140:143], v16 offset:2048
	ds_read_b128 v[144:147], v16 offset:4096
	ds_read_b128 v[148:151], v16 offset:6144
	ds_read_b128 v[124:127], v14 offset:2048
	ds_read_b128 v[128:131], v14 offset:4096
	ds_read_b128 v[132:135], v14 offset:6144
	s_waitcnt lgkmcnt(14)
	v_mfma_f32_16x16x32_f16 v[56:59], v[152:155], v[168:171], v[56:59]
	s_waitcnt lgkmcnt(13)
	v_mfma_f32_16x16x32_f16 v[60:63], v[152:155], v[172:175], v[60:63]
	s_waitcnt lgkmcnt(12)
	v_mfma_f32_16x16x32_f16 v[64:67], v[152:155], v[176:179], v[64:67]
	s_waitcnt lgkmcnt(11)
	v_mfma_f32_16x16x32_f16 v[68:71], v[152:155], v[180:183], v[68:71]
	s_waitcnt lgkmcnt(10)
	v_mfma_f32_16x16x32_f16 v[72:75], v[156:159], v[168:171], v[72:75]
	v_mfma_f32_16x16x32_f16 v[76:79], v[156:159], v[172:175], v[76:79]
	v_mfma_f32_16x16x32_f16 v[80:83], v[156:159], v[176:179], v[80:83]
	v_mfma_f32_16x16x32_f16 v[84:87], v[156:159], v[180:183], v[84:87]
	s_waitcnt lgkmcnt(9)
	v_mfma_f32_16x16x32_f16 v[88:91], v[160:163], v[168:171], v[88:91]
	v_mfma_f32_16x16x32_f16 v[92:95], v[160:163], v[172:175], v[92:95]
	v_mfma_f32_16x16x32_f16 v[96:99], v[160:163], v[176:179], v[96:99]
	v_mfma_f32_16x16x32_f16 v[100:103], v[160:163], v[180:183], v[100:103]
	s_waitcnt lgkmcnt(8)
	v_mfma_f32_16x16x32_f16 v[104:107], v[164:167], v[168:171], v[104:107]
	v_mfma_f32_16x16x32_f16 v[108:111], v[164:167], v[172:175], v[108:111]
	v_mfma_f32_16x16x32_f16 v[112:115], v[164:167], v[176:179], v[112:115]
	v_mfma_f32_16x16x32_f16 v[116:119], v[164:167], v[180:183], v[116:119]
	s_waitcnt lgkmcnt(7)
	ds_read_b128 v[152:155], v15
	ds_read_b128 v[168:171], v17
	ds_read_b128 v[172:175], v17 offset:2048
	ds_read_b128 v[176:179], v17 offset:4096
	ds_read_b128 v[180:183], v17 offset:6144
	ds_read_b128 v[156:159], v15 offset:2048
	ds_read_b128 v[160:163], v15 offset:4096
	ds_read_b128 v[164:167], v15 offset:6144
	s_waitcnt lgkmcnt(14)
	v_mfma_f32_16x16x32_f16 v[56:59], v[120:123], v[136:139], v[56:59]
	s_waitcnt lgkmcnt(13)
	v_mfma_f32_16x16x32_f16 v[60:63], v[120:123], v[140:143], v[60:63]
	s_waitcnt lgkmcnt(12)
	v_mfma_f32_16x16x32_f16 v[64:67], v[120:123], v[144:147], v[64:67]
	s_waitcnt lgkmcnt(11)
	v_mfma_f32_16x16x32_f16 v[68:71], v[120:123], v[148:151], v[68:71]
	s_waitcnt lgkmcnt(10)
	v_mfma_f32_16x16x32_f16 v[72:75], v[124:127], v[136:139], v[72:75]
	v_mfma_f32_16x16x32_f16 v[76:79], v[124:127], v[140:143], v[76:79]
	v_mfma_f32_16x16x32_f16 v[80:83], v[124:127], v[144:147], v[80:83]
	v_mfma_f32_16x16x32_f16 v[84:87], v[124:127], v[148:151], v[84:87]
	s_waitcnt lgkmcnt(9)
	v_mfma_f32_16x16x32_f16 v[88:91], v[128:131], v[136:139], v[88:91]
	v_mfma_f32_16x16x32_f16 v[92:95], v[128:131], v[140:143], v[92:95]
	v_mfma_f32_16x16x32_f16 v[96:99], v[128:131], v[144:147], v[96:99]
	v_mfma_f32_16x16x32_f16 v[100:103], v[128:131], v[148:151], v[100:103]
	s_waitcnt lgkmcnt(8)
	v_mfma_f32_16x16x32_f16 v[104:107], v[132:135], v[136:139], v[104:107]
	v_mfma_f32_16x16x32_f16 v[108:111], v[132:135], v[140:143], v[108:111]
	v_mfma_f32_16x16x32_f16 v[112:115], v[132:135], v[144:147], v[112:115]
	v_mfma_f32_16x16x32_f16 v[116:119], v[132:135], v[148:151], v[116:119]
	s_waitcnt vmcnt(6) lgkmcnt(0)
	s_barrier
	s_add_u32 m0, s28, 0x0
	s_nop 0
	global_load_lds_dwordx4 v10, s[4:5]
	s_add_u32 m0, s28, 0x2000
	s_nop 0
	global_load_lds_dwordx4 v11, s[4:5]
	s_add_u32 m0, s28, 0x4000
	s_nop 0
	global_load_lds_dwordx4 v12, s[4:5]
	s_add_u32 m0, s28, 0x6000
	s_nop 0
	global_load_lds_dwordx4 v13, s[4:5]
	s_add_u32 m0, s28, 0x8000
	s_nop 0
	global_load_lds_dwordx4 v10, s[6:7]
	s_add_u32 m0, s28, 0xa000
	s_nop 0
	global_load_lds_dwordx4 v11, s[6:7]
	s_add_u32 s4, s4, s20
	s_addc_u32 s5, s5, 0
	s_add_u32 s6, s6, s20
	s_addc_u32 s7, s7, 0
	s_waitcnt lgkmcnt(7)
	ds_read_b128 v[120:123], v14 offset:49152
	ds_read_b128 v[136:139], v16 offset:49152
	ds_read_b128 v[140:143], v16 offset:51200
	ds_read_b128 v[144:147], v16 offset:53248
	ds_read_b128 v[148:151], v16 offset:55296
	ds_read_b128 v[124:127], v14 offset:51200
	ds_read_b128 v[128:131], v14 offset:53248
	ds_read_b128 v[132:135], v14 offset:55296
	s_waitcnt lgkmcnt(14)
	v_mfma_f32_16x16x32_f16 v[56:59], v[152:155], v[168:171], v[56:59]
	s_waitcnt lgkmcnt(13)
	v_mfma_f32_16x16x32_f16 v[60:63], v[152:155], v[172:175], v[60:63]
	s_waitcnt lgkmcnt(12)
	v_mfma_f32_16x16x32_f16 v[64:67], v[152:155], v[176:179], v[64:67]
	s_waitcnt lgkmcnt(11)
	v_mfma_f32_16x16x32_f16 v[68:71], v[152:155], v[180:183], v[68:71]
	s_waitcnt lgkmcnt(10)
	v_mfma_f32_16x16x32_f16 v[72:75], v[156:159], v[168:171], v[72:75]
	v_mfma_f32_16x16x32_f16 v[76:79], v[156:159], v[172:175], v[76:79]
	v_mfma_f32_16x16x32_f16 v[80:83], v[156:159], v[176:179], v[80:83]
	v_mfma_f32_16x16x32_f16 v[84:87], v[156:159], v[180:183], v[84:87]
	s_waitcnt lgkmcnt(9)
	v_mfma_f32_16x16x32_f16 v[88:91], v[160:163], v[168:171], v[88:91]
	v_mfma_f32_16x16x32_f16 v[92:95], v[160:163], v[172:175], v[92:95]
	v_mfma_f32_16x16x32_f16 v[96:99], v[160:163], v[176:179], v[96:99]
	v_mfma_f32_16x16x32_f16 v[100:103], v[160:163], v[180:183], v[100:103]
	s_waitcnt lgkmcnt(8)
	v_mfma_f32_16x16x32_f16 v[104:107], v[164:167], v[168:171], v[104:107]
	v_mfma_f32_16x16x32_f16 v[108:111], v[164:167], v[172:175], v[108:111]
	v_mfma_f32_16x16x32_f16 v[112:115], v[164:167], v[176:179], v[112:115]
	v_mfma_f32_16x16x32_f16 v[116:119], v[164:167], v[180:183], v[116:119]
	s_waitcnt lgkmcnt(7)
	ds_read_b128 v[152:155], v15 offset:49152
	ds_read_b128 v[168:171], v17 offset:49152
	ds_read_b128 v[172:175], v17 offset:51200
	ds_read_b128 v[176:179], v17 offset:53248
	ds_read_b128 v[180:183], v17 offset:55296
	ds_read_b128 v[156:159], v15 offset:51200
	ds_read_b128 v[160:163], v15 offset:53248
	ds_read_b128 v[164:167], v15 offset:55296
	s_waitcnt lgkmcnt(14)
	v_mfma_f32_16x16x32_f16 v[56:59], v[120:123], v[136:139], v[56:59]
	s_waitcnt lgkmcnt(13)
	v_mfma_f32_16x16x32_f16 v[60:63], v[120:123], v[140:143], v[60:63]
	s_waitcnt lgkmcnt(12)
	v_mfma_f32_16x16x32_f16 v[64:67], v[120:123], v[144:147], v[64:67]
	s_waitcnt lgkmcnt(11)
	v_mfma_f32_16x16x32_f16 v[68:71], v[120:123], v[148:151], v[68:71]
	s_waitcnt lgkmcnt(10)
	v_mfma_f32_16x16x32_f16 v[72:75], v[124:127], v[136:139], v[72:75]
	v_mfma_f32_16x16x32_f16 v[76:79], v[124:127], v[140:143], v[76:79]
	v_mfma_f32_16x16x32_f16 v[80:83], v[124:127], v[144:147], v[80:83]
	v_mfma_f32_16x16x32_f16 v[84:87], v[124:127], v[148:151], v[84:87]
	s_waitcnt lgkmcnt(9)
	v_mfma_f32_16x16x32_f16 v[88:91], v[128:131], v[136:139], v[88:91]
	v_mfma_f32_16x16x32_f16 v[92:95], v[128:131], v[140:143], v[92:95]
	v_mfma_f32_16x16x32_f16 v[96:99], v[128:131], v[144:147], v[96:99]
	v_mfma_f32_16x16x32_f16 v[100:103], v[128:131], v[148:151], v[100:103]
	s_waitcnt lgkmcnt(8)
	v_mfma_f32_16x16x32_f16 v[104:107], v[132:135], v[136:139], v[104:107]
	v_mfma_f32_16x16x32_f16 v[108:111], v[132:135], v[140:143], v[108:111]
	v_mfma_f32_16x16x32_f16 v[112:115], v[132:135], v[144:147], v[112:115]
	v_mfma_f32_16x16x32_f16 v[116:119], v[132:135], v[148:151], v[116:119]
	s_waitcnt vmcnt(6) lgkmcnt(0)
	s_barrier
	s_waitcnt lgkmcnt(7)
	ds_read_b128 v[120:123], v18
	ds_read_b128 v[136:139], v20
	ds_read_b128 v[140:143], v20 offset:2048
	ds_read_b128 v[144:147], v20 offset:4096
	ds_read_b128 v[148:151], v20 offset:6144
	ds_read_b128 v[124:127], v18 offset:2048
	ds_read_b128 v[128:131], v18 offset:4096
	ds_read_b128 v[132:135], v18 offset:6144
	s_waitcnt lgkmcnt(14)
	v_mfma_f32_16x16x32_f16 v[56:59], v[152:155], v[168:171], v[56:59]
	s_waitcnt lgkmcnt(13)
	v_mfma_f32_16x16x32_f16 v[60:63], v[152:155], v[172:175], v[60:63]
	s_waitcnt lgkmcnt(12)
	v_mfma_f32_16x16x32_f16 v[64:67], v[152:155], v[176:179], v[64:67]
	s_waitcnt lgkmcnt(11)
	v_mfma_f32_16x16x32_f16 v[68:71], v[152:155], v[180:183], v[68:71]
	s_waitcnt lgkmcnt(10)
	v_mfma_f32_16x16x32_f16 v[72:75], v[156:159], v[168:171], v[72:75]
	v_mfma_f32_16x16x32_f16 v[76:79], v[156:159], v[172:175], v[76:79]
	v_mfma_f32_16x16x32_f16 v[80:83], v[156:159], v[176:179], v[80:83]
	v_mfma_f32_16x16x32_f16 v[84:87], v[156:159], v[180:183], v[84:87]
	s_waitcnt lgkmcnt(9)
	v_mfma_f32_16x16x32_f16 v[88:91], v[160:163], v[168:171], v[88:91]
	v_mfma_f32_16x16x32_f16 v[92:95], v[160:163], v[172:175], v[92:95]
	v_mfma_f32_16x16x32_f16 v[96:99], v[160:163], v[176:179], v[96:99]
	v_mfma_f32_16x16x32_f16 v[100:103], v[160:163], v[180:183], v[100:103]
	s_waitcnt lgkmcnt(8)
	v_mfma_f32_16x16x32_f16 v[104:107], v[164:167], v[168:171], v[104:107]
	v_mfma_f32_16x16x32_f16 v[108:111], v[164:167], v[172:175], v[108:111]
	v_mfma_f32_16x16x32_f16 v[112:115], v[164:167], v[176:179], v[112:115]
	v_mfma_f32_16x16x32_f16 v[116:119], v[164:167], v[180:183], v[116:119]
	s_waitcnt lgkmcnt(7)
	ds_read_b128 v[152:155], v19
	ds_read_b128 v[168:171], v21
	ds_read_b128 v[172:175], v21 offset:2048
	ds_read_b128 v[176:179], v21 offset:4096
	ds_read_b128 v[180:183], v21 offset:6144
	ds_read_b128 v[156:159], v19 offset:2048
	ds_read_b128 v[160:163], v19 offset:4096
	ds_read_b128 v[164:167], v19 offset:6144
	s_waitcnt lgkmcnt(14)
	v_mfma_f32_16x16x32_f16 v[56:59], v[120:123], v[136:139], v[56:59]
	s_waitcnt lgkmcnt(13)
	v_mfma_f32_16x16x32_f16 v[60:63], v[120:123], v[140:143], v[60:63]
	s_waitcnt lgkmcnt(12)
	v_mfma_f32_16x16x32_f16 v[64:67], v[120:123], v[144:147], v[64:67]
	s_waitcnt lgkmcnt(11)
	v_mfma_f32_16x16x32_f16 v[68:71], v[120:123], v[148:151], v[68:71]
	s_waitcnt lgkmcnt(10)
	v_mfma_f32_16x16x32_f16 v[72:75], v[124:127], v[136:139], v[72:75]
	v_mfma_f32_16x16x32_f16 v[76:79], v[124:127], v[140:143], v[76:79]
	v_mfma_f32_16x16x32_f16 v[80:83], v[124:127], v[144:147], v[80:83]
	v_mfma_f32_16x16x32_f16 v[84:87], v[124:127], v[148:151], v[84:87]
	s_waitcnt lgkmcnt(9)
	v_mfma_f32_16x16x32_f16 v[88:91], v[128:131], v[136:139], v[88:91]
	v_mfma_f32_16x16x32_f16 v[92:95], v[128:131], v[140:143], v[92:95]
	v_mfma_f32_16x16x32_f16 v[96:99], v[128:131], v[144:147], v[96:99]
	v_mfma_f32_16x16x32_f16 v[100:103], v[128:131], v[148:151], v[100:103]
	s_waitcnt lgkmcnt(8)
	v_mfma_f32_16x16x32_f16 v[104:107], v[132:135], v[136:139], v[104:107]
	v_mfma_f32_16x16x32_f16 v[108:111], v[132:135], v[140:143], v[108:111]
	v_mfma_f32_16x16x32_f16 v[112:115], v[132:135], v[144:147], v[112:115]
	v_mfma_f32_16x16x32_f16 v[116:119], v[132:135], v[148:151], v[116:119]
	s_waitcnt vmcnt(0) lgkmcnt(0)
	s_barrier
	s_waitcnt lgkmcnt(7)
	ds_read_b128 v[120:123], v14
	ds_read_b128 v[136:139], v16
	ds_read_b128 v[140:143], v16 offset:2048
	ds_read_b128 v[144:147], v16 offset:4096
	ds_read_b128 v[148:151], v16 offset:6144
	ds_read_b128 v[124:127], v14 offset:2048
	ds_read_b128 v[128:131], v14 offset:4096
	ds_read_b128 v[132:135], v14 offset:6144
	s_waitcnt lgkmcnt(14)
	v_mfma_f32_16x16x32_f16 v[56:59], v[152:155], v[168:171], v[56:59]
	s_waitcnt lgkmcnt(13)
	v_mfma_f32_16x16x32_f16 v[60:63], v[152:155], v[172:175], v[60:63]
	s_waitcnt lgkmcnt(12)
	v_mfma_f32_16x16x32_f16 v[64:67], v[152:155], v[176:179], v[64:67]
	s_waitcnt lgkmcnt(11)
	v_mfma_f32_16x16x32_f16 v[68:71], v[152:155], v[180:183], v[68:71]
	s_waitcnt lgkmcnt(10)
	v_mfma_f32_16x16x32_f16 v[72:75], v[156:159], v[168:171], v[72:75]
	v_mfma_f32_16x16x32_f16 v[76:79], v[156:159], v[172:175], v[76:79]
	v_mfma_f32_16x16x32_f16 v[80:83], v[156:159], v[176:179], v[80:83]
	v_mfma_f32_16x16x32_f16 v[84:87], v[156:159], v[180:183], v[84:87]
	s_waitcnt lgkmcnt(9)
	v_mfma_f32_16x16x32_f16 v[88:91], v[160:163], v[168:171], v[88:91]
	v_mfma_f32_16x16x32_f16 v[92:95], v[160:163], v[172:175], v[92:95]
	v_mfma_f32_16x16x32_f16 v[96:99], v[160:163], v[176:179], v[96:99]
	v_mfma_f32_16x16x32_f16 v[100:103], v[160:163], v[180:183], v[100:103]
	s_waitcnt lgkmcnt(8)
	v_mfma_f32_16x16x32_f16 v[104:107], v[164:167], v[168:171], v[104:107]
	v_mfma_f32_16x16x32_f16 v[108:111], v[164:167], v[172:175], v[108:111]
	v_mfma_f32_16x16x32_f16 v[112:115], v[164:167], v[176:179], v[112:115]
	v_mfma_f32_16x16x32_f16 v[116:119], v[164:167], v[180:183], v[116:119]
	s_waitcnt lgkmcnt(7)
	ds_read_b128 v[152:155], v15
	ds_read_b128 v[168:171], v17
	ds_read_b128 v[172:175], v17 offset:2048
	ds_read_b128 v[176:179], v17 offset:4096
	ds_read_b128 v[180:183], v17 offset:6144
	ds_read_b128 v[156:159], v15 offset:2048
	ds_read_b128 v[160:163], v15 offset:4096
	ds_read_b128 v[164:167], v15 offset:6144
	s_waitcnt lgkmcnt(14)
	v_mfma_f32_16x16x32_f16 v[56:59], v[120:123], v[136:139], v[56:59]
	s_waitcnt lgkmcnt(13)
	v_mfma_f32_16x16x32_f16 v[60:63], v[120:123], v[140:143], v[60:63]
	s_waitcnt lgkmcnt(12)
	v_mfma_f32_16x16x32_f16 v[64:67], v[120:123], v[144:147], v[64:67]
	s_waitcnt lgkmcnt(11)
	v_mfma_f32_16x16x32_f16 v[68:71], v[120:123], v[148:151], v[68:71]
	s_waitcnt lgkmcnt(10)
	v_mfma_f32_16x16x32_f16 v[72:75], v[124:127], v[136:139], v[72:75]
	v_mfma_f32_16x16x32_f16 v[76:79], v[124:127], v[140:143], v[76:79]
	v_mfma_f32_16x16x32_f16 v[80:83], v[124:127], v[144:147], v[80:83]
	v_mfma_f32_16x16x32_f16 v[84:87], v[124:127], v[148:151], v[84:87]
	s_waitcnt lgkmcnt(9)
	v_mfma_f32_16x16x32_f16 v[88:91], v[128:131], v[136:139], v[88:91]
	v_mfma_f32_16x16x32_f16 v[92:95], v[128:131], v[140:143], v[92:95]
	v_mfma_f32_16x16x32_f16 v[96:99], v[128:131], v[144:147], v[96:99]
	v_mfma_f32_16x16x32_f16 v[100:103], v[128:131], v[148:151], v[100:103]
	s_waitcnt lgkmcnt(8)
	v_mfma_f32_16x16x32_f16 v[104:107], v[132:135], v[136:139], v[104:107]
	v_mfma_f32_16x16x32_f16 v[108:111], v[132:135], v[140:143], v[108:111]
	v_mfma_f32_16x16x32_f16 v[112:115], v[132:135], v[144:147], v[112:115]
	v_mfma_f32_16x16x32_f16 v[116:119], v[132:135], v[148:151], v[116:119]
	s_waitcnt lgkmcnt(6)
	v_mfma_f32_16x16x32_f16 v[56:59], v[152:155], v[168:171], v[56:59]
	s_waitcnt lgkmcnt(5)
	v_mfma_f32_16x16x32_f16 v[60:63], v[152:155], v[172:175], v[60:63]
	s_waitcnt lgkmcnt(4)
	v_mfma_f32_16x16x32_f16 v[64:67], v[152:155], v[176:179], v[64:67]
	s_waitcnt lgkmcnt(3)
	v_mfma_f32_16x16x32_f16 v[68:71], v[152:155], v[180:183], v[68:71]
	s_waitcnt lgkmcnt(2)
	v_mfma_f32_16x16x32_f16 v[72:75], v[156:159], v[168:171], v[72:75]
	v_mfma_f32_16x16x32_f16 v[76:79], v[156:159], v[172:175], v[76:79]
	v_mfma_f32_16x16x32_f16 v[80:83], v[156:159], v[176:179], v[80:83]
	v_mfma_f32_16x16x32_f16 v[84:87], v[156:159], v[180:183], v[84:87]
	s_waitcnt lgkmcnt(1)
	v_mfma_f32_16x16x32_f16 v[88:91], v[160:163], v[168:171], v[88:91]
	v_mfma_f32_16x16x32_f16 v[92:95], v[160:163], v[172:175], v[92:95]
	v_mfma_f32_16x16x32_f16 v[96:99], v[160:163], v[176:179], v[96:99]
	v_mfma_f32_16x16x32_f16 v[100:103], v[160:163], v[180:183], v[100:103]
	s_waitcnt lgkmcnt(0)
	v_mfma_f32_16x16x32_f16 v[104:107], v[164:167], v[168:171], v[104:107]
	v_mfma_f32_16x16x32_f16 v[108:111], v[164:167], v[172:175], v[108:111]
	v_mfma_f32_16x16x32_f16 v[112:115], v[164:167], v[176:179], v[112:115]
	v_mfma_f32_16x16x32_f16 v[116:119], v[164:167], v[180:183], v[116:119]
	s_nop 7
	s_nop 1
	v_add_f32_e32 v56, v56, v24
	v_add_f32_e32 v57, v57, v24
	v_add_f32_e32 v58, v58, v24
	v_add_f32_e32 v59, v59, v24
	v_cvt_pk_f16_f32 v56, v56, v57
	v_cvt_pk_f16_f32 v57, v58, v59
	global_store_dwordx2 v22, v[56:57], s[22:23] offset:0
	v_add_f32_e32 v60, v60, v25
	v_add_f32_e32 v61, v61, v25
	v_add_f32_e32 v62, v62, v25
	v_add_f32_e32 v63, v63, v25
	v_cvt_pk_f16_f32 v60, v60, v61
	v_cvt_pk_f16_f32 v61, v62, v63
	global_store_dwordx2 v22, v[60:61], s[22:23] offset:256
	v_add_f32_e32 v64, v64, v26
	v_add_f32_e32 v65, v65, v26
	v_add_f32_e32 v66, v66, v26
	v_add_f32_e32 v67, v67, v26
	v_cvt_pk_f16_f32 v64, v64, v65
	v_cvt_pk_f16_f32 v65, v66, v67
	global_store_dwordx2 v22, v[64:65], s[22:23] offset:1024
	v_add_f32_e32 v68, v68, v27
	v_add_f32_e32 v69, v69, v27
	v_add_f32_e32 v70, v70, v27
	v_add_f32_e32 v71, v71, v27
	v_cvt_pk_f16_f32 v68, v68, v69
	v_cvt_pk_f16_f32 v69, v70, v71
	global_store_dwordx2 v22, v[68:69], s[22:23] offset:1280
	v_add_f32_e32 v72, v72, v24
	v_add_f32_e32 v73, v73, v24
	v_add_f32_e32 v74, v74, v24
	v_add_f32_e32 v75, v75, v24
	v_cvt_pk_f16_f32 v72, v72, v73
	v_cvt_pk_f16_f32 v73, v74, v75
	global_store_dwordx2 v22, v[72:73], s[22:23] offset:2048
	v_add_f32_e32 v76, v76, v25
	v_add_f32_e32 v77, v77, v25
	v_add_f32_e32 v78, v78, v25
	v_add_f32_e32 v79, v79, v25
	v_cvt_pk_f16_f32 v76, v76, v77
	v_cvt_pk_f16_f32 v77, v78, v79
	global_store_dwordx2 v22, v[76:77], s[22:23] offset:2304
	v_add_f32_e32 v80, v80, v26
	v_add_f32_e32 v81, v81, v26
	v_add_f32_e32 v82, v82, v26
	v_add_f32_e32 v83, v83, v26
	v_cvt_pk_f16_f32 v80, v80, v81
	v_cvt_pk_f16_f32 v81, v82, v83
	global_store_dwordx2 v22, v[80:81], s[22:23] offset:3072
	v_add_f32_e32 v84, v84, v27
	v_add_f32_e32 v85, v85, v27
	v_add_f32_e32 v86, v86, v27
	v_add_f32_e32 v87, v87, v27
	v_cvt_pk_f16_f32 v84, v84, v85
	v_cvt_pk_f16_f32 v85, v86, v87
	global_store_dwordx2 v22, v[84:85], s[22:23] offset:3328
	v_add_f32_e32 v88, v88, v24
	v_add_f32_e32 v89, v89, v24
	v_add_f32_e32 v90, v90, v24
	v_add_f32_e32 v91, v91, v24
	v_cvt_pk_f16_f32 v88, v88, v89
	v_cvt_pk_f16_f32 v89, v90, v91
	global_store_dwordx2 v23, v[88:89], s[22:23] offset:0
	v_add_f32_e32 v92, v92, v25
	v_add_f32_e32 v93, v93, v25
	v_add_f32_e32 v94, v94, v25
	v_add_f32_e32 v95, v95, v25
	v_cvt_pk_f16_f32 v92, v92, v93
	v_cvt_pk_f16_f32 v93, v94, v95
	global_store_dwordx2 v23, v[92:93], s[22:23] offset:256
	v_add_f32_e32 v96, v96, v26
	v_add_f32_e32 v97, v97, v26
	v_add_f32_e32 v98, v98, v26
	v_add_f32_e32 v99, v99, v26
	v_cvt_pk_f16_f32 v96, v96, v97
	v_cvt_pk_f16_f32 v97, v98, v99
	global_store_dwordx2 v23, v[96:97], s[22:23] offset:1024
	v_add_f32_e32 v100, v100, v27
	v_add_f32_e32 v101, v101, v27
	v_add_f32_e32 v102, v102, v27
	v_add_f32_e32 v103, v103, v27
	v_cvt_pk_f16_f32 v100, v100, v101
	v_cvt_pk_f16_f32 v101, v102, v103
	global_store_dwordx2 v23, v[100:101], s[22:23] offset:1280
	v_add_f32_e32 v104, v104, v24
	v_add_f32_e32 v105, v105, v24
	v_add_f32_e32 v106, v106, v24
	v_add_f32_e32 v107, v107, v24
	v_cvt_pk_f16_f32 v104, v104, v105
	v_cvt_pk_f16_f32 v105, v106, v107
	global_store_dwordx2 v23, v[104:105], s[22:23] offset:2048
	v_add_f32_e32 v108, v108, v25
	v_add_f32_e32 v109, v109, v25
	v_add_f32_e32 v110, v110, v25
	v_add_f32_e32 v111, v111, v25
	v_cvt_pk_f16_f32 v108, v108, v109
	v_cvt_pk_f16_f32 v109, v110, v111
	global_store_dwordx2 v23, v[108:109], s[22:23] offset:2304
	v_add_f32_e32 v112, v112, v26
	v_add_f32_e32 v113, v113, v26
	v_add_f32_e32 v114, v114, v26
	v_add_f32_e32 v115, v115, v26
	v_cvt_pk_f16_f32 v112, v112, v113
	v_cvt_pk_f16_f32 v113, v114, v115
	global_store_dwordx2 v23, v[112:113], s[22:23] offset:3072
	v_add_f32_e32 v116, v116, v27
	v_add_f32_e32 v117, v117, v27
	v_add_f32_e32 v118, v118, v27
	v_add_f32_e32 v119, v119, v27
	v_cvt_pk_f16_f32 v116, v116, v117
	v_cvt_pk_f16_f32 v117, v118, v119
	global_store_dwordx2 v23, v[116:117], s[22:23] offset:3328
	s_endpgm
.Lpf_old:
	s_load_dwordx4 s[16:19], s[0:1], 0x58
	s_load_dwordx8 s[8:15], s[0:1], 0x8
	s_load_dwordx2 s[6:7], s[0:1], 0x48
	s_load_dwordx4 s[20:23], s[0:1], 0x30
	v_and_b32_e32 v1, 63, v0
	v_lshrrev_b32_e32 v152, 6, v0
	s_cmpk_lt_i32 s2, 0x300
	s_mov_b64 s[4:5], -1
	s_cbranch_scc0 .LBB1_13
	s_ashr_i32 s3, s2, 3
	s_cmp_lt_i32 s3, 32
	s_cselect_b64 s[4:5], -1, 0
	s_cmp_gt_i32 s3, 31
	s_cbranch_scc0 .LBB1_5
	s_lshr_b32 s25, s3, 1
	s_and_b32 s24, s2, 2
	s_and_b32 s25, s25, 12
	s_cmp_gt_u32 s3, 63
	s_cselect_b32 s26, 16, 0
	s_and_b32 s29, s2, 1
	s_lshl_b32 s27, s29, 2
	s_waitcnt lgkmcnt(0)
	s_load_dword s30, s[14:15], s27 offset:0x0
	s_or_b32 s24, s26, s24
	s_or_b32 s33, s24, s25
	s_lshl_b32 s31, s33, 6
	s_mov_b64 s[26:27], 0
	s_waitcnt lgkmcnt(0)
	s_cmp_lt_i32 s31, s30
	s_mov_b64 s[24:25], 0
	s_cbranch_scc1 .LBB1_6
	s_bfe_u32 s30, s2, 0x10002
	s_and_b64 vcc, exec, s[26:27]
	s_cbranch_vccnz .LBB1_7

	.amdhsa_kernel _Z11proj_kernelPKDF16_S0_S0_S0_PKiPKfS4_S4_S4_S4_PDF16_S5_S5_
		.amdhsa_group_segment_fixed_size 16384
		.amdhsa_private_segment_fixed_size 0
		.amdhsa_kernarg_size 104
		.amdhsa_user_sgpr_count 2
		.amdhsa_user_sgpr_dispatch_ptr 0
		.amdhsa_user_sgpr_queue_ptr 0
		.amdhsa_user_sgpr_kernarg_segment_ptr 1
		.amdhsa_user_sgpr_dispatch_id 0
		.amdhsa_user_sgpr_kernarg_preload_length 0
		.amdhsa_user_sgpr_kernarg_preload_offset 0
		.amdhsa_user_sgpr_private_segment_size 0
		.amdhsa_uses_dynamic_stack 0
		.amdhsa_enable_private_segment 0
		.amdhsa_system_sgpr_workgroup_id_x 1
		.amdhsa_system_sgpr_workgroup_id_y 0
		.amdhsa_system_sgpr_workgroup_id_z 0
		.amdhsa_system_sgpr_workgroup_info 0
		.amdhsa_system_vgpr_workitem_id 0
		.amdhsa_next_free_vgpr 200
		.amdhsa_next_free_sgpr 56
		.amdhsa_accum_offset 200
		.amdhsa_reserve_vcc 1
		.amdhsa_float_round_mode_32 0
		.amdhsa_float_round_mode_16_64 0
		.amdhsa_float_denorm_mode_32 3
		.amdhsa_float_denorm_mode_16_64 3
		.amdhsa_dx10_clamp 1
		.amdhsa_ieee_mode 1
		.amdhsa_fp16_overflow 0
		.amdhsa_tg_split 0
		.amdhsa_exception_fp_ieee_invalid_op 0
		.amdhsa_exception_fp_denorm_src 0
		.amdhsa_exception_fp_ieee_div_zero 0
		.amdhsa_exception_fp_ieee_overflow 0
		.amdhsa_exception_fp_ieee_underflow 0
		.amdhsa_exception_fp_ieee_inexact 0
		.amdhsa_exception_int_div_zero 0
	.end_amdhsa_kernel

amdhsa.kernels:
  - .agpr_count:     0
    .args:
      - .actual_access:  read_only
        .address_space:  global
        .offset:         0
        .size:           8
        .value_kind:     global_buffer
      - .actual_access:  read_only
        .address_space:  global
        .offset:         8
        .size:           8
        .value_kind:     global_buffer
      - .actual_access:  read_only
        .address_space:  global
        .offset:         16
        .size:           8
        .value_kind:     global_buffer
      - .actual_access:  read_only
        .address_space:  global
        .offset:         24
        .size:           8
        .value_kind:     global_buffer
      - .actual_access:  read_only
        .address_space:  global
        .offset:         32
        .size:           8
        .value_kind:     global_buffer
      - .actual_access:  read_only
        .address_space:  global
        .offset:         40
        .size:           8
        .value_kind:     global_buffer
      - .actual_access:  read_only
        .address_space:  global
        .offset:         48
        .size:           8
        .value_kind:     global_buffer
      - .actual_access:  read_only
        .address_space:  global
        .offset:         56
        .size:           8
        .value_kind:     global_buffer
      - .actual_access:  write_only
        .address_space:  global
        .offset:         64
        .size:           8
        .value_kind:     global_buffer
      - .actual_access:  write_only
        .address_space:  global
        .offset:         72
        .size:           8
        .value_kind:     global_buffer
      - .actual_access:  write_only
        .address_space:  global
        .offset:         80
        .size:           8
        .value_kind:     global_buffer
      - .actual_access:  write_only
        .address_space:  global
        .offset:         88
        .size:           8
        .value_kind:     global_buffer
      - .actual_access:  write_only
        .address_space:  global
        .offset:         96
        .size:           8
        .value_kind:     global_buffer
    .group_segment_fixed_size: 80
    .kernarg_segment_align: 8
    .kernarg_segment_size: 104
    .language:       OpenCL C
    .language_version:
      - 2
      - 0
    .max_flat_workgroup_size: 256
    .name:           _Z11prep_kernelPKfS0_S0_PKiS0_S0_S0_S0_PDF16_S3_S3_S3_Pi
    .private_segment_fixed_size: 0
    .sgpr_count:     43
    .sgpr_spill_count: 0
    .symbol:         _Z11prep_kernelPKfS0_S0_PKiS0_S0_S0_S0_PDF16_S3_S3_S3_Pi.kd
    .uniform_work_group_size: 1
    .uses_dynamic_stack: false
    .vgpr_count:     64
    .vgpr_spill_count: 0
    .wavefront_size: 64
  - .agpr_count:     0
    .args:
      - .address_space:  global
        .offset:         0
        .size:           8
        .value_kind:     global_buffer
      - .address_space:  global
        .offset:         8
        .size:           8
        .value_kind:     global_buffer
      - .address_space:  global
        .offset:         16
        .size:           8
        .value_kind:     global_buffer
      - .address_space:  global
        .offset:         24
        .size:           8
        .value_kind:     global_buffer
      - .actual_access:  read_only
        .address_space:  global
        .offset:         32
        .size:           8
        .value_kind:     global_buffer
      - .actual_access:  read_only
        .address_space:  global
        .offset:         40
        .size:           8
        .value_kind:     global_buffer
      - .actual_access:  read_only
        .address_space:  global
        .offset:         48
        .size:           8
        .value_kind:     global_buffer
      - .actual_access:  read_only
        .address_space:  global
        .offset:         56
        .size:           8
        .value_kind:     global_buffer
      - .actual_access:  read_only
        .address_space:  global
        .offset:         64
        .size:           8
        .value_kind:     global_buffer
      - .actual_access:  read_only
        .address_space:  global
        .offset:         72
        .size:           8
        .value_kind:     global_buffer
      - .actual_access:  write_only
        .address_space:  global
        .offset:         80
        .size:           8
        .value_kind:     global_buffer
      - .actual_access:  write_only
        .address_space:  global
        .offset:         88
        .size:           8
        .value_kind:     global_buffer
      - .actual_access:  write_only
        .address_space:  global
        .offset:         96
        .size:           8
        .value_kind:     global_buffer
    .group_segment_fixed_size: 16384
    .kernarg_segment_align: 8
    .kernarg_segment_size: 104
    .language:       OpenCL C
    .language_version:
      - 2
      - 0
    .max_flat_workgroup_size: 512
    .name:           _Z11proj_kernelPKDF16_S0_S0_S0_PKiPKfS4_S4_S4_S4_PDF16_S5_S5_
    .private_segment_fixed_size: 0
    .sgpr_count:     62
    .sgpr_spill_count: 0
    .symbol:         _Z11proj_kernelPKDF16_S0_S0_S0_PKiPKfS4_S4_S4_S4_PDF16_S5_S5_.kd
    .uniform_work_group_size: 1
    .uses_dynamic_stack: false
    .vgpr_count:     200
    .vgpr_spill_count: 0
    .wavefront_size: 64
  - .agpr_count:     0
    .args:
      - .actual_access:  read_only
        .address_space:  global
        .offset:         0
        .size:           8
        .value_kind:     global_buffer
      - .address_space:  global
        .offset:         8
        .size:           8
        .value_kind:     global_buffer
      - .address_space:  global
        .offset:         16
        .size:           8
        .value_kind:     global_buffer
      - .actual_access:  read_only
        .address_space:  global
        .offset:         24
        .size:           8
        .value_kind:     global_buffer
      - .actual_access:  write_only
        .address_space:  global
        .offset:         32
        .size:           8
        .value_kind:     global_buffer
      - .actual_access:  read_only
        .address_space:  global
        .offset:         40
        .size:           8
        .value_kind:     global_buffer
      - .actual_access:  write_only
        .address_space:  global
        .offset:         48
        .size:           8
        .value_kind:     global_buffer
    .group_segment_fixed_size: 0
    .kernarg_segment_align: 8
    .kernarg_segment_size: 56
    .language:       OpenCL C
    .language_version:
      - 2
      - 0
    .max_flat_workgroup_size: 512
    .name:           _Z11attn_kernelPKDF16_S0_S0_PKiPDF16_PKfS3_
    .private_segment_fixed_size: 0
    .sgpr_count:     100
    .sgpr_spill_count: 0
    .symbol:         _Z11attn_kernelPKDF16_S0_S0_PKiPDF16_PKfS3_.kd
    .uniform_work_group_size: 1
    .uses_dynamic_stack: false
    .vgpr_count:     204
    .vgpr_spill_count: 0
    .wavefront_size: 64
  - .agpr_count:     0
    .args:
      - .address_space:  global
        .offset:         0
        .size:           8
        .value_kind:     global_buffer
      - .address_space:  global
        .offset:         8
        .size:           8
        .value_kind:     global_buffer
      - .actual_access:  read_only
        .address_space:  global
        .offset:         16
        .size:           8
        .value_kind:     global_buffer
      - .actual_access:  write_only
        .address_space:  global
        .offset:         24
        .size:           8
        .value_kind:     global_buffer
    .group_segment_fixed_size: 0
    .kernarg_segment_align: 8
    .kernarg_segment_size: 32
    .language:       OpenCL C
    .language_version:
      - 2
      - 0
    .max_flat_workgroup_size: 512
    .name:           _Z12oproj_kernelPKDF16_S0_PKfPf
    .private_segment_fixed_size: 0
    .sgpr_count:     33
    .sgpr_spill_count: 0
    .symbol:         _Z12oproj_kernelPKDF16_S0_PKfPf.kd
    .uniform_work_group_size: 1
    .uses_dynamic_stack: false
    .vgpr_count:     108
    .vgpr_spill_count: 0
    .wavefront_size: 64
